# GEMM K-loops: per-phase s_setprio flips replaced by s_nop (same size); on top of QK double-buffer, merge-loop fix, unscaled fp8 MFMA
# baseline (speedup 1.0000x reference)
.LBB0_578:
	s_add_u32 s2, s2, 0x40000
	s_addc_u32 s3, s3, 0
	s_mov_b32 m0, s41
	v_lshl_add_u64 v[48:49], s[2:3], 0, v[192:193]
	global_load_lds_dwordx4 v[48:49], off
	v_lshl_add_u64 v[48:49], s[2:3], 0, v[196:197]
	s_mov_b32 m0, s52
	s_nop 0
	global_load_lds_dwordx4 v[48:49], off
	s_waitcnt lgkmcnt(8)
	s_barrier
	s_waitcnt lgkmcnt(0)
	s_nop 0
	s_waitcnt lgkmcnt(0)
	v_mfma_f32_16x16x128_f8f6f4 v[188:191], v[8:15], v[40:47], v[188:191]
	v_mfma_f32_16x16x128_f8f6f4 v[180:183], v[0:7], v[40:47], v[180:183]
	v_mfma_f32_16x16x128_f8f6f4 v[172:175], v[8:15], v[32:39], v[172:175]
	v_mfma_f32_16x16x128_f8f6f4 v[164:167], v[0:7], v[32:39], v[164:167]
	v_mfma_f32_16x16x128_f8f6f4 v[156:159], v[8:15], v[24:31], v[156:159]
	v_mfma_f32_16x16x128_f8f6f4 v[148:151], v[0:7], v[24:31], v[148:151]
	v_mfma_f32_16x16x128_f8f6f4 v[140:143], v[8:15], v[16:23], v[140:143]
	v_mfma_f32_16x16x128_f8f6f4 v[132:135], v[0:7], v[16:23], v[132:135]
	s_nop 0
	s_barrier
	s_add_i32 s78, 0, 0x1c000
	s_mov_b32 m0, s62
	v_add_u32_e32 v60, s78, v232
	v_lshl_add_u64 v[222:223], v[222:223], 0, s[28:29]
	ds_read_b128 v[48:51], v60
	ds_read_b128 v[52:55], v60 offset:1024
	ds_read_b128 v[56:59], v60 offset:2048
	ds_read_b128 v[60:63], v60 offset:3072
	global_load_lds_dwordx4 v[222:223], off
	v_lshl_add_u64 v[222:223], v[224:225], 0, s[28:29]
	s_mov_b32 m0, s96
	s_nop 0
	global_load_lds_dwordx4 v[222:223], off
	s_barrier
	s_waitcnt lgkmcnt(0)
	s_nop 0
	s_waitcnt lgkmcnt(0)
	v_mfma_f32_16x16x128_f8f6f4 v[184:187], v[48:55], v[40:47], v[184:187]
	v_mfma_f32_16x16x128_f8f6f4 v[176:179], v[56:63], v[40:47], v[176:179]
	v_mfma_f32_16x16x128_f8f6f4 v[168:171], v[48:55], v[32:39], v[168:171]
	v_mfma_f32_16x16x128_f8f6f4 v[160:163], v[56:63], v[32:39], v[160:163]
	v_mfma_f32_16x16x128_f8f6f4 v[152:155], v[48:55], v[24:31], v[152:155]
	v_mfma_f32_16x16x128_f8f6f4 v[144:147], v[56:63], v[24:31], v[144:147]
	v_mfma_f32_16x16x128_f8f6f4 v[136:139], v[48:55], v[16:23], v[136:139]
	v_mfma_f32_16x16x128_f8f6f4 v[128:131], v[56:63], v[16:23], v[128:131]
	s_nop 0
	s_mov_b32 m0, s97
	v_lshl_add_u64 v[222:223], v[226:227], 0, s[28:29]
	s_barrier
	ds_read_b128 v[16:19], v235 offset:49152
	ds_read_b128 v[20:23], v235 offset:50176
	ds_read_b128 v[24:27], v235 offset:51200
	ds_read_b128 v[28:31], v235 offset:52224
	ds_read_b128 v[32:35], v235 offset:53248
	ds_read_b128 v[36:39], v235 offset:54272
	ds_read_b128 v[40:43], v235 offset:55296
	ds_read_b128 v[44:47], v235 offset:56320
	global_load_lds_dwordx4 v[222:223], off
	v_lshl_add_u64 v[222:223], v[228:229], 0, s[28:29]
	s_mov_b32 m0, s39
	s_nop 0
	global_load_lds_dwordx4 v[222:223], off
	s_barrier
	s_waitcnt lgkmcnt(0)
	s_nop 0
	s_waitcnt lgkmcnt(0)
	v_mfma_f32_16x16x128_f8f6f4 v[116:119], v[8:15], v[16:23], v[116:119]
	v_mfma_f32_16x16x128_f8f6f4 v[112:115], v[0:7], v[16:23], v[112:115]
	v_mfma_f32_16x16x128_f8f6f4 v[100:103], v[8:15], v[24:31], v[100:103]
	v_mfma_f32_16x16x128_f8f6f4 v[96:99], v[0:7], v[24:31], v[96:99]
	v_mfma_f32_16x16x128_f8f6f4 v[84:87], v[8:15], v[32:39], v[84:87]
	v_mfma_f32_16x16x128_f8f6f4 v[80:83], v[0:7], v[32:39], v[80:83]
	v_mfma_f32_16x16x128_f8f6f4 v[68:71], v[8:15], v[40:47], v[68:71]
	v_mfma_f32_16x16x128_f8f6f4 v[64:67], v[0:7], v[40:47], v[64:67]
	s_nop 0
	s_barrier
	s_add_u32 s2, s76, 0x40080
	s_addc_u32 s3, s77, 0
	s_add_i32 s76, s78, s53
	v_lshl_add_u64 v[0:1], s[2:3], 0, v[194:195]
	s_mov_b32 m0, s76
	s_nop 0
	global_load_lds_dwordx4 v[0:1], off
	v_lshl_add_u64 v[0:1], s[2:3], 0, v[198:199]
	s_add_i32 m0, s76, 0x2000
	s_nop 0
	global_load_lds_dwordx4 v[0:1], off
	s_waitcnt vmcnt(6)
	s_barrier
	s_nop 0
	v_mfma_f32_16x16x128_f8f6f4 v[124:127], v[48:55], v[16:23], v[124:127]
	v_mfma_f32_16x16x128_f8f6f4 v[120:123], v[56:63], v[16:23], v[120:123]
	v_mfma_f32_16x16x128_f8f6f4 v[108:111], v[48:55], v[24:31], v[108:111]
	v_mfma_f32_16x16x128_f8f6f4 v[104:107], v[56:63], v[24:31], v[104:107]
	v_mfma_f32_16x16x128_f8f6f4 v[92:95], v[48:55], v[32:39], v[92:95]
	v_mfma_f32_16x16x128_f8f6f4 v[88:91], v[56:63], v[32:39], v[88:91]
	v_mfma_f32_16x16x128_f8f6f4 v[76:79], v[48:55], v[40:47], v[76:79]
	v_mfma_f32_16x16x128_f8f6f4 v[72:75], v[56:63], v[40:47], v[72:75]
	s_nop 0
	s_add_i32 s82, s82, 2
	s_add_u32 s36, s36, 0x100
	s_addc_u32 s37, s37, 0
	s_add_u32 s54, s54, 0x100
	s_addc_u32 s57, s57, 0
	s_cmp_gt_u32 s82, 13
	s_barrier
	s_cbranch_scc1 .LBB0_591
.LBB0_579:
	ds_read_b128 v[0:3], v234
	ds_read_b128 v[4:7], v234 offset:1024
	ds_read_b128 v[8:11], v234 offset:2048
	ds_read_b128 v[12:15], v234 offset:3072
	s_xor_b64 s[78:79], s[66:67], -1
	v_lshl_add_u64 v[16:17], s[36:37], 0, v[208:209]
	s_add_i32 m0, s9, 0xc000
	ds_read_b128 v[56:59], v235
	ds_read_b128 v[60:63], v235 offset:1024
	ds_read_b128 v[48:51], v235 offset:2048
	ds_read_b128 v[52:55], v235 offset:3072
	ds_read_b128 v[40:43], v235 offset:4096
	ds_read_b128 v[44:47], v235 offset:5120
	ds_read_b128 v[32:35], v235 offset:6144
	ds_read_b128 v[36:39], v235 offset:7168
	global_load_lds_dwordx4 v[16:17], off
	v_lshl_add_u64 v[16:17], s[36:37], 0, v[210:211]
	s_add_i32 m0, s9, 0xe000
	s_nop 0
	global_load_lds_dwordx4 v[16:17], off
	s_waitcnt lgkmcnt(8)
	s_barrier
	s_waitcnt lgkmcnt(0)
	s_nop 0
	s_waitcnt lgkmcnt(0)
	v_mfma_f32_16x16x128_f8f6f4 v[188:191], v[0:7], v[56:63], v[188:191]
	v_mfma_f32_16x16x128_f8f6f4 v[180:183], v[8:15], v[56:63], v[180:183]
	v_mfma_f32_16x16x128_f8f6f4 v[172:175], v[0:7], v[48:55], v[172:175]
	v_mfma_f32_16x16x128_f8f6f4 v[164:167], v[8:15], v[48:55], v[164:167]
	v_mfma_f32_16x16x128_f8f6f4 v[156:159], v[0:7], v[40:47], v[156:159]
	v_mfma_f32_16x16x128_f8f6f4 v[148:151], v[8:15], v[40:47], v[148:151]
	v_mfma_f32_16x16x128_f8f6f4 v[140:143], v[0:7], v[32:39], v[140:143]
	v_mfma_f32_16x16x128_f8f6f4 v[132:135], v[8:15], v[32:39], v[132:135]
	s_nop 0
	s_barrier
	ds_read_b128 v[24:27], v237
	ds_read_b128 v[28:31], v237 offset:1024
	ds_read_b128 v[16:19], v237 offset:2048
	ds_read_b128 v[20:23], v237 offset:3072
	s_and_b64 vcc, exec, s[78:79]
	s_cbranch_vccnz .LBB0_581
	v_add_u32_e32 v218, v231, v230
	ds_read2_b32 v[212:213], v218 offset1:32
	ds_read2_b32 v[214:215], v218 offset0:64 offset1:96
	ds_read2_b32 v[216:217], v218 offset0:128 offset1:160
	ds_read2_b32 v[218:219], v218 offset0:192 offset1:224

.LBB0_583:
	s_nop 0
	s_waitcnt lgkmcnt(0)
	v_mfma_f32_16x16x128_f8f6f4 v[184:187], v[24:31], v[56:63], v[184:187]
	v_mfma_f32_16x16x128_f8f6f4 v[176:179], v[16:23], v[56:63], v[176:179]
	v_mfma_f32_16x16x128_f8f6f4 v[168:171], v[24:31], v[48:55], v[168:171]
	v_mfma_f32_16x16x128_f8f6f4 v[160:163], v[16:23], v[48:55], v[160:163]
	v_mfma_f32_16x16x128_f8f6f4 v[152:155], v[24:31], v[40:47], v[152:155]
	v_mfma_f32_16x16x128_f8f6f4 v[144:147], v[16:23], v[40:47], v[144:147]
	v_mfma_f32_16x16x128_f8f6f4 v[136:139], v[24:31], v[32:39], v[136:139]
	v_mfma_f32_16x16x128_f8f6f4 v[128:131], v[16:23], v[32:39], v[128:131]
	s_nop 0
	s_barrier
	ds_read_b128 v[56:59], v235 offset:16384
	ds_read_b128 v[60:63], v235 offset:17408
	ds_read_b128 v[48:51], v235 offset:18432
	ds_read_b128 v[52:55], v235 offset:19456
	ds_read_b128 v[40:43], v235 offset:20480
	ds_read_b128 v[44:47], v235 offset:21504
	ds_read_b128 v[32:35], v235 offset:22528
	ds_read_b128 v[36:39], v235 offset:23552
	s_and_b64 vcc, exec, s[2:3]
	s_cbranch_vccnz .LBB0_585
	v_lshl_add_u64 v[226:227], v[204:205], 0, s[42:43]
	global_store_dwordx2 v[226:227], v[220:221], off
.LBB0_585:
	s_add_u32 s66, s36, 0xfffc0080
	s_addc_u32 s67, s37, -1
	s_and_b64 s[2:3], s[80:81], exec
	s_cselect_b32 s3, s5, s67
	s_cselect_b32 s2, s8, s66
	s_mov_b32 m0, s9
	v_lshl_add_u64 v[226:227], s[2:3], 0, v[192:193]
	global_load_lds_dwordx4 v[226:227], off
	v_lshl_add_u64 v[228:229], s[2:3], 0, v[196:197]
	s_mov_b32 m0, s15
	s_nop 0
	global_load_lds_dwordx4 v[228:229], off
	s_barrier
	s_waitcnt lgkmcnt(0)
	s_nop 0
	s_waitcnt lgkmcnt(0)
	v_mfma_f32_16x16x128_f8f6f4 v[116:119], v[0:7], v[56:63], v[116:119]
	v_mfma_f32_16x16x128_f8f6f4 v[112:115], v[8:15], v[56:63], v[112:115]
	v_mfma_f32_16x16x128_f8f6f4 v[100:103], v[0:7], v[48:55], v[100:103]
	v_mfma_f32_16x16x128_f8f6f4 v[96:99], v[8:15], v[48:55], v[96:99]
	v_mfma_f32_16x16x128_f8f6f4 v[84:87], v[0:7], v[40:47], v[84:87]
	v_mfma_f32_16x16x128_f8f6f4 v[80:83], v[8:15], v[40:47], v[80:83]
	v_mfma_f32_16x16x128_f8f6f4 v[68:71], v[0:7], v[32:39], v[68:71]
	v_mfma_f32_16x16x128_f8f6f4 v[64:67], v[8:15], v[32:39], v[64:67]
	s_nop 0
	s_barrier
	s_add_u32 s66, s76, 0x40000
	s_addc_u32 s67, s77, 0
	s_mov_b32 m0, s33
	v_lshl_add_u64 v[0:1], s[66:67], 0, v[194:195]
	global_load_lds_dwordx4 v[0:1], off
	v_lshl_add_u64 v[0:1], s[66:67], 0, v[198:199]
	s_mov_b32 m0, s40
	s_mov_b64 s[66:67], -1
	global_load_lds_dwordx4 v[0:1], off
	s_and_b64 vcc, exec, s[78:79]
	s_cbranch_vccz .LBB0_587
	s_waitcnt vmcnt(6)
	s_mov_b64 s[66:67], 0

.LBB0_589:
	s_barrier
	s_nop 0
	v_mfma_f32_16x16x128_f8f6f4 v[124:127], v[24:31], v[56:63], v[124:127]
	v_mfma_f32_16x16x128_f8f6f4 v[120:123], v[16:23], v[56:63], v[120:123]
	v_mfma_f32_16x16x128_f8f6f4 v[108:111], v[24:31], v[48:55], v[108:111]
	v_mfma_f32_16x16x128_f8f6f4 v[104:107], v[16:23], v[48:55], v[104:107]
	v_mfma_f32_16x16x128_f8f6f4 v[92:95], v[24:31], v[40:47], v[92:95]
	v_mfma_f32_16x16x128_f8f6f4 v[88:91], v[16:23], v[40:47], v[88:91]
	v_mfma_f32_16x16x128_f8f6f4 v[76:79], v[24:31], v[32:39], v[76:79]
	v_mfma_f32_16x16x128_f8f6f4 v[72:75], v[16:23], v[32:39], v[72:75]
	s_nop 0
	v_add_u32_e32 v4, 0x18000, v233
	s_barrier
	ds_read_b128 v[8:11], v4
	ds_read_b128 v[12:15], v4 offset:1024
	ds_read_b128 v[0:3], v4 offset:2048
	ds_read_b128 v[4:7], v4 offset:3072
	ds_read_b128 v[40:43], v235 offset:32768
	ds_read_b128 v[44:47], v235 offset:33792
	ds_read_b128 v[32:35], v235 offset:34816
	ds_read_b128 v[36:39], v235 offset:35840
	ds_read_b128 v[24:27], v235 offset:36864
	ds_read_b128 v[28:31], v235 offset:37888
	ds_read_b128 v[16:19], v235 offset:38912
	ds_read_b128 v[20:23], v235 offset:39936
	s_mul_i32 s78, s63, s19
	s_add_i32 s78, s78, s18
	s_cmp_lt_i32 s78, 0xa000
	s_cselect_b64 s[66:67], -1, 0
	s_cmp_gt_i32 s78, 0x9fff
	s_cbranch_scc1 .LBB0_578
	s_lshl_b32 s43, s78, 1
	s_and_b32 s43, s43, 0xe0
	s_and_b32 s79, s78, 0x780
	s_or_b32 s80, s43, s79
	s_add_i32 s79, s79, s43
	s_ashr_i32 s42, s78, 11
	s_addk_i32 s79, 0x780
	s_cmpk_lt_u32 s43, 0x80
	s_cselect_b32 s79, s80, s79
	s_lshl_b32 s80, s78, 7
	s_and_b32 s83, s80, 0x780
	s_ashr_i32 s43, s42, 31
	s_lshl_b32 s80, s83, 12
	s_lshl_b64 s[42:43], s[42:43], 23
	s_or_b32 s79, s79, s80
	s_or_b32 s80, s42, s79
	s_mov_b32 s81, s43
	v_lshl_add_u64 v[48:49], s[80:81], 2, v[206:207]
	s_add_i32 m0, s10, 0x20000
	s_mov_b64 s[80:81], 0x20000
	global_load_lds_dwordx4 v[48:49], off nt
	v_lshl_add_u64 v[48:49], v[48:49], 0, s[80:81]
	s_mov_b32 m0, s48
	s_lshl_b32 s78, s78, 12
	global_load_lds_dwordx4 v[48:49], off nt
	s_and_b32 s78, s78, 0x7f0000
	s_or_b32 s78, s83, s78
	s_or_b32 s42, s42, s78
	s_add_i32 s63, s63, 1
	s_branch .LBB0_578

.LBB0_917:
	s_add_u32 s0, s0, 0x80000
	s_addc_u32 s1, s1, 0
	s_mov_b32 m0, s8
	v_lshl_add_u64 v[120:121], s[0:1], 0, v[200:201]
	global_load_lds_dwordx4 v[120:121], off
	v_lshl_add_u64 v[120:121], s[0:1], 0, v[204:205]
	s_mov_b32 m0, s9
	s_nop 0
	global_load_lds_dwordx4 v[120:121], off
	s_waitcnt lgkmcnt(8)
	s_barrier
	s_waitcnt lgkmcnt(0)
	s_nop 0
	s_waitcnt lgkmcnt(0)
	v_mfma_f32_16x16x32_bf16 v[80:83], v[128:131], v[184:187], v[80:83]
	v_mfma_f32_16x16x32_bf16 v[148:151], v[132:135], v[188:191], v[80:83]
	v_mfma_f32_16x16x32_bf16 v[80:83], v[152:155], v[184:187], v[84:87]
	v_mfma_f32_16x16x32_bf16 v[144:147], v[156:159], v[188:191], v[80:83]
	v_mfma_f32_16x16x32_bf16 v[80:83], v[128:131], v[176:179], v[104:107]
	v_mfma_f32_16x16x32_bf16 v[124:127], v[132:135], v[180:183], v[80:83]
	v_mfma_f32_16x16x32_bf16 v[80:83], v[152:155], v[176:179], v[108:111]
	v_mfma_f32_16x16x32_bf16 v[120:123], v[156:159], v[180:183], v[80:83]
	v_mfma_f32_16x16x32_bf16 v[80:83], v[128:131], v[168:171], v[100:103]
	v_mfma_f32_16x16x32_bf16 v[100:103], v[132:135], v[172:175], v[80:83]
	v_mfma_f32_16x16x32_bf16 v[80:83], v[152:155], v[168:171], v[96:99]
	v_mfma_f32_16x16x32_bf16 v[76:79], v[128:131], v[160:163], v[76:79]
	v_mfma_f32_16x16x32_bf16 v[72:75], v[152:155], v[160:163], v[72:75]
	v_mfma_f32_16x16x32_bf16 v[96:99], v[156:159], v[172:175], v[80:83]
	v_mfma_f32_16x16x32_bf16 v[76:79], v[132:135], v[164:167], v[76:79]
	v_mfma_f32_16x16x32_bf16 v[72:75], v[156:159], v[164:167], v[72:75]
	s_nop 0
	s_barrier
	s_add_i32 s34, 0, 0x1c000
	s_mov_b32 m0, s96
	v_add_u32_e32 v108, s34, v238
	v_lshl_add_u64 v[196:197], v[230:231], 0, s[44:45]
	ds_read_b128 v[80:83], v108
	ds_read_b128 v[84:87], v108 offset:1024
	ds_read_b128 v[104:107], v108 offset:2048
	ds_read_b128 v[108:111], v108 offset:3072
	global_load_lds_dwordx4 v[196:197], off
	v_lshl_add_u64 v[196:197], v[232:233], 0, s[44:45]
	s_mov_b32 m0, s97
	s_nop 0
	global_load_lds_dwordx4 v[196:197], off
	s_barrier
	s_waitcnt lgkmcnt(0)
	s_nop 0
	s_waitcnt lgkmcnt(0)
	v_mfma_f32_16x16x32_bf16 v[140:143], v[80:83], v[184:187], v[140:143]
	v_mfma_f32_16x16x32_bf16 v[136:139], v[104:107], v[184:187], v[136:139]
	v_mfma_f32_16x16x32_bf16 v[116:119], v[80:83], v[176:179], v[116:119]
	v_mfma_f32_16x16x32_bf16 v[112:115], v[104:107], v[176:179], v[112:115]
	v_mfma_f32_16x16x32_bf16 v[92:95], v[80:83], v[168:171], v[92:95]
	v_mfma_f32_16x16x32_bf16 v[88:91], v[104:107], v[168:171], v[88:91]
	v_mfma_f32_16x16x32_bf16 v[68:71], v[80:83], v[160:163], v[68:71]
	v_mfma_f32_16x16x32_bf16 v[64:67], v[104:107], v[160:163], v[64:67]
	v_mfma_f32_16x16x32_bf16 v[140:143], v[84:87], v[188:191], v[140:143]
	v_mfma_f32_16x16x32_bf16 v[136:139], v[108:111], v[188:191], v[136:139]
	v_mfma_f32_16x16x32_bf16 v[116:119], v[84:87], v[180:183], v[116:119]
	v_mfma_f32_16x16x32_bf16 v[112:115], v[108:111], v[180:183], v[112:115]
	v_mfma_f32_16x16x32_bf16 v[92:95], v[84:87], v[172:175], v[92:95]
	v_mfma_f32_16x16x32_bf16 v[88:91], v[108:111], v[172:175], v[88:91]
	v_mfma_f32_16x16x32_bf16 v[68:71], v[84:87], v[164:167], v[68:71]
	v_mfma_f32_16x16x32_bf16 v[64:67], v[108:111], v[164:167], v[64:67]
	s_nop 0
	s_mov_b32 m0, s48
	v_lshl_add_u64 v[192:193], v[192:193], 0, s[44:45]
	s_barrier
	ds_read_b128 v[160:163], v241 offset:49152
	ds_read_b128 v[164:167], v241 offset:50176
	ds_read_b128 v[168:171], v241 offset:51200
	ds_read_b128 v[172:175], v241 offset:52224
	ds_read_b128 v[176:179], v241 offset:53248
	ds_read_b128 v[180:183], v241 offset:54272
	ds_read_b128 v[184:187], v241 offset:55296
	ds_read_b128 v[188:191], v241 offset:56320
	global_load_lds_dwordx4 v[192:193], off
	v_lshl_add_u64 v[192:193], v[194:195], 0, s[44:45]
	s_mov_b32 m0, s49
	s_nop 0
	global_load_lds_dwordx4 v[192:193], off
	s_barrier
	s_waitcnt lgkmcnt(0)
	s_nop 0
	s_waitcnt lgkmcnt(0)
	v_mfma_f32_16x16x32_bf16 v[60:63], v[128:131], v[160:163], v[60:63]
	v_mfma_f32_16x16x32_bf16 v[56:59], v[152:155], v[160:163], v[56:59]
	v_mfma_f32_16x16x32_bf16 v[36:39], v[128:131], v[168:171], v[36:39]
	v_mfma_f32_16x16x32_bf16 v[32:35], v[152:155], v[168:171], v[32:35]
	v_mfma_f32_16x16x32_bf16 v[20:23], v[128:131], v[176:179], v[20:23]
	v_mfma_f32_16x16x32_bf16 v[16:19], v[152:155], v[176:179], v[16:19]
	v_mfma_f32_16x16x32_bf16 v[4:7], v[128:131], v[184:187], v[4:7]
	v_mfma_f32_16x16x32_bf16 v[0:3], v[152:155], v[184:187], v[0:3]
	v_mfma_f32_16x16x32_bf16 v[60:63], v[132:135], v[164:167], v[60:63]
	v_mfma_f32_16x16x32_bf16 v[56:59], v[156:159], v[164:167], v[56:59]
	v_mfma_f32_16x16x32_bf16 v[36:39], v[132:135], v[172:175], v[36:39]
	v_mfma_f32_16x16x32_bf16 v[32:35], v[156:159], v[172:175], v[32:35]
	v_mfma_f32_16x16x32_bf16 v[20:23], v[132:135], v[180:183], v[20:23]
	v_mfma_f32_16x16x32_bf16 v[16:19], v[156:159], v[180:183], v[16:19]
	v_mfma_f32_16x16x32_bf16 v[4:7], v[132:135], v[188:191], v[4:7]
	v_mfma_f32_16x16x32_bf16 v[0:3], v[156:159], v[188:191], v[0:3]
	s_nop 0
	s_barrier
	s_add_u32 s0, s30, 0x80080
	s_addc_u32 s1, s31, 0
	s_add_i32 s30, s34, s53
	v_lshl_add_u64 v[128:129], s[0:1], 0, v[202:203]
	s_mov_b32 m0, s30
	s_nop 0
	global_load_lds_dwordx4 v[128:129], off
	v_lshl_add_u64 v[128:129], s[0:1], 0, v[206:207]
	s_add_i32 m0, s30, 0x2000
	s_nop 0
	global_load_lds_dwordx4 v[128:129], off
	s_waitcnt vmcnt(6)
	s_barrier
	s_nop 0
	v_mfma_f32_16x16x32_bf16 v[48:51], v[80:83], v[160:163], v[48:51]
	v_mfma_f32_16x16x32_bf16 v[52:55], v[104:107], v[160:163], v[52:55]
	v_mfma_f32_16x16x32_bf16 v[40:43], v[80:83], v[168:171], v[40:43]
	v_mfma_f32_16x16x32_bf16 v[44:47], v[104:107], v[168:171], v[44:47]
	v_mfma_f32_16x16x32_bf16 v[24:27], v[80:83], v[176:179], v[24:27]
	v_mfma_f32_16x16x32_bf16 v[28:31], v[104:107], v[176:179], v[28:31]
	v_mfma_f32_16x16x32_bf16 v[8:11], v[80:83], v[184:187], v[8:11]
	v_mfma_f32_16x16x32_bf16 v[12:15], v[104:107], v[184:187], v[12:15]
	v_mfma_f32_16x16x32_bf16 v[48:51], v[84:87], v[164:167], v[48:51]
	v_mfma_f32_16x16x32_bf16 v[52:55], v[108:111], v[164:167], v[52:55]
	v_mfma_f32_16x16x32_bf16 v[40:43], v[84:87], v[172:175], v[40:43]
	v_mfma_f32_16x16x32_bf16 v[44:47], v[108:111], v[172:175], v[44:47]
	v_mfma_f32_16x16x32_bf16 v[24:27], v[84:87], v[180:183], v[24:27]
	v_mfma_f32_16x16x32_bf16 v[28:31], v[108:111], v[180:183], v[28:31]
	v_mfma_f32_16x16x32_bf16 v[8:11], v[84:87], v[188:191], v[8:11]
	v_mfma_f32_16x16x32_bf16 v[12:15], v[108:111], v[188:191], v[12:15]
	s_nop 0
	s_add_i32 s43, s43, 2
	s_add_u32 s28, s28, 0x100
	s_addc_u32 s29, s29, 0
	s_add_u32 s39, s39, 0x100
	s_addc_u32 s42, s42, 0
	s_cmp_gt_u32 s43, 29
	s_barrier
	s_cbranch_scc1 .LBB0_930
.LBB0_918:
	ds_read_b128 v[152:155], v240
	ds_read_b128 v[156:159], v240 offset:1024
	ds_read_b128 v[160:163], v240 offset:2048
	ds_read_b128 v[164:167], v240 offset:3072
	s_xor_b64 s[34:35], s[82:83], -1
	v_lshl_add_u64 v[80:81], s[28:29], 0, v[216:217]
	s_add_i32 m0, s60, 0xc000
	ds_read_b128 v[192:195], v241
	ds_read_b128 v[196:199], v241 offset:1024
	ds_read_b128 v[184:187], v241 offset:2048
	ds_read_b128 v[188:191], v241 offset:3072
	ds_read_b128 v[176:179], v241 offset:4096
	ds_read_b128 v[180:183], v241 offset:5120
	ds_read_b128 v[168:171], v241 offset:6144
	ds_read_b128 v[172:175], v241 offset:7168
	global_load_lds_dwordx4 v[80:81], off
	v_lshl_add_u64 v[80:81], s[28:29], 0, v[218:219]
	s_add_i32 m0, s60, 0xe000
	s_nop 0
	global_load_lds_dwordx4 v[80:81], off
	s_waitcnt lgkmcnt(8)
	s_barrier
	s_waitcnt lgkmcnt(0)
	s_nop 0
	s_waitcnt lgkmcnt(0)
	v_mfma_f32_16x16x32_bf16 v[80:83], v[152:155], v[192:195], v[148:151]
	v_mfma_f32_16x16x32_bf16 v[84:87], v[160:163], v[192:195], v[144:147]
	v_mfma_f32_16x16x32_bf16 v[104:107], v[152:155], v[184:187], v[124:127]
	v_mfma_f32_16x16x32_bf16 v[108:111], v[160:163], v[184:187], v[120:123]
	v_mfma_f32_16x16x32_bf16 v[100:103], v[152:155], v[176:179], v[100:103]
	v_mfma_f32_16x16x32_bf16 v[96:99], v[160:163], v[176:179], v[96:99]
	v_mfma_f32_16x16x32_bf16 v[76:79], v[152:155], v[168:171], v[76:79]
	v_mfma_f32_16x16x32_bf16 v[72:75], v[160:163], v[168:171], v[72:75]
	v_mfma_f32_16x16x32_bf16 v[80:83], v[156:159], v[196:199], v[80:83]
	v_mfma_f32_16x16x32_bf16 v[84:87], v[164:167], v[196:199], v[84:87]
	v_mfma_f32_16x16x32_bf16 v[104:107], v[156:159], v[188:191], v[104:107]
	v_mfma_f32_16x16x32_bf16 v[108:111], v[164:167], v[188:191], v[108:111]
	v_mfma_f32_16x16x32_bf16 v[100:103], v[156:159], v[180:183], v[100:103]
	v_mfma_f32_16x16x32_bf16 v[96:99], v[164:167], v[180:183], v[96:99]
	v_mfma_f32_16x16x32_bf16 v[76:79], v[156:159], v[172:175], v[76:79]
	v_mfma_f32_16x16x32_bf16 v[72:75], v[164:167], v[172:175], v[72:75]
	s_nop 0
	s_barrier
	ds_read_b128 v[120:123], v242
	ds_read_b128 v[124:127], v242 offset:1024
	ds_read_b128 v[128:131], v242 offset:2048
	ds_read_b128 v[132:135], v242 offset:3072
	s_and_b64 vcc, exec, s[34:35]
	s_cbranch_vccnz .LBB0_920
	v_add_u32_e32 v144, v237, v236
	ds_read2_b32 v[220:221], v144 offset1:32
	ds_read2_b32 v[222:223], v144 offset0:64 offset1:96
	ds_read2_b32 v[224:225], v144 offset0:128 offset1:160
	ds_read2_b32 v[226:227], v144 offset0:192 offset1:224

.LBB0_922:
	s_nop 0
	s_waitcnt lgkmcnt(0)
	v_mfma_f32_16x16x32_bf16 v[140:143], v[120:123], v[192:195], v[140:143]
	v_mfma_f32_16x16x32_bf16 v[136:139], v[128:131], v[192:195], v[136:139]
	v_mfma_f32_16x16x32_bf16 v[116:119], v[120:123], v[184:187], v[116:119]
	v_mfma_f32_16x16x32_bf16 v[112:115], v[128:131], v[184:187], v[112:115]
	v_mfma_f32_16x16x32_bf16 v[92:95], v[120:123], v[176:179], v[92:95]
	v_mfma_f32_16x16x32_bf16 v[88:91], v[128:131], v[176:179], v[88:91]
	v_mfma_f32_16x16x32_bf16 v[68:71], v[120:123], v[168:171], v[68:71]
	v_mfma_f32_16x16x32_bf16 v[64:67], v[128:131], v[168:171], v[64:67]
	v_mfma_f32_16x16x32_bf16 v[140:143], v[124:127], v[196:199], v[140:143]
	v_mfma_f32_16x16x32_bf16 v[136:139], v[132:135], v[196:199], v[136:139]
	v_mfma_f32_16x16x32_bf16 v[116:119], v[124:127], v[188:191], v[116:119]
	v_mfma_f32_16x16x32_bf16 v[112:115], v[132:135], v[188:191], v[112:115]
	v_mfma_f32_16x16x32_bf16 v[92:95], v[124:127], v[180:183], v[92:95]
	v_mfma_f32_16x16x32_bf16 v[88:91], v[132:135], v[180:183], v[88:91]
	v_mfma_f32_16x16x32_bf16 v[68:71], v[124:127], v[172:175], v[68:71]
	v_mfma_f32_16x16x32_bf16 v[64:67], v[132:135], v[172:175], v[64:67]
	s_nop 0
	s_barrier
	ds_read_b128 v[184:187], v241 offset:16384
	ds_read_b128 v[188:191], v241 offset:17408
	ds_read_b128 v[176:179], v241 offset:18432
	ds_read_b128 v[180:183], v241 offset:19456
	ds_read_b128 v[168:171], v241 offset:20480
	ds_read_b128 v[172:175], v241 offset:21504
	ds_read_b128 v[144:147], v241 offset:22528
	ds_read_b128 v[148:151], v241 offset:23552
	s_and_b64 vcc, exec, s[0:1]
	s_cbranch_vccnz .LBB0_924
	v_lshl_add_u64 v[192:193], v[212:213], 0, s[54:55]
	global_store_dwordx2 v[192:193], v[228:229], off
.LBB0_924:
	s_add_u32 s56, s28, 0xfff80080
	s_addc_u32 s57, s29, -1
	s_and_b64 s[0:1], s[36:37], exec
	s_cselect_b32 s1, s3, s57
	s_cselect_b32 s0, s4, s56
	s_mov_b32 m0, s60
	v_lshl_add_u64 v[192:193], s[0:1], 0, v[200:201]
	global_load_lds_dwordx4 v[192:193], off
	v_lshl_add_u64 v[194:195], s[0:1], 0, v[204:205]
	s_mov_b32 m0, s40
	s_nop 0
	global_load_lds_dwordx4 v[194:195], off
	s_barrier
	s_waitcnt lgkmcnt(0)
	s_nop 0
	s_waitcnt lgkmcnt(0)
	v_mfma_f32_16x16x32_bf16 v[60:63], v[152:155], v[184:187], v[60:63]
	v_mfma_f32_16x16x32_bf16 v[56:59], v[160:163], v[184:187], v[56:59]
	v_mfma_f32_16x16x32_bf16 v[36:39], v[152:155], v[176:179], v[36:39]
	v_mfma_f32_16x16x32_bf16 v[32:35], v[160:163], v[176:179], v[32:35]
	v_mfma_f32_16x16x32_bf16 v[20:23], v[152:155], v[168:171], v[20:23]
	v_mfma_f32_16x16x32_bf16 v[16:19], v[160:163], v[168:171], v[16:19]
	v_mfma_f32_16x16x32_bf16 v[4:7], v[152:155], v[144:147], v[4:7]
	v_mfma_f32_16x16x32_bf16 v[0:3], v[160:163], v[144:147], v[0:3]
	v_mfma_f32_16x16x32_bf16 v[60:63], v[156:159], v[188:191], v[60:63]
	v_mfma_f32_16x16x32_bf16 v[56:59], v[164:167], v[188:191], v[56:59]
	v_mfma_f32_16x16x32_bf16 v[36:39], v[156:159], v[180:183], v[36:39]
	v_mfma_f32_16x16x32_bf16 v[32:35], v[164:167], v[180:183], v[32:35]
	v_mfma_f32_16x16x32_bf16 v[20:23], v[156:159], v[172:175], v[20:23]
	v_mfma_f32_16x16x32_bf16 v[16:19], v[164:167], v[172:175], v[16:19]
	v_mfma_f32_16x16x32_bf16 v[4:7], v[156:159], v[148:151], v[4:7]
	v_mfma_f32_16x16x32_bf16 v[0:3], v[164:167], v[148:151], v[0:3]
	s_nop 0
	s_barrier
	s_add_u32 s36, s30, 0x80000
	s_addc_u32 s37, s31, 0
	s_mov_b32 m0, s41
	v_lshl_add_u64 v[152:153], s[36:37], 0, v[202:203]
	global_load_lds_dwordx4 v[152:153], off
	v_lshl_add_u64 v[152:153], s[36:37], 0, v[206:207]
	s_mov_b32 m0, s52
	s_mov_b64 s[36:37], -1
	global_load_lds_dwordx4 v[152:153], off
	s_and_b64 vcc, exec, s[34:35]
	s_cbranch_vccz .LBB0_926
	s_waitcnt vmcnt(6)
	s_mov_b64 s[36:37], 0

.LBB0_928:
	s_barrier
	s_nop 0
	v_mfma_f32_16x16x32_bf16 v[48:51], v[120:123], v[184:187], v[48:51]
	v_mfma_f32_16x16x32_bf16 v[52:55], v[128:131], v[184:187], v[52:55]
	v_mfma_f32_16x16x32_bf16 v[40:43], v[120:123], v[176:179], v[40:43]
	v_mfma_f32_16x16x32_bf16 v[44:47], v[128:131], v[176:179], v[44:47]
	v_mfma_f32_16x16x32_bf16 v[24:27], v[120:123], v[168:171], v[24:27]
	v_mfma_f32_16x16x32_bf16 v[28:31], v[128:131], v[168:171], v[28:31]
	v_mfma_f32_16x16x32_bf16 v[8:11], v[120:123], v[144:147], v[8:11]
	v_mfma_f32_16x16x32_bf16 v[12:15], v[128:131], v[144:147], v[12:15]
	v_mfma_f32_16x16x32_bf16 v[48:51], v[124:127], v[188:191], v[48:51]
	v_mfma_f32_16x16x32_bf16 v[52:55], v[132:135], v[188:191], v[52:55]
	v_mfma_f32_16x16x32_bf16 v[40:43], v[124:127], v[180:183], v[40:43]
	v_mfma_f32_16x16x32_bf16 v[44:47], v[132:135], v[180:183], v[44:47]
	v_mfma_f32_16x16x32_bf16 v[24:27], v[124:127], v[172:175], v[24:27]
	v_mfma_f32_16x16x32_bf16 v[28:31], v[132:135], v[172:175], v[28:31]
	v_mfma_f32_16x16x32_bf16 v[8:11], v[124:127], v[148:151], v[8:11]
	v_mfma_f32_16x16x32_bf16 v[12:15], v[132:135], v[148:151], v[12:15]
	s_nop 0
	v_add_u32_e32 v120, 0x18000, v239
	s_barrier
	ds_read_b128 v[128:131], v120
	ds_read_b128 v[132:135], v120 offset:1024
	ds_read_b128 v[152:155], v120 offset:2048
	ds_read_b128 v[156:159], v120 offset:3072
	ds_read_b128 v[184:187], v241 offset:32768
	ds_read_b128 v[188:191], v241 offset:33792
	ds_read_b128 v[176:179], v241 offset:34816
	ds_read_b128 v[180:183], v241 offset:35840
	ds_read_b128 v[168:171], v241 offset:36864
	ds_read_b128 v[172:175], v241 offset:37888
	ds_read_b128 v[160:163], v241 offset:38912
	ds_read_b128 v[164:167], v241 offset:39936
	s_add_i32 s34, s62, s63
	s_mul_i32 s34, s34, s19
	s_add_i32 s34, s34, s18
	s_cmp_lt_i32 s34, 0xa000
	s_cselect_b64 s[82:83], -1, 0
	s_cmp_gt_i32 s34, 0x9fff
	s_cbranch_scc1 .LBB0_917
	s_lshl_b32 s35, s34, 1
	s_and_b32 s35, s35, 0xe0
	s_and_b32 s37, s34, 0x780
	s_or_b32 s54, s35, s37
	s_add_i32 s37, s37, s35
	s_ashr_i32 s36, s34, 11
	s_addk_i32 s37, 0x780
	s_cmpk_lt_u32 s35, 0x80
	s_cselect_b32 s35, s54, s37
	s_ashr_i32 s37, s36, 31
	s_lshl_b64 s[54:55], s[36:37], 23
	s_lshl_b32 s36, s34, 7
	s_and_b32 s56, s36, 0x780
	s_lshl_b32 s36, s56, 12
	s_or_b32 s35, s35, s36
	s_or_b32 s36, s54, s35
	s_mov_b32 s37, s55
	v_lshl_add_u64 v[120:121], s[36:37], 2, v[214:215]
	s_add_i32 m0, s84, 0x20000
	s_mov_b64 s[36:37], 0x20000
	global_load_lds_dwordx4 v[120:121], off nt
	v_lshl_add_u64 v[120:121], v[120:121], 0, s[36:37]
	s_mov_b32 m0, s85
	s_lshl_b32 s34, s34, 12
	global_load_lds_dwordx4 v[120:121], off nt
	s_and_b32 s34, s34, 0x7f0000
	s_or_b32 s34, s56, s34
	s_or_b32 s54, s54, s34
	s_add_i32 s62, s62, 1
	s_branch .LBB0_917

.LBB0_2052:
	s_add_u32 s0, s0, 0x80000
	s_addc_u32 s1, s1, 0
	s_mov_b32 m0, s65
	v_lshl_add_u64 v[176:177], s[0:1], 0, v[192:193]
	global_load_lds_dwordx4 v[176:177], off
	v_lshl_add_u64 v[176:177], s[0:1], 0, v[196:197]
	s_mov_b32 m0, s66
	s_nop 0
	global_load_lds_dwordx4 v[176:177], off
	s_waitcnt lgkmcnt(8)
	s_barrier
	s_waitcnt lgkmcnt(0)
	s_nop 0
	s_waitcnt lgkmcnt(0)
	v_mfma_f32_16x16x32_bf16 v[124:127], v[128:131], v[168:171], v[124:127]
	v_mfma_f32_16x16x32_bf16 v[120:123], v[136:139], v[168:171], v[120:123]
	v_mfma_f32_16x16x32_bf16 v[116:119], v[128:131], v[160:163], v[116:119]
	v_mfma_f32_16x16x32_bf16 v[112:115], v[136:139], v[160:163], v[112:115]
	v_mfma_f32_16x16x32_bf16 v[100:103], v[128:131], v[152:155], v[100:103]
	v_mfma_f32_16x16x32_bf16 v[96:99], v[136:139], v[152:155], v[96:99]
	v_mfma_f32_16x16x32_bf16 v[84:87], v[128:131], v[144:147], v[84:87]
	v_mfma_f32_16x16x32_bf16 v[80:83], v[136:139], v[144:147], v[80:83]
	v_mfma_f32_16x16x32_bf16 v[124:127], v[132:135], v[172:175], v[124:127]
	v_mfma_f32_16x16x32_bf16 v[120:123], v[140:143], v[172:175], v[120:123]
	v_mfma_f32_16x16x32_bf16 v[116:119], v[132:135], v[164:167], v[116:119]
	v_mfma_f32_16x16x32_bf16 v[112:115], v[140:143], v[164:167], v[112:115]
	v_mfma_f32_16x16x32_bf16 v[100:103], v[132:135], v[156:159], v[100:103]
	v_mfma_f32_16x16x32_bf16 v[96:99], v[140:143], v[156:159], v[96:99]
	v_mfma_f32_16x16x32_bf16 v[84:87], v[132:135], v[148:151], v[84:87]
	v_mfma_f32_16x16x32_bf16 v[80:83], v[140:143], v[148:151], v[80:83]
	s_nop 0
	s_barrier
	s_add_i32 s48, 0, 0x1c000
	s_mov_b32 m0, s76
	v_add_u32_e32 v188, s48, v232
	v_lshl_add_u64 v[222:223], v[222:223], 0, s[10:11]
	ds_read_b128 v[176:179], v188
	ds_read_b128 v[180:183], v188 offset:1024
	ds_read_b128 v[184:187], v188 offset:2048
	ds_read_b128 v[188:191], v188 offset:3072
	global_load_lds_dwordx4 v[222:223], off
	v_lshl_add_u64 v[222:223], v[224:225], 0, s[10:11]
	s_mov_b32 m0, s77
	s_nop 0
	global_load_lds_dwordx4 v[222:223], off
	s_barrier
	s_waitcnt lgkmcnt(0)
	s_nop 0
	s_waitcnt lgkmcnt(0)
	v_mfma_f32_16x16x32_bf16 v[108:111], v[176:179], v[168:171], v[108:111]
	v_mfma_f32_16x16x32_bf16 v[104:107], v[184:187], v[168:171], v[104:107]
	v_mfma_f32_16x16x32_bf16 v[92:95], v[176:179], v[160:163], v[92:95]
	v_mfma_f32_16x16x32_bf16 v[88:91], v[184:187], v[160:163], v[88:91]
	v_mfma_f32_16x16x32_bf16 v[76:79], v[176:179], v[152:155], v[76:79]
	v_mfma_f32_16x16x32_bf16 v[72:75], v[184:187], v[152:155], v[72:75]
	v_mfma_f32_16x16x32_bf16 v[68:71], v[176:179], v[144:147], v[68:71]
	v_mfma_f32_16x16x32_bf16 v[64:67], v[184:187], v[144:147], v[64:67]
	v_mfma_f32_16x16x32_bf16 v[108:111], v[180:183], v[172:175], v[108:111]
	v_mfma_f32_16x16x32_bf16 v[104:107], v[188:191], v[172:175], v[104:107]
	v_mfma_f32_16x16x32_bf16 v[92:95], v[180:183], v[164:167], v[92:95]
	v_mfma_f32_16x16x32_bf16 v[88:91], v[188:191], v[164:167], v[88:91]
	v_mfma_f32_16x16x32_bf16 v[76:79], v[180:183], v[156:159], v[76:79]
	v_mfma_f32_16x16x32_bf16 v[72:75], v[188:191], v[156:159], v[72:75]
	v_mfma_f32_16x16x32_bf16 v[68:71], v[180:183], v[148:151], v[68:71]
	v_mfma_f32_16x16x32_bf16 v[64:67], v[188:191], v[148:151], v[64:67]
	s_nop 0
	s_mov_b32 m0, s78
	v_lshl_add_u64 v[222:223], v[226:227], 0, s[10:11]
	s_barrier
	ds_read_b128 v[144:147], v235 offset:49152
	ds_read_b128 v[148:151], v235 offset:50176
	ds_read_b128 v[152:155], v235 offset:51200
	ds_read_b128 v[156:159], v235 offset:52224
	ds_read_b128 v[160:163], v235 offset:53248
	ds_read_b128 v[164:167], v235 offset:54272
	ds_read_b128 v[168:171], v235 offset:55296
	ds_read_b128 v[172:175], v235 offset:56320
	global_load_lds_dwordx4 v[222:223], off
	v_lshl_add_u64 v[222:223], v[228:229], 0, s[10:11]
	s_mov_b32 m0, s79
	s_nop 0
	global_load_lds_dwordx4 v[222:223], off
	s_barrier
	s_waitcnt lgkmcnt(0)
	s_nop 0
	s_waitcnt lgkmcnt(0)
	v_mfma_f32_16x16x32_bf16 v[60:63], v[128:131], v[144:147], v[60:63]
	v_mfma_f32_16x16x32_bf16 v[52:55], v[136:139], v[144:147], v[52:55]
	v_mfma_f32_16x16x32_bf16 v[44:47], v[128:131], v[152:155], v[44:47]
	v_mfma_f32_16x16x32_bf16 v[32:35], v[136:139], v[152:155], v[32:35]
	v_mfma_f32_16x16x32_bf16 v[20:23], v[128:131], v[160:163], v[20:23]
	v_mfma_f32_16x16x32_bf16 v[16:19], v[136:139], v[160:163], v[16:19]
	v_mfma_f32_16x16x32_bf16 v[4:7], v[128:131], v[168:171], v[4:7]
	v_mfma_f32_16x16x32_bf16 v[0:3], v[136:139], v[168:171], v[0:3]
	v_mfma_f32_16x16x32_bf16 v[60:63], v[132:135], v[148:151], v[60:63]
	v_mfma_f32_16x16x32_bf16 v[52:55], v[140:143], v[148:151], v[52:55]
	v_mfma_f32_16x16x32_bf16 v[44:47], v[132:135], v[156:159], v[44:47]
	v_mfma_f32_16x16x32_bf16 v[32:35], v[140:143], v[156:159], v[32:35]
	v_mfma_f32_16x16x32_bf16 v[20:23], v[132:135], v[164:167], v[20:23]
	v_mfma_f32_16x16x32_bf16 v[16:19], v[140:143], v[164:167], v[16:19]
	v_mfma_f32_16x16x32_bf16 v[4:7], v[132:135], v[172:175], v[4:7]
	v_mfma_f32_16x16x32_bf16 v[0:3], v[140:143], v[172:175], v[0:3]
	s_nop 0
	s_barrier
	s_add_u32 s0, s44, 0x80080
	s_addc_u32 s1, s45, 0
	s_add_i32 s44, s48, s58
	v_lshl_add_u64 v[128:129], s[0:1], 0, v[194:195]
	s_mov_b32 m0, s44
	s_nop 0
	global_load_lds_dwordx4 v[128:129], off
	v_lshl_add_u64 v[128:129], s[0:1], 0, v[198:199]
	s_add_i32 m0, s44, 0x2000
	s_nop 0
	global_load_lds_dwordx4 v[128:129], off
	s_waitcnt vmcnt(6)
	s_barrier
	s_nop 0
	v_mfma_f32_16x16x32_bf16 v[56:59], v[176:179], v[144:147], v[56:59]
	v_mfma_f32_16x16x32_bf16 v[48:51], v[184:187], v[144:147], v[48:51]
	v_mfma_f32_16x16x32_bf16 v[40:43], v[176:179], v[152:155], v[40:43]
	v_mfma_f32_16x16x32_bf16 v[36:39], v[184:187], v[152:155], v[36:39]
	v_mfma_f32_16x16x32_bf16 v[28:31], v[176:179], v[160:163], v[28:31]
	v_mfma_f32_16x16x32_bf16 v[24:27], v[184:187], v[160:163], v[24:27]
	v_mfma_f32_16x16x32_bf16 v[12:15], v[176:179], v[168:171], v[12:15]
	v_mfma_f32_16x16x32_bf16 v[8:11], v[184:187], v[168:171], v[8:11]
	v_mfma_f32_16x16x32_bf16 v[56:59], v[180:183], v[148:151], v[56:59]
	v_mfma_f32_16x16x32_bf16 v[48:51], v[188:191], v[148:151], v[48:51]
	v_mfma_f32_16x16x32_bf16 v[40:43], v[180:183], v[156:159], v[40:43]
	v_mfma_f32_16x16x32_bf16 v[36:39], v[188:191], v[156:159], v[36:39]
	v_mfma_f32_16x16x32_bf16 v[28:31], v[180:183], v[164:167], v[28:31]
	v_mfma_f32_16x16x32_bf16 v[24:27], v[188:191], v[164:167], v[24:27]
	v_mfma_f32_16x16x32_bf16 v[12:15], v[180:183], v[172:175], v[12:15]
	v_mfma_f32_16x16x32_bf16 v[8:11], v[188:191], v[172:175], v[8:11]
	s_nop 0
	s_add_i32 s91, s91, 2
	s_add_u32 s42, s42, 0x100
	s_addc_u32 s43, s43, 0
	s_add_u32 s29, s29, 0x100
	s_addc_u32 s41, s41, 0
	s_cmp_gt_u32 s91, 29
	s_barrier
	s_cbranch_scc1 .LBB0_2065
.LBB0_2053:
	ds_read_b128 v[144:147], v234
	ds_read_b128 v[148:151], v234 offset:1024
	ds_read_b128 v[152:155], v234 offset:2048
	ds_read_b128 v[156:159], v234 offset:3072
	s_xor_b64 s[48:49], s[38:39], -1
	v_lshl_add_u64 v[128:129], s[42:43], 0, v[208:209]
	s_add_i32 m0, s59, 0xc000
	ds_read_b128 v[184:187], v235
	ds_read_b128 v[188:191], v235 offset:1024
	ds_read_b128 v[176:179], v235 offset:2048
	ds_read_b128 v[180:183], v235 offset:3072
	ds_read_b128 v[168:171], v235 offset:4096
	ds_read_b128 v[172:175], v235 offset:5120
	ds_read_b128 v[160:163], v235 offset:6144
	ds_read_b128 v[164:167], v235 offset:7168
	global_load_lds_dwordx4 v[128:129], off
	v_lshl_add_u64 v[128:129], s[42:43], 0, v[210:211]
	s_add_i32 m0, s59, 0xe000
	s_nop 0
	global_load_lds_dwordx4 v[128:129], off
	s_waitcnt lgkmcnt(8)
	s_barrier
	s_waitcnt lgkmcnt(0)
	s_nop 0
	s_waitcnt lgkmcnt(0)
	v_mfma_f32_16x16x32_bf16 v[124:127], v[144:147], v[184:187], v[124:127]
	v_mfma_f32_16x16x32_bf16 v[120:123], v[152:155], v[184:187], v[120:123]
	v_mfma_f32_16x16x32_bf16 v[116:119], v[144:147], v[176:179], v[116:119]
	v_mfma_f32_16x16x32_bf16 v[112:115], v[152:155], v[176:179], v[112:115]
	v_mfma_f32_16x16x32_bf16 v[100:103], v[144:147], v[168:171], v[100:103]
	v_mfma_f32_16x16x32_bf16 v[96:99], v[152:155], v[168:171], v[96:99]
	v_mfma_f32_16x16x32_bf16 v[84:87], v[144:147], v[160:163], v[84:87]
	v_mfma_f32_16x16x32_bf16 v[80:83], v[152:155], v[160:163], v[80:83]
	v_mfma_f32_16x16x32_bf16 v[124:127], v[148:151], v[188:191], v[124:127]
	v_mfma_f32_16x16x32_bf16 v[120:123], v[156:159], v[188:191], v[120:123]
	v_mfma_f32_16x16x32_bf16 v[116:119], v[148:151], v[180:183], v[116:119]
	v_mfma_f32_16x16x32_bf16 v[112:115], v[156:159], v[180:183], v[112:115]
	v_mfma_f32_16x16x32_bf16 v[100:103], v[148:151], v[172:175], v[100:103]
	v_mfma_f32_16x16x32_bf16 v[96:99], v[156:159], v[172:175], v[96:99]
	v_mfma_f32_16x16x32_bf16 v[84:87], v[148:151], v[164:167], v[84:87]
	v_mfma_f32_16x16x32_bf16 v[80:83], v[156:159], v[164:167], v[80:83]
	s_nop 0
	s_barrier
	ds_read_b128 v[128:131], v236
	ds_read_b128 v[132:135], v236 offset:1024
	ds_read_b128 v[136:139], v236 offset:2048
	ds_read_b128 v[140:143], v236 offset:3072
	s_and_b64 vcc, exec, s[48:49]
	s_cbranch_vccnz .LBB0_2055
	v_add_u32_e32 v218, v231, v230
	ds_read2_b32 v[212:213], v218 offset1:32
	ds_read2_b32 v[214:215], v218 offset0:64 offset1:96
	ds_read2_b32 v[216:217], v218 offset0:128 offset1:160
	ds_read2_b32 v[218:219], v218 offset0:192 offset1:224

.LBB0_2057:
	s_nop 0
	s_waitcnt lgkmcnt(0)
	v_mfma_f32_16x16x32_bf16 v[108:111], v[128:131], v[184:187], v[108:111]
	v_mfma_f32_16x16x32_bf16 v[104:107], v[136:139], v[184:187], v[104:107]
	v_mfma_f32_16x16x32_bf16 v[92:95], v[128:131], v[176:179], v[92:95]
	v_mfma_f32_16x16x32_bf16 v[88:91], v[136:139], v[176:179], v[88:91]
	v_mfma_f32_16x16x32_bf16 v[76:79], v[128:131], v[168:171], v[76:79]
	v_mfma_f32_16x16x32_bf16 v[72:75], v[136:139], v[168:171], v[72:75]
	v_mfma_f32_16x16x32_bf16 v[68:71], v[128:131], v[160:163], v[68:71]
	v_mfma_f32_16x16x32_bf16 v[64:67], v[136:139], v[160:163], v[64:67]
	v_mfma_f32_16x16x32_bf16 v[108:111], v[132:135], v[188:191], v[108:111]
	v_mfma_f32_16x16x32_bf16 v[104:107], v[140:143], v[188:191], v[104:107]
	v_mfma_f32_16x16x32_bf16 v[92:95], v[132:135], v[180:183], v[92:95]
	v_mfma_f32_16x16x32_bf16 v[88:91], v[140:143], v[180:183], v[88:91]
	v_mfma_f32_16x16x32_bf16 v[76:79], v[132:135], v[172:175], v[76:79]
	v_mfma_f32_16x16x32_bf16 v[72:75], v[140:143], v[172:175], v[72:75]
	v_mfma_f32_16x16x32_bf16 v[68:71], v[132:135], v[164:167], v[68:71]
	v_mfma_f32_16x16x32_bf16 v[64:67], v[140:143], v[164:167], v[64:67]
	s_nop 0
	s_barrier
	ds_read_b128 v[184:187], v235 offset:16384
	ds_read_b128 v[188:191], v235 offset:17408
	ds_read_b128 v[176:179], v235 offset:18432
	ds_read_b128 v[180:183], v235 offset:19456
	ds_read_b128 v[168:171], v235 offset:20480
	ds_read_b128 v[172:175], v235 offset:21504
	ds_read_b128 v[160:163], v235 offset:22528
	ds_read_b128 v[164:167], v235 offset:23552
	s_and_b64 vcc, exec, s[0:1]
	s_cbranch_vccnz .LBB0_2059
	v_lshl_add_u64 v[226:227], v[204:205], 0, s[12:13]
	global_store_dwordx2 v[226:227], v[220:221], off
.LBB0_2059:
	s_add_u32 s38, s42, 0xfff80080
	s_addc_u32 s39, s43, -1
	s_and_b64 s[0:1], s[54:55], exec
	s_cselect_b32 s1, s35, s39
	s_cselect_b32 s0, s34, s38
	s_mov_b32 m0, s59
	v_lshl_add_u64 v[226:227], s[0:1], 0, v[192:193]
	global_load_lds_dwordx4 v[226:227], off
	v_lshl_add_u64 v[228:229], s[0:1], 0, v[196:197]
	s_mov_b32 m0, s62
	s_nop 0
	global_load_lds_dwordx4 v[228:229], off
	s_barrier
	s_waitcnt lgkmcnt(0)
	s_nop 0
	s_waitcnt lgkmcnt(0)
	v_mfma_f32_16x16x32_bf16 v[60:63], v[144:147], v[184:187], v[60:63]
	v_mfma_f32_16x16x32_bf16 v[52:55], v[152:155], v[184:187], v[52:55]
	v_mfma_f32_16x16x32_bf16 v[44:47], v[144:147], v[176:179], v[44:47]
	v_mfma_f32_16x16x32_bf16 v[32:35], v[152:155], v[176:179], v[32:35]
	v_mfma_f32_16x16x32_bf16 v[20:23], v[144:147], v[168:171], v[20:23]
	v_mfma_f32_16x16x32_bf16 v[16:19], v[152:155], v[168:171], v[16:19]
	v_mfma_f32_16x16x32_bf16 v[4:7], v[144:147], v[160:163], v[4:7]
	v_mfma_f32_16x16x32_bf16 v[0:3], v[152:155], v[160:163], v[0:3]
	v_mfma_f32_16x16x32_bf16 v[60:63], v[148:151], v[188:191], v[60:63]
	v_mfma_f32_16x16x32_bf16 v[52:55], v[156:159], v[188:191], v[52:55]
	v_mfma_f32_16x16x32_bf16 v[44:47], v[148:151], v[180:183], v[44:47]
	v_mfma_f32_16x16x32_bf16 v[32:35], v[156:159], v[180:183], v[32:35]
	v_mfma_f32_16x16x32_bf16 v[20:23], v[148:151], v[172:175], v[20:23]
	v_mfma_f32_16x16x32_bf16 v[16:19], v[156:159], v[172:175], v[16:19]
	v_mfma_f32_16x16x32_bf16 v[4:7], v[148:151], v[164:167], v[4:7]
	v_mfma_f32_16x16x32_bf16 v[0:3], v[156:159], v[164:167], v[0:3]
	s_nop 0
	s_barrier
	s_add_u32 s38, s44, 0x80000
	s_addc_u32 s39, s45, 0
	s_mov_b32 m0, s63
	v_lshl_add_u64 v[144:145], s[38:39], 0, v[194:195]
	global_load_lds_dwordx4 v[144:145], off
	v_lshl_add_u64 v[144:145], s[38:39], 0, v[198:199]
	s_mov_b32 m0, s64
	s_mov_b64 s[38:39], -1
	global_load_lds_dwordx4 v[144:145], off
	s_and_b64 vcc, exec, s[48:49]
	s_cbranch_vccz .LBB0_2061
	s_waitcnt vmcnt(6)
	s_mov_b64 s[38:39], 0

.LBB0_2063:
	s_barrier
	s_nop 0
	v_mfma_f32_16x16x32_bf16 v[56:59], v[128:131], v[184:187], v[56:59]
	v_mfma_f32_16x16x32_bf16 v[48:51], v[136:139], v[184:187], v[48:51]
	v_mfma_f32_16x16x32_bf16 v[40:43], v[128:131], v[176:179], v[40:43]
	v_mfma_f32_16x16x32_bf16 v[36:39], v[136:139], v[176:179], v[36:39]
	v_mfma_f32_16x16x32_bf16 v[28:31], v[128:131], v[168:171], v[28:31]
	v_mfma_f32_16x16x32_bf16 v[24:27], v[136:139], v[168:171], v[24:27]
	v_mfma_f32_16x16x32_bf16 v[12:15], v[128:131], v[160:163], v[12:15]
	v_mfma_f32_16x16x32_bf16 v[8:11], v[136:139], v[160:163], v[8:11]
	v_mfma_f32_16x16x32_bf16 v[56:59], v[132:135], v[188:191], v[56:59]
	v_mfma_f32_16x16x32_bf16 v[48:51], v[140:143], v[188:191], v[48:51]
	v_mfma_f32_16x16x32_bf16 v[40:43], v[132:135], v[180:183], v[40:43]
	v_mfma_f32_16x16x32_bf16 v[36:39], v[140:143], v[180:183], v[36:39]
	v_mfma_f32_16x16x32_bf16 v[28:31], v[132:135], v[172:175], v[28:31]
	v_mfma_f32_16x16x32_bf16 v[24:27], v[140:143], v[172:175], v[24:27]
	v_mfma_f32_16x16x32_bf16 v[12:15], v[132:135], v[164:167], v[12:15]
	v_mfma_f32_16x16x32_bf16 v[8:11], v[140:143], v[164:167], v[8:11]
	s_nop 0
	v_add_u32_e32 v140, 0x18000, v233
	s_barrier
	ds_read_b128 v[128:131], v140
	ds_read_b128 v[132:135], v140 offset:1024
	ds_read_b128 v[136:139], v140 offset:2048
	ds_read_b128 v[140:143], v140 offset:3072
	ds_read_b128 v[168:171], v235 offset:32768
	ds_read_b128 v[172:175], v235 offset:33792
	ds_read_b128 v[160:163], v235 offset:34816
	ds_read_b128 v[164:167], v235 offset:35840
	ds_read_b128 v[152:155], v235 offset:36864
	ds_read_b128 v[156:159], v235 offset:37888
	ds_read_b128 v[144:147], v235 offset:38912
	ds_read_b128 v[148:151], v235 offset:39936
	s_mul_i32 s38, s80, s19
	s_add_i32 s48, s33, s38
	s_cmp_lt_i32 s48, 0x10000
	s_cselect_b64 s[38:39], -1, 0
	s_cmp_gt_i32 s48, 0xffff
	s_cbranch_scc1 .LBB0_2052
	s_lshl_b32 s13, s48, 1
	s_and_b32 s13, s13, 0xe0
	s_and_b32 s49, s48, 0x780
	s_or_b32 s54, s13, s49
	s_add_i32 s49, s49, s13
	s_ashr_i32 s12, s48, 11
	s_addk_i32 s49, 0x780
	s_cmpk_lt_u32 s13, 0x80
	s_cselect_b32 s49, s54, s49
	s_lshl_b32 s54, s48, 7
	s_and_b32 s92, s54, 0x780
	s_ashr_i32 s13, s12, 31
	s_lshl_b32 s54, s92, 12
	s_lshl_b64 s[12:13], s[12:13], 23
	s_or_b32 s49, s49, s54
	s_or_b32 s54, s12, s49
	s_mov_b32 s55, s13
	v_lshl_add_u64 v[176:177], s[54:55], 2, v[206:207]
	s_add_i32 m0, s82, 0x20000
	s_lshl_b32 s48, s48, 12
	global_load_lds_dwordx4 v[176:177], off nt
	v_lshl_add_u64 v[176:177], v[176:177], 0, s[14:15]
	s_mov_b32 m0, s83
	s_and_b32 s48, s48, 0x7f0000
	global_load_lds_dwordx4 v[176:177], off nt
	s_or_b32 s48, s92, s48
	s_or_b32 s12, s12, s48
	s_add_i32 s80, s80, 1
	s_branch .LBB0_2052

.LBB0_2168:
	ds_read_b128 v[156:159], v145
	ds_read_b128 v[160:163], v145 offset:1024
	ds_read_b128 v[164:167], v145 offset:2048
	ds_read_b128 v[168:171], v145 offset:3072
	s_add_u32 s28, s16, 0xfff80080
	s_addc_u32 s29, s17, -1
	s_cmp_eq_u32 s56, 28
	s_cselect_b32 s31, s13, s29
	s_cselect_b32 s30, s12, s28
	s_cselect_b32 s29, s15, s55
	s_cselect_b32 s28, s14, s54
	v_lshl_add_u64 v[142:143], s[16:17], 0, v[136:137]
	s_add_i32 m0, s38, 0xc000
	ds_read_b128 v[172:175], v146
	ds_read_b128 v[176:179], v146 offset:1024
	ds_read_b128 v[180:183], v146 offset:2048
	ds_read_b128 v[184:187], v146 offset:3072
	ds_read_b128 v[188:191], v146 offset:4096
	ds_read_b128 v[192:195], v146 offset:5120
	ds_read_b128 v[196:199], v146 offset:6144
	ds_read_b128 v[200:203], v146 offset:7168
	global_load_lds_dwordx4 v[142:143], off
	v_lshl_add_u64 v[142:143], s[16:17], 0, v[138:139]
	s_add_i32 m0, s38, 0xe000
	s_nop 0
	global_load_lds_dwordx4 v[142:143], off
	s_waitcnt lgkmcnt(8)
	s_barrier
	s_waitcnt lgkmcnt(0)
	s_nop 0
	s_waitcnt lgkmcnt(0)
	v_mfma_f32_16x16x32_bf16 v[124:127], v[156:159], v[172:175], v[124:127]
	v_mfma_f32_16x16x32_bf16 v[120:123], v[164:167], v[172:175], v[120:123]
	v_mfma_f32_16x16x32_bf16 v[108:111], v[156:159], v[180:183], v[108:111]
	v_mfma_f32_16x16x32_bf16 v[104:107], v[164:167], v[180:183], v[104:107]
	v_mfma_f32_16x16x32_bf16 v[92:95], v[156:159], v[188:191], v[92:95]
	v_mfma_f32_16x16x32_bf16 v[88:91], v[164:167], v[188:191], v[88:91]
	v_mfma_f32_16x16x32_bf16 v[76:79], v[156:159], v[196:199], v[76:79]
	v_mfma_f32_16x16x32_bf16 v[72:75], v[164:167], v[196:199], v[72:75]
	v_mfma_f32_16x16x32_bf16 v[124:127], v[160:163], v[176:179], v[124:127]
	v_mfma_f32_16x16x32_bf16 v[120:123], v[168:171], v[176:179], v[120:123]
	v_mfma_f32_16x16x32_bf16 v[108:111], v[160:163], v[184:187], v[108:111]
	v_mfma_f32_16x16x32_bf16 v[104:107], v[168:171], v[184:187], v[104:107]
	v_mfma_f32_16x16x32_bf16 v[92:95], v[160:163], v[192:195], v[92:95]
	v_mfma_f32_16x16x32_bf16 v[88:91], v[168:171], v[192:195], v[88:91]
	v_mfma_f32_16x16x32_bf16 v[76:79], v[160:163], v[200:203], v[76:79]
	v_mfma_f32_16x16x32_bf16 v[72:75], v[168:171], v[200:203], v[72:75]
	s_nop 0
	s_barrier
	s_add_i32 s57, s45, s37
	v_lshl_add_u64 v[142:143], s[28:29], 0, v[130:131]
	s_mov_b32 m0, s57
	ds_read_b128 v[204:207], v147
	ds_read_b128 v[208:211], v147 offset:1024
	ds_read_b128 v[212:215], v147 offset:2048
	ds_read_b128 v[216:219], v147 offset:3072
	global_load_lds_dwordx4 v[142:143], off
	v_lshl_add_u64 v[220:221], s[28:29], 0, v[134:135]
	s_add_i32 m0, s57, 0x2000
	s_nop 0
	global_load_lds_dwordx4 v[220:221], off
	s_barrier
	s_waitcnt lgkmcnt(0)
	s_nop 0
	s_waitcnt lgkmcnt(0)
	v_mfma_f32_16x16x32_bf16 v[116:119], v[204:207], v[172:175], v[116:119]
	v_mfma_f32_16x16x32_bf16 v[112:115], v[212:215], v[172:175], v[112:115]
	v_mfma_f32_16x16x32_bf16 v[100:103], v[204:207], v[180:183], v[100:103]
	v_mfma_f32_16x16x32_bf16 v[96:99], v[212:215], v[180:183], v[96:99]
	v_mfma_f32_16x16x32_bf16 v[84:87], v[204:207], v[188:191], v[84:87]
	v_mfma_f32_16x16x32_bf16 v[80:83], v[212:215], v[188:191], v[80:83]
	v_mfma_f32_16x16x32_bf16 v[68:71], v[204:207], v[196:199], v[68:71]
	v_mfma_f32_16x16x32_bf16 v[64:67], v[212:215], v[196:199], v[64:67]
	v_mfma_f32_16x16x32_bf16 v[116:119], v[208:211], v[176:179], v[116:119]
	v_mfma_f32_16x16x32_bf16 v[112:115], v[216:219], v[176:179], v[112:115]
	v_mfma_f32_16x16x32_bf16 v[100:103], v[208:211], v[184:187], v[100:103]
	v_mfma_f32_16x16x32_bf16 v[96:99], v[216:219], v[184:187], v[96:99]
	v_mfma_f32_16x16x32_bf16 v[84:87], v[208:211], v[192:195], v[84:87]
	v_mfma_f32_16x16x32_bf16 v[80:83], v[216:219], v[192:195], v[80:83]
	v_mfma_f32_16x16x32_bf16 v[68:71], v[208:211], v[200:203], v[68:71]
	v_mfma_f32_16x16x32_bf16 v[64:67], v[216:219], v[200:203], v[64:67]
	s_nop 0
	s_mov_b32 m0, s38
	v_lshl_add_u64 v[222:223], s[30:31], 0, v[128:129]
	s_barrier
	ds_read_b128 v[172:175], v146 offset:16384
	ds_read_b128 v[176:179], v146 offset:17408
	ds_read_b128 v[180:183], v146 offset:18432
	ds_read_b128 v[184:187], v146 offset:19456
	ds_read_b128 v[188:191], v146 offset:20480
	ds_read_b128 v[192:195], v146 offset:21504
	ds_read_b128 v[196:199], v146 offset:22528
	ds_read_b128 v[200:203], v146 offset:23552
	global_load_lds_dwordx4 v[222:223], off
	v_lshl_add_u64 v[224:225], s[30:31], 0, v[132:133]
	s_mov_b32 m0, s39
	s_nop 0
	global_load_lds_dwordx4 v[224:225], off
	s_barrier
	s_waitcnt lgkmcnt(0)
	s_nop 0
	s_waitcnt lgkmcnt(0)
	v_mfma_f32_16x16x32_bf16 v[60:63], v[156:159], v[172:175], v[60:63]
	v_mfma_f32_16x16x32_bf16 v[56:59], v[164:167], v[172:175], v[56:59]
	v_mfma_f32_16x16x32_bf16 v[44:47], v[156:159], v[180:183], v[44:47]
	v_mfma_f32_16x16x32_bf16 v[40:43], v[164:167], v[180:183], v[40:43]
	v_mfma_f32_16x16x32_bf16 v[28:31], v[156:159], v[188:191], v[28:31]
	v_mfma_f32_16x16x32_bf16 v[24:27], v[164:167], v[188:191], v[24:27]
	v_mfma_f32_16x16x32_bf16 v[12:15], v[156:159], v[196:199], v[12:15]
	v_mfma_f32_16x16x32_bf16 v[8:11], v[164:167], v[196:199], v[8:11]
	v_mfma_f32_16x16x32_bf16 v[60:63], v[160:163], v[176:179], v[60:63]
	v_mfma_f32_16x16x32_bf16 v[56:59], v[168:171], v[176:179], v[56:59]
	v_mfma_f32_16x16x32_bf16 v[44:47], v[160:163], v[184:187], v[44:47]
	v_mfma_f32_16x16x32_bf16 v[40:43], v[168:171], v[184:187], v[40:43]
	v_mfma_f32_16x16x32_bf16 v[28:31], v[160:163], v[192:195], v[28:31]
	v_mfma_f32_16x16x32_bf16 v[24:27], v[168:171], v[192:195], v[24:27]
	v_mfma_f32_16x16x32_bf16 v[12:15], v[160:163], v[200:203], v[12:15]
	v_mfma_f32_16x16x32_bf16 v[8:11], v[168:171], v[200:203], v[8:11]
	s_nop 0
	s_barrier
	s_add_u32 s58, s28, 0x80000
	s_addc_u32 s59, s29, 0
	s_add_i32 s57, s48, s37
	v_lshl_add_u64 v[156:157], s[58:59], 0, v[130:131]
	s_mov_b32 m0, s57
	s_nop 0
	global_load_lds_dwordx4 v[156:157], off
	v_lshl_add_u64 v[156:157], s[58:59], 0, v[134:135]
	s_add_i32 m0, s57, 0x2000
	s_nop 0
	global_load_lds_dwordx4 v[156:157], off
	s_waitcnt vmcnt(6)
	s_barrier
	s_nop 0
	v_mfma_f32_16x16x32_bf16 v[52:55], v[204:207], v[172:175], v[52:55]
	v_mfma_f32_16x16x32_bf16 v[48:51], v[212:215], v[172:175], v[48:51]
	v_mfma_f32_16x16x32_bf16 v[36:39], v[204:207], v[180:183], v[36:39]
	v_mfma_f32_16x16x32_bf16 v[32:35], v[212:215], v[180:183], v[32:35]
	v_mfma_f32_16x16x32_bf16 v[20:23], v[204:207], v[188:191], v[20:23]
	v_mfma_f32_16x16x32_bf16 v[16:19], v[212:215], v[188:191], v[16:19]
	v_mfma_f32_16x16x32_bf16 v[4:7], v[204:207], v[196:199], v[4:7]
	v_mfma_f32_16x16x32_bf16 v[0:3], v[212:215], v[196:199], v[0:3]
	v_mfma_f32_16x16x32_bf16 v[52:55], v[208:211], v[176:179], v[52:55]
	v_mfma_f32_16x16x32_bf16 v[48:51], v[216:219], v[176:179], v[48:51]
	v_mfma_f32_16x16x32_bf16 v[36:39], v[208:211], v[184:187], v[36:39]
	v_mfma_f32_16x16x32_bf16 v[32:35], v[216:219], v[184:187], v[32:35]
	v_mfma_f32_16x16x32_bf16 v[20:23], v[208:211], v[192:195], v[20:23]
	v_mfma_f32_16x16x32_bf16 v[16:19], v[216:219], v[192:195], v[16:19]
	v_mfma_f32_16x16x32_bf16 v[4:7], v[208:211], v[200:203], v[4:7]
	v_mfma_f32_16x16x32_bf16 v[0:3], v[216:219], v[200:203], v[0:3]
	s_nop 0
	s_add_i32 s57, 0, 0x18000
	v_add_u32_e32 v140, s57, v144
	s_barrier
	ds_read_b128 v[156:159], v140
	ds_read_b128 v[160:163], v140 offset:1024
	ds_read_b128 v[164:167], v140 offset:2048
	ds_read_b128 v[168:171], v140 offset:3072
	s_add_u32 s30, s30, 0x80000
	s_addc_u32 s31, s31, 0
	s_mov_b32 m0, s40
	v_lshl_add_u64 v[204:205], s[30:31], 0, v[128:129]
	ds_read_b128 v[172:175], v146 offset:32768
	ds_read_b128 v[176:179], v146 offset:33792
	ds_read_b128 v[180:183], v146 offset:34816
	ds_read_b128 v[184:187], v146 offset:35840
	ds_read_b128 v[188:191], v146 offset:36864
	ds_read_b128 v[192:195], v146 offset:37888
	ds_read_b128 v[196:199], v146 offset:38912
	ds_read_b128 v[200:203], v146 offset:39936
	global_load_lds_dwordx4 v[204:205], off
	v_lshl_add_u64 v[204:205], s[30:31], 0, v[132:133]
	s_mov_b32 m0, s41
	s_nop 0
	global_load_lds_dwordx4 v[204:205], off
	s_waitcnt lgkmcnt(8)
	s_barrier
	s_waitcnt lgkmcnt(0)
	s_nop 0
	s_waitcnt lgkmcnt(0)
	v_mfma_f32_16x16x32_bf16 v[124:127], v[156:159], v[172:175], v[124:127]
	v_mfma_f32_16x16x32_bf16 v[120:123], v[164:167], v[172:175], v[120:123]
	v_mfma_f32_16x16x32_bf16 v[108:111], v[156:159], v[180:183], v[108:111]
	v_mfma_f32_16x16x32_bf16 v[104:107], v[164:167], v[180:183], v[104:107]
	v_mfma_f32_16x16x32_bf16 v[92:95], v[156:159], v[188:191], v[92:95]
	v_mfma_f32_16x16x32_bf16 v[88:91], v[164:167], v[188:191], v[88:91]
	v_mfma_f32_16x16x32_bf16 v[76:79], v[156:159], v[196:199], v[76:79]
	v_mfma_f32_16x16x32_bf16 v[72:75], v[164:167], v[196:199], v[72:75]
	v_mfma_f32_16x16x32_bf16 v[124:127], v[160:163], v[176:179], v[124:127]
	v_mfma_f32_16x16x32_bf16 v[120:123], v[168:171], v[176:179], v[120:123]
	v_mfma_f32_16x16x32_bf16 v[108:111], v[160:163], v[184:187], v[108:111]
	v_mfma_f32_16x16x32_bf16 v[104:107], v[168:171], v[184:187], v[104:107]
	v_mfma_f32_16x16x32_bf16 v[92:95], v[160:163], v[192:195], v[92:95]
	v_mfma_f32_16x16x32_bf16 v[88:91], v[168:171], v[192:195], v[88:91]
	v_mfma_f32_16x16x32_bf16 v[76:79], v[160:163], v[200:203], v[76:79]
	v_mfma_f32_16x16x32_bf16 v[72:75], v[168:171], v[200:203], v[72:75]
	s_nop 0
	s_barrier
	s_add_i32 s30, 0, 0x1c000
	s_add_i32 s31, s57, s37
	v_add_u32_e32 v140, s30, v144
	v_lshl_add_u64 v[142:143], v[142:143], 0, s[6:7]
	s_mov_b32 m0, s31
	ds_read_b128 v[204:207], v140
	ds_read_b128 v[208:211], v140 offset:1024
	ds_read_b128 v[212:215], v140 offset:2048
	ds_read_b128 v[216:219], v140 offset:3072
	global_load_lds_dwordx4 v[142:143], off
	v_lshl_add_u64 v[142:143], v[220:221], 0, s[6:7]
	s_add_i32 m0, s31, 0x2000
	s_nop 0
	global_load_lds_dwordx4 v[142:143], off
	s_barrier
	s_waitcnt lgkmcnt(0)
	s_nop 0
	s_waitcnt lgkmcnt(0)
	v_mfma_f32_16x16x32_bf16 v[116:119], v[204:207], v[172:175], v[116:119]
	v_mfma_f32_16x16x32_bf16 v[112:115], v[212:215], v[172:175], v[112:115]
	v_mfma_f32_16x16x32_bf16 v[100:103], v[204:207], v[180:183], v[100:103]
	v_mfma_f32_16x16x32_bf16 v[96:99], v[212:215], v[180:183], v[96:99]
	v_mfma_f32_16x16x32_bf16 v[84:87], v[204:207], v[188:191], v[84:87]
	v_mfma_f32_16x16x32_bf16 v[80:83], v[212:215], v[188:191], v[80:83]
	v_mfma_f32_16x16x32_bf16 v[68:71], v[204:207], v[196:199], v[68:71]
	v_mfma_f32_16x16x32_bf16 v[64:67], v[212:215], v[196:199], v[64:67]
	v_mfma_f32_16x16x32_bf16 v[116:119], v[208:211], v[176:179], v[116:119]
	v_mfma_f32_16x16x32_bf16 v[112:115], v[216:219], v[176:179], v[112:115]
	v_mfma_f32_16x16x32_bf16 v[100:103], v[208:211], v[184:187], v[100:103]
	v_mfma_f32_16x16x32_bf16 v[96:99], v[216:219], v[184:187], v[96:99]
	v_mfma_f32_16x16x32_bf16 v[84:87], v[208:211], v[192:195], v[84:87]
	v_mfma_f32_16x16x32_bf16 v[80:83], v[216:219], v[192:195], v[80:83]
	v_mfma_f32_16x16x32_bf16 v[68:71], v[208:211], v[200:203], v[68:71]
	v_mfma_f32_16x16x32_bf16 v[64:67], v[216:219], v[200:203], v[64:67]
	s_nop 0
	s_mov_b32 m0, s43
	v_lshl_add_u64 v[142:143], v[222:223], 0, s[6:7]
	s_barrier
	ds_read_b128 v[172:175], v146 offset:49152
	ds_read_b128 v[176:179], v146 offset:50176
	ds_read_b128 v[180:183], v146 offset:51200
	ds_read_b128 v[184:187], v146 offset:52224
	ds_read_b128 v[188:191], v146 offset:53248
	ds_read_b128 v[192:195], v146 offset:54272
	ds_read_b128 v[196:199], v146 offset:55296
	ds_read_b128 v[200:203], v146 offset:56320
	global_load_lds_dwordx4 v[142:143], off
	v_lshl_add_u64 v[142:143], v[224:225], 0, s[6:7]
	s_mov_b32 m0, s44
	s_nop 0
	global_load_lds_dwordx4 v[142:143], off
	s_barrier
;     __device__ __forceinline__ void operator()(const f32x4 (&acc)[2][2][4][2], const Unit& u, int wr, int wc, int fr, int fq, const Pre& pr) const {
;         const float (&rsv)[8] = pr.rsv;
; #pragma unroll
;         for (int ai = 0; ai < 2; ++ai)
; #pragma unroll
;             for (int m = 0; m < 4; ++m) {
;                 const int row = u.pm * 256 + ai * 128 + wr * 64 + m * 16 + fr; const float rs = __builtin_amdgcn_rsqf(rsv[ai * 4 + m] * (1.0f / DM) + NORM_EPS);
; #pragma unroll
;                 for (int bj = 0; bj < 2; ++bj) st_bf16x8(out + (size_t)row * ldo + u.pn * 256 + 128 * bj + 32 * wc + 8 * fq, acc[ai][bj][m][0] * rs, acc[ai][bj][m][1] * rs);
;             }
	s_waitcnt lgkmcnt(0)
	s_nop 0
	s_waitcnt lgkmcnt(0)
	v_mfma_f32_16x16x32_bf16 v[60:63], v[156:159], v[172:175], v[60:63]
	v_mfma_f32_16x16x32_bf16 v[56:59], v[164:167], v[172:175], v[56:59]
	v_mfma_f32_16x16x32_bf16 v[44:47], v[156:159], v[180:183], v[44:47]
	v_mfma_f32_16x16x32_bf16 v[40:43], v[164:167], v[180:183], v[40:43]
	v_mfma_f32_16x16x32_bf16 v[28:31], v[156:159], v[188:191], v[28:31]
	v_mfma_f32_16x16x32_bf16 v[24:27], v[164:167], v[188:191], v[24:27]
	v_mfma_f32_16x16x32_bf16 v[12:15], v[156:159], v[196:199], v[12:15]
	v_mfma_f32_16x16x32_bf16 v[8:11], v[164:167], v[196:199], v[8:11]
	v_mfma_f32_16x16x32_bf16 v[60:63], v[160:163], v[176:179], v[60:63]
	v_mfma_f32_16x16x32_bf16 v[56:59], v[168:171], v[176:179], v[56:59]
	v_mfma_f32_16x16x32_bf16 v[44:47], v[160:163], v[184:187], v[44:47]
	v_mfma_f32_16x16x32_bf16 v[40:43], v[168:171], v[184:187], v[40:43]
	v_mfma_f32_16x16x32_bf16 v[28:31], v[160:163], v[192:195], v[28:31]
	v_mfma_f32_16x16x32_bf16 v[24:27], v[168:171], v[192:195], v[24:27]
	v_mfma_f32_16x16x32_bf16 v[12:15], v[160:163], v[200:203], v[12:15]
	v_mfma_f32_16x16x32_bf16 v[8:11], v[168:171], v[200:203], v[8:11]
	s_nop 0
	s_barrier
	s_add_u32 s28, s28, 0x80080
	s_addc_u32 s29, s29, 0
	s_add_i32 s30, s30, s37
	v_lshl_add_u64 v[142:143], s[28:29], 0, v[130:131]
	s_mov_b32 m0, s30
	s_nop 0
	global_load_lds_dwordx4 v[142:143], off
	v_lshl_add_u64 v[142:143], s[28:29], 0, v[134:135]
	s_add_i32 m0, s30, 0x2000
	s_nop 0
	global_load_lds_dwordx4 v[142:143], off
	s_waitcnt vmcnt(6)
	s_barrier
	s_nop 0
	v_mfma_f32_16x16x32_bf16 v[52:55], v[204:207], v[172:175], v[52:55]
	v_mfma_f32_16x16x32_bf16 v[48:51], v[212:215], v[172:175], v[48:51]
	v_mfma_f32_16x16x32_bf16 v[36:39], v[204:207], v[180:183], v[36:39]
	v_mfma_f32_16x16x32_bf16 v[32:35], v[212:215], v[180:183], v[32:35]
	v_mfma_f32_16x16x32_bf16 v[20:23], v[204:207], v[188:191], v[20:23]
	v_mfma_f32_16x16x32_bf16 v[16:19], v[212:215], v[188:191], v[16:19]
	v_mfma_f32_16x16x32_bf16 v[4:7], v[204:207], v[196:199], v[4:7]
	v_mfma_f32_16x16x32_bf16 v[0:3], v[212:215], v[196:199], v[0:3]
	v_mfma_f32_16x16x32_bf16 v[52:55], v[208:211], v[176:179], v[52:55]
	v_mfma_f32_16x16x32_bf16 v[48:51], v[216:219], v[176:179], v[48:51]
	v_mfma_f32_16x16x32_bf16 v[36:39], v[208:211], v[184:187], v[36:39]
	v_mfma_f32_16x16x32_bf16 v[32:35], v[216:219], v[184:187], v[32:35]
	v_mfma_f32_16x16x32_bf16 v[20:23], v[208:211], v[192:195], v[20:23]
	v_mfma_f32_16x16x32_bf16 v[16:19], v[216:219], v[192:195], v[16:19]
	v_mfma_f32_16x16x32_bf16 v[4:7], v[208:211], v[200:203], v[4:7]
	v_mfma_f32_16x16x32_bf16 v[0:3], v[216:219], v[200:203], v[0:3]
	s_nop 0
	s_add_i32 s56, s56, 2
	s_add_u32 s16, s16, 0x100
	s_addc_u32 s17, s17, 0
	s_add_u32 s54, s54, 0x100
	s_addc_u32 s55, s55, 0
	s_cmp_gt_u32 s56, 29
	s_barrier
	s_cbranch_scc0 .LBB0_2168
	v_mbcnt_lo_u32_b32 v142, -1, 0
	v_mbcnt_hi_u32_b32 v142, -1, v142
	s_waitcnt vmcnt(0)
	v_fmamk_f32 v141, v141, 0x3a000000, v148
	v_and_or_b32 v140, v142, 15, s11
	s_lshl_b32 s16, s53, 8
	v_rsq_f32_e32 v156, v141
	v_ashrrev_i32_e32 v141, 31, v140
	s_ashr_i32 s17, s16, 31
	v_ashrrev_i32_e32 v142, 1, v142
	v_lshlrev_b64 v[158:159], 10, v[140:141]
	v_and_b32_e32 v142, -8, v142
	v_lshl_add_u64 v[158:159], s[4:5], 0, v[158:159]
	s_lshl_b64 s[16:17], s[16:17], 1
	v_ashrrev_i32_e32 v143, 31, v142
	v_lshl_add_u64 v[158:159], v[158:159], 0, s[16:17]
	v_lshl_add_u64 v[158:159], v[158:159], 0, s[0:1]
	v_lshlrev_b64 v[142:143], 1, v[142:143]
	v_lshl_add_u64 v[158:159], v[158:159], 0, v[142:143]
	v_pk_mul_f32 v[126:127], v[156:157], v[126:127] op_sel_hi:[0,1]
	v_pk_mul_f32 v[124:125], v[156:157], v[124:125] op_sel_hi:[0,1]
	v_pk_mul_f32 v[160:161], v[156:157], v[122:123] op_sel_hi:[0,1]
	v_pk_mul_f32 v[122:123], v[156:157], v[120:121] op_sel_hi:[0,1]
	v_cvt_pk_bf16_f32 v120, v124, v125
	v_cvt_pk_bf16_f32 v121, v126, v127
	v_cvt_pk_bf16_f32 v122, v122, v123
	v_cvt_pk_bf16_f32 v123, v160, v161
	global_store_dwordx4 v[158:159], v[120:123], off
	v_pk_mul_f32 v[118:119], v[156:157], v[118:119] op_sel_hi:[0,1]
	v_pk_mul_f32 v[116:117], v[156:157], v[116:117] op_sel_hi:[0,1]
	v_pk_mul_f32 v[120:121], v[156:157], v[114:115] op_sel_hi:[0,1]
	v_pk_mul_f32 v[114:115], v[156:157], v[112:113] op_sel_hi:[0,1]
	v_cvt_pk_bf16_f32 v112, v116, v117
	v_cvt_pk_bf16_f32 v113, v118, v119
	v_cvt_pk_bf16_f32 v114, v114, v115
	v_cvt_pk_bf16_f32 v115, v120, v121
	global_store_dwordx4 v[158:159], v[112:115], off offset:256
	s_and_b64 vcc, exec, s[8:9]
	s_mov_b32 s30, s10
	v_or_b32_e32 v112, 16, v140
	v_fmamk_f32 v113, v155, 0x3a000000, v148
	v_rsq_f32_e32 v114, v113
	v_ashrrev_i32_e32 v113, 31, v112
	v_lshlrev_b64 v[112:113], 10, v[112:113]
	v_lshl_add_u64 v[112:113], s[4:5], 0, v[112:113]
	v_lshl_add_u64 v[112:113], v[112:113], 0, s[16:17]
	v_lshl_add_u64 v[112:113], v[112:113], 0, s[0:1]
	v_lshl_add_u64 v[112:113], v[112:113], 0, v[142:143]
	v_pk_mul_f32 v[110:111], v[114:115], v[110:111] op_sel_hi:[0,1]
	v_pk_mul_f32 v[108:109], v[114:115], v[108:109] op_sel_hi:[0,1]
	v_pk_mul_f32 v[116:117], v[114:115], v[106:107] op_sel_hi:[0,1]
	v_pk_mul_f32 v[106:107], v[114:115], v[104:105] op_sel_hi:[0,1]
	v_cvt_pk_bf16_f32 v104, v108, v109
	v_cvt_pk_bf16_f32 v105, v110, v111
	v_cvt_pk_bf16_f32 v106, v106, v107
	v_cvt_pk_bf16_f32 v107, v116, v117
	global_store_dwordx4 v[112:113], v[104:107], off
	v_pk_mul_f32 v[102:103], v[114:115], v[102:103] op_sel_hi:[0,1]
	v_pk_mul_f32 v[100:101], v[114:115], v[100:101] op_sel_hi:[0,1]
	v_pk_mul_f32 v[104:105], v[114:115], v[98:99] op_sel_hi:[0,1]
	v_pk_mul_f32 v[98:99], v[114:115], v[96:97] op_sel_hi:[0,1]
	v_cvt_pk_bf16_f32 v96, v100, v101
	v_cvt_pk_bf16_f32 v97, v102, v103
;     __device__ __forceinline__ void operator()(const f32x4 (&acc)[2][2][4][2], const Unit& u, int wr, int wc, int fr, int fq, const Pre& pr) const {
;         const float (&rsv)[8] = pr.rsv;
; #pragma unroll
;         for (int ai = 0; ai < 2; ++ai)
; #pragma unroll
;             for (int m = 0; m < 4; ++m) {
;                 const int row = u.pm * 256 + ai * 128 + wr * 64 + m * 16 + fr; const float rs = __builtin_amdgcn_rsqf(rsv[ai * 4 + m] * (1.0f / DM) + NORM_EPS);
; #pragma unroll
;                 for (int bj = 0; bj < 2; ++bj) st_bf16x8(out + (size_t)row * ldo + u.pn * 256 + 128 * bj + 32 * wc + 8 * fq, acc[ai][bj][m][0] * rs, acc[ai][bj][m][1] * rs);
;             }
	v_cvt_pk_bf16_f32 v98, v98, v99
	v_cvt_pk_bf16_f32 v99, v104, v105
	global_store_dwordx4 v[112:113], v[96:99], off offset:256
	s_mov_b32 s53, s52
	s_mov_b64 s[28:29], s[14:15]
	v_or_b32_e32 v96, 32, v140
	v_fmamk_f32 v97, v154, 0x3a000000, v148
	v_rsq_f32_e32 v98, v97
	v_ashrrev_i32_e32 v97, 31, v96
	v_lshlrev_b64 v[96:97], 10, v[96:97]
	v_lshl_add_u64 v[96:97], s[4:5], 0, v[96:97]
	v_lshl_add_u64 v[96:97], v[96:97], 0, s[16:17]
	v_lshl_add_u64 v[96:97], v[96:97], 0, s[0:1]
	v_lshl_add_u64 v[96:97], v[96:97], 0, v[142:143]
	v_pk_mul_f32 v[94:95], v[98:99], v[94:95] op_sel_hi:[0,1]
	v_pk_mul_f32 v[92:93], v[98:99], v[92:93] op_sel_hi:[0,1]
	v_pk_mul_f32 v[100:101], v[98:99], v[90:91] op_sel_hi:[0,1]
	v_pk_mul_f32 v[90:91], v[98:99], v[88:89] op_sel_hi:[0,1]
	v_cvt_pk_bf16_f32 v88, v92, v93
	v_cvt_pk_bf16_f32 v89, v94, v95
	v_cvt_pk_bf16_f32 v90, v90, v91
	v_cvt_pk_bf16_f32 v91, v100, v101
	global_store_dwordx4 v[96:97], v[88:91], off
	v_pk_mul_f32 v[86:87], v[98:99], v[86:87] op_sel_hi:[0,1]
	v_pk_mul_f32 v[84:85], v[98:99], v[84:85] op_sel_hi:[0,1]
	v_pk_mul_f32 v[88:89], v[98:99], v[82:83] op_sel_hi:[0,1]
	v_pk_mul_f32 v[82:83], v[98:99], v[80:81] op_sel_hi:[0,1]
	v_cvt_pk_bf16_f32 v80, v84, v85
	v_cvt_pk_bf16_f32 v81, v86, v87
	v_cvt_pk_bf16_f32 v82, v82, v83
	v_cvt_pk_bf16_f32 v83, v88, v89
	global_store_dwordx4 v[96:97], v[80:83], off offset:256
	s_nop 1
	v_or_b32_e32 v80, 48, v140
	v_fmamk_f32 v81, v153, 0x3a000000, v148
	v_rsq_f32_e32 v82, v81
	v_ashrrev_i32_e32 v81, 31, v80
	v_lshlrev_b64 v[80:81], 10, v[80:81]
	v_lshl_add_u64 v[80:81], s[4:5], 0, v[80:81]
	v_lshl_add_u64 v[80:81], v[80:81], 0, s[16:17]
	v_lshl_add_u64 v[80:81], v[80:81], 0, s[0:1]
	v_lshl_add_u64 v[80:81], v[80:81], 0, v[142:143]
	v_pk_mul_f32 v[78:79], v[82:83], v[78:79] op_sel_hi:[0,1]
	v_pk_mul_f32 v[76:77], v[82:83], v[76:77] op_sel_hi:[0,1]
	v_pk_mul_f32 v[84:85], v[82:83], v[74:75] op_sel_hi:[0,1]
	v_pk_mul_f32 v[74:75], v[82:83], v[72:73] op_sel_hi:[0,1]
	v_cvt_pk_bf16_f32 v72, v76, v77
	v_cvt_pk_bf16_f32 v73, v78, v79
	v_cvt_pk_bf16_f32 v74, v74, v75
	v_cvt_pk_bf16_f32 v75, v84, v85
	global_store_dwordx4 v[80:81], v[72:75], off
	v_pk_mul_f32 v[70:71], v[82:83], v[70:71] op_sel_hi:[0,1]
	v_pk_mul_f32 v[68:69], v[82:83], v[68:69] op_sel_hi:[0,1]
	v_pk_mul_f32 v[72:73], v[82:83], v[66:67] op_sel_hi:[0,1]
	v_pk_mul_f32 v[66:67], v[82:83], v[64:65] op_sel_hi:[0,1]
	v_cvt_pk_bf16_f32 v64, v68, v69
	v_cvt_pk_bf16_f32 v65, v70, v71
	v_cvt_pk_bf16_f32 v66, v66, v67
	v_cvt_pk_bf16_f32 v67, v72, v73
	global_store_dwordx4 v[80:81], v[64:67], off offset:256
	s_nop 1
	v_add_u32_e32 v64, 0x80, v140
	v_fmamk_f32 v65, v152, 0x3a000000, v148
	v_rsq_f32_e32 v66, v65
	v_ashrrev_i32_e32 v65, 31, v64
	v_lshlrev_b64 v[64:65], 10, v[64:65]
	v_lshl_add_u64 v[64:65], s[4:5], 0, v[64:65]
	v_lshl_add_u64 v[64:65], v[64:65], 0, s[16:17]
	v_lshl_add_u64 v[64:65], v[64:65], 0, s[0:1]
	v_lshl_add_u64 v[64:65], v[64:65], 0, v[142:143]
	v_pk_mul_f32 v[62:63], v[66:67], v[62:63] op_sel_hi:[0,1]
	v_pk_mul_f32 v[60:61], v[66:67], v[60:61] op_sel_hi:[0,1]
	v_pk_mul_f32 v[68:69], v[66:67], v[58:59] op_sel_hi:[0,1]
	v_pk_mul_f32 v[58:59], v[66:67], v[56:57] op_sel_hi:[0,1]
	v_cvt_pk_bf16_f32 v56, v60, v61
	v_cvt_pk_bf16_f32 v57, v62, v63
	v_cvt_pk_bf16_f32 v58, v58, v59
	v_cvt_pk_bf16_f32 v59, v68, v69
	global_store_dwordx4 v[64:65], v[56:59], off
	v_pk_mul_f32 v[54:55], v[66:67], v[54:55] op_sel_hi:[0,1]
	v_pk_mul_f32 v[52:53], v[66:67], v[52:53] op_sel_hi:[0,1]
	v_pk_mul_f32 v[56:57], v[66:67], v[50:51] op_sel_hi:[0,1]
	v_pk_mul_f32 v[50:51], v[66:67], v[48:49] op_sel_hi:[0,1]
	v_cvt_pk_bf16_f32 v48, v52, v53
	v_cvt_pk_bf16_f32 v49, v54, v55
	v_cvt_pk_bf16_f32 v50, v50, v51
	v_cvt_pk_bf16_f32 v51, v56, v57
;     __device__ __forceinline__ void operator()(const f32x4 (&acc)[2][2][4][2], const Unit& u, int wr, int wc, int fr, int fq, const Pre& pr) const {
;         const float (&rsv)[8] = pr.rsv;
; #pragma unroll
;         for (int ai = 0; ai < 2; ++ai)
; #pragma unroll
;             for (int m = 0; m < 4; ++m) {
;                 const int row = u.pm * 256 + ai * 128 + wr * 64 + m * 16 + fr; const float rs = __builtin_amdgcn_rsqf(rsv[ai * 4 + m] * (1.0f / DM) + NORM_EPS);
; #pragma unroll
;                 for (int bj = 0; bj < 2; ++bj) st_bf16x8(out + (size_t)row * ldo + u.pn * 256 + 128 * bj + 32 * wc + 8 * fq, acc[ai][bj][m][0] * rs, acc[ai][bj][m][1] * rs);
;             }
	global_store_dwordx4 v[64:65], v[48:51], off offset:256
	s_nop 1
	v_add_u32_e32 v48, 0x90, v140
	v_fmamk_f32 v49, v151, 0x3a000000, v148
	v_rsq_f32_e32 v50, v49
	v_ashrrev_i32_e32 v49, 31, v48
	v_lshlrev_b64 v[48:49], 10, v[48:49]
	v_lshl_add_u64 v[48:49], s[4:5], 0, v[48:49]
	v_lshl_add_u64 v[48:49], v[48:49], 0, s[16:17]
	v_lshl_add_u64 v[48:49], v[48:49], 0, s[0:1]
	v_lshl_add_u64 v[48:49], v[48:49], 0, v[142:143]
	v_pk_mul_f32 v[46:47], v[50:51], v[46:47] op_sel_hi:[0,1]
	v_pk_mul_f32 v[44:45], v[50:51], v[44:45] op_sel_hi:[0,1]
	v_pk_mul_f32 v[52:53], v[50:51], v[42:43] op_sel_hi:[0,1]
	v_pk_mul_f32 v[42:43], v[50:51], v[40:41] op_sel_hi:[0,1]
	v_cvt_pk_bf16_f32 v40, v44, v45
	v_cvt_pk_bf16_f32 v41, v46, v47
	v_cvt_pk_bf16_f32 v42, v42, v43
	v_cvt_pk_bf16_f32 v43, v52, v53
	global_store_dwordx4 v[48:49], v[40:43], off
	v_pk_mul_f32 v[38:39], v[50:51], v[38:39] op_sel_hi:[0,1]
	v_pk_mul_f32 v[36:37], v[50:51], v[36:37] op_sel_hi:[0,1]
	v_pk_mul_f32 v[40:41], v[50:51], v[34:35] op_sel_hi:[0,1]
	v_pk_mul_f32 v[34:35], v[50:51], v[32:33] op_sel_hi:[0,1]
	v_cvt_pk_bf16_f32 v32, v36, v37
	v_cvt_pk_bf16_f32 v33, v38, v39
	v_cvt_pk_bf16_f32 v34, v34, v35
	v_cvt_pk_bf16_f32 v35, v40, v41
	global_store_dwordx4 v[48:49], v[32:35], off offset:256
	s_nop 1
	v_add_u32_e32 v32, 0xa0, v140
	v_fmamk_f32 v33, v150, 0x3a000000, v148
	v_rsq_f32_e32 v34, v33
	v_ashrrev_i32_e32 v33, 31, v32
	v_lshlrev_b64 v[32:33], 10, v[32:33]
	v_lshl_add_u64 v[32:33], s[4:5], 0, v[32:33]
	v_lshl_add_u64 v[32:33], v[32:33], 0, s[16:17]
	v_lshl_add_u64 v[32:33], v[32:33], 0, s[0:1]
	v_lshl_add_u64 v[32:33], v[32:33], 0, v[142:143]
	v_pk_mul_f32 v[30:31], v[34:35], v[30:31] op_sel_hi:[0,1]
	v_pk_mul_f32 v[28:29], v[34:35], v[28:29] op_sel_hi:[0,1]
	v_pk_mul_f32 v[36:37], v[34:35], v[26:27] op_sel_hi:[0,1]
	v_pk_mul_f32 v[26:27], v[34:35], v[24:25] op_sel_hi:[0,1]
	v_cvt_pk_bf16_f32 v24, v28, v29
	v_cvt_pk_bf16_f32 v25, v30, v31
	v_cvt_pk_bf16_f32 v26, v26, v27
	v_cvt_pk_bf16_f32 v27, v36, v37
	global_store_dwordx4 v[32:33], v[24:27], off
	v_pk_mul_f32 v[22:23], v[34:35], v[22:23] op_sel_hi:[0,1]
	v_pk_mul_f32 v[20:21], v[34:35], v[20:21] op_sel_hi:[0,1]
	v_pk_mul_f32 v[24:25], v[34:35], v[18:19] op_sel_hi:[0,1]
	v_pk_mul_f32 v[18:19], v[34:35], v[16:17] op_sel_hi:[0,1]
	v_cvt_pk_bf16_f32 v16, v20, v21
	v_cvt_pk_bf16_f32 v17, v22, v23
	v_cvt_pk_bf16_f32 v18, v18, v19
	v_cvt_pk_bf16_f32 v19, v24, v25
	global_store_dwordx4 v[32:33], v[16:19], off offset:256
	s_nop 1
	v_add_u32_e32 v16, 0xb0, v140
	v_fmamk_f32 v17, v149, 0x3a000000, v148
	v_rsq_f32_e32 v18, v17
	v_ashrrev_i32_e32 v17, 31, v16
	v_lshlrev_b64 v[16:17], 10, v[16:17]
	v_lshl_add_u64 v[16:17], s[4:5], 0, v[16:17]
	v_lshl_add_u64 v[16:17], v[16:17], 0, s[16:17]
	v_lshl_add_u64 v[16:17], v[16:17], 0, s[0:1]
	v_lshl_add_u64 v[16:17], v[16:17], 0, v[142:143]
	v_pk_mul_f32 v[14:15], v[18:19], v[14:15] op_sel_hi:[0,1]
	v_pk_mul_f32 v[12:13], v[18:19], v[12:13] op_sel_hi:[0,1]
	v_pk_mul_f32 v[20:21], v[18:19], v[10:11] op_sel_hi:[0,1]
	v_pk_mul_f32 v[10:11], v[18:19], v[8:9] op_sel_hi:[0,1]
	v_cvt_pk_bf16_f32 v8, v12, v13
	v_cvt_pk_bf16_f32 v9, v14, v15
	v_cvt_pk_bf16_f32 v10, v10, v11
	v_cvt_pk_bf16_f32 v11, v20, v21
	global_store_dwordx4 v[16:17], v[8:11], off
	s_mov_b64 s[16:17], s[12:13]
	v_pk_mul_f32 v[6:7], v[18:19], v[6:7] op_sel_hi:[0,1]
	v_pk_mul_f32 v[8:9], v[18:19], v[2:3] op_sel_hi:[0,1]
	v_pk_mul_f32 v[2:3], v[18:19], v[0:1] op_sel_hi:[0,1]
	v_pk_mul_f32 v[4:5], v[18:19], v[4:5] op_sel_hi:[0,1]
	v_cvt_pk_bf16_f32 v0, v4, v5
	v_cvt_pk_bf16_f32 v1, v6, v7
	v_cvt_pk_bf16_f32 v2, v2, v3
	v_cvt_pk_bf16_f32 v3, v8, v9
	global_store_dwordx4 v[16:17], v[0:3], off offset:256
	s_cbranch_vccz .LBB0_2161
	s_waitcnt vmcnt(0)
	s_cmpk_gt_u32 s96, 0xff
	s_cbranch_scc1 .LBB0_2172
	s_barrier

.LBB0_2485:
	ds_read_b128 v[128:131], v179
	ds_read_b128 v[132:135], v179 offset:1024
	ds_read_b128 v[136:139], v179 offset:2048
	ds_read_b128 v[140:143], v179 offset:3072
	s_add_u32 s30, s28, 0xfffe0080
	s_addc_u32 s31, s29, -1
	s_cmp_eq_u32 s63, 4
	s_cselect_b32 s35, s13, s31
	s_cselect_b32 s34, s12, s30
	s_cselect_b32 s31, s15, s62
	s_cselect_b32 s30, s14, s11
	v_lshl_add_u64 v[176:177], s[28:29], 0, v[168:169]
	s_add_i32 m0, s17, 0xc000
	ds_read_b128 v[144:147], v180
	ds_read_b128 v[148:151], v180 offset:1024
	ds_read_b128 v[152:155], v180 offset:2048
	ds_read_b128 v[156:159], v180 offset:3072
	ds_read_b128 v[172:175], v180 offset:4096
	ds_read_b128 v[182:185], v180 offset:5120
	ds_read_b128 v[186:189], v180 offset:6144
	ds_read_b128 v[190:193], v180 offset:7168
	global_load_lds_dwordx4 v[176:177], off
	v_lshl_add_u64 v[176:177], s[28:29], 0, v[170:171]
	s_add_i32 m0, s17, 0xe000
	s_nop 0
	global_load_lds_dwordx4 v[176:177], off
	s_waitcnt lgkmcnt(8)
	s_barrier
	s_waitcnt lgkmcnt(0)
	s_nop 0
	s_waitcnt lgkmcnt(0)
	v_mfma_f32_16x16x32_bf16 v[124:127], v[128:131], v[144:147], v[124:127]
	v_mfma_f32_16x16x32_bf16 v[120:123], v[136:139], v[144:147], v[120:123]
	v_mfma_f32_16x16x32_bf16 v[112:115], v[128:131], v[152:155], v[112:115]
	v_mfma_f32_16x16x32_bf16 v[104:107], v[136:139], v[152:155], v[104:107]
	v_mfma_f32_16x16x32_bf16 v[96:99], v[128:131], v[172:175], v[96:99]
	v_mfma_f32_16x16x32_bf16 v[88:91], v[136:139], v[172:175], v[88:91]
	v_mfma_f32_16x16x32_bf16 v[80:83], v[128:131], v[186:189], v[80:83]
	v_mfma_f32_16x16x32_bf16 v[72:75], v[136:139], v[186:189], v[72:75]
	v_mfma_f32_16x16x32_bf16 v[124:127], v[132:135], v[148:151], v[124:127]
	v_mfma_f32_16x16x32_bf16 v[120:123], v[140:143], v[148:151], v[120:123]
	v_mfma_f32_16x16x32_bf16 v[112:115], v[132:135], v[156:159], v[112:115]
	v_mfma_f32_16x16x32_bf16 v[104:107], v[140:143], v[156:159], v[104:107]
	v_mfma_f32_16x16x32_bf16 v[96:99], v[132:135], v[182:185], v[96:99]
	v_mfma_f32_16x16x32_bf16 v[88:91], v[140:143], v[182:185], v[88:91]
	v_mfma_f32_16x16x32_bf16 v[80:83], v[132:135], v[190:193], v[80:83]
	v_mfma_f32_16x16x32_bf16 v[72:75], v[140:143], v[190:193], v[72:75]
	s_nop 0
	s_barrier
	s_add_i32 s64, s49, s39
	v_lshl_add_u64 v[176:177], s[30:31], 0, v[162:163]
	s_mov_b32 m0, s64
	ds_read_b128 v[194:197], v181
	ds_read_b128 v[198:201], v181 offset:1024
	ds_read_b128 v[202:205], v181 offset:2048
	ds_read_b128 v[206:209], v181 offset:3072
	global_load_lds_dwordx4 v[176:177], off
	v_lshl_add_u64 v[210:211], s[30:31], 0, v[166:167]
	s_add_i32 m0, s64, 0x2000
	s_nop 0
	global_load_lds_dwordx4 v[210:211], off
	s_barrier
	s_waitcnt lgkmcnt(0)
	s_nop 0
	s_waitcnt lgkmcnt(0)
	v_mfma_f32_16x16x32_bf16 v[116:119], v[194:197], v[144:147], v[116:119]
	v_mfma_f32_16x16x32_bf16 v[108:111], v[202:205], v[144:147], v[108:111]
	v_mfma_f32_16x16x32_bf16 v[100:103], v[194:197], v[152:155], v[100:103]
	v_mfma_f32_16x16x32_bf16 v[92:95], v[202:205], v[152:155], v[92:95]
	v_mfma_f32_16x16x32_bf16 v[84:87], v[194:197], v[172:175], v[84:87]
	v_mfma_f32_16x16x32_bf16 v[76:79], v[202:205], v[172:175], v[76:79]
	v_mfma_f32_16x16x32_bf16 v[68:71], v[194:197], v[186:189], v[68:71]
	v_mfma_f32_16x16x32_bf16 v[64:67], v[202:205], v[186:189], v[64:67]
	v_mfma_f32_16x16x32_bf16 v[116:119], v[198:201], v[148:151], v[116:119]
	v_mfma_f32_16x16x32_bf16 v[108:111], v[206:209], v[148:151], v[108:111]
	v_mfma_f32_16x16x32_bf16 v[100:103], v[198:201], v[156:159], v[100:103]
	v_mfma_f32_16x16x32_bf16 v[92:95], v[206:209], v[156:159], v[92:95]
	v_mfma_f32_16x16x32_bf16 v[84:87], v[198:201], v[182:185], v[84:87]
	v_mfma_f32_16x16x32_bf16 v[76:79], v[206:209], v[182:185], v[76:79]
	v_mfma_f32_16x16x32_bf16 v[68:71], v[198:201], v[190:193], v[68:71]
	v_mfma_f32_16x16x32_bf16 v[64:67], v[206:209], v[190:193], v[64:67]
	s_nop 0
	s_mov_b32 m0, s17
	v_lshl_add_u64 v[212:213], s[34:35], 0, v[160:161]
	s_barrier
	ds_read_b128 v[144:147], v180 offset:16384
	ds_read_b128 v[148:151], v180 offset:17408
	ds_read_b128 v[152:155], v180 offset:18432
	ds_read_b128 v[156:159], v180 offset:19456
	ds_read_b128 v[172:175], v180 offset:20480
	ds_read_b128 v[182:185], v180 offset:21504
	ds_read_b128 v[186:189], v180 offset:22528
	ds_read_b128 v[190:193], v180 offset:23552
	global_load_lds_dwordx4 v[212:213], off
	v_lshl_add_u64 v[214:215], s[34:35], 0, v[164:165]
	s_mov_b32 m0, s40
	s_nop 0
	global_load_lds_dwordx4 v[214:215], off
	s_barrier
	s_waitcnt lgkmcnt(0)
	s_nop 0
	s_waitcnt lgkmcnt(0)
	v_mfma_f32_16x16x32_bf16 v[60:63], v[128:131], v[144:147], v[60:63]
	v_mfma_f32_16x16x32_bf16 v[56:59], v[136:139], v[144:147], v[56:59]
	v_mfma_f32_16x16x32_bf16 v[48:51], v[128:131], v[152:155], v[48:51]
	v_mfma_f32_16x16x32_bf16 v[40:43], v[136:139], v[152:155], v[40:43]
	v_mfma_f32_16x16x32_bf16 v[32:35], v[128:131], v[172:175], v[32:35]
	v_mfma_f32_16x16x32_bf16 v[24:27], v[136:139], v[172:175], v[24:27]
	v_mfma_f32_16x16x32_bf16 v[16:19], v[128:131], v[186:189], v[16:19]
	v_mfma_f32_16x16x32_bf16 v[8:11], v[136:139], v[186:189], v[8:11]
	v_mfma_f32_16x16x32_bf16 v[60:63], v[132:135], v[148:151], v[60:63]
	v_mfma_f32_16x16x32_bf16 v[56:59], v[140:143], v[148:151], v[56:59]
	v_mfma_f32_16x16x32_bf16 v[48:51], v[132:135], v[156:159], v[48:51]
	v_mfma_f32_16x16x32_bf16 v[40:43], v[140:143], v[156:159], v[40:43]
	v_mfma_f32_16x16x32_bf16 v[32:35], v[132:135], v[182:185], v[32:35]
	v_mfma_f32_16x16x32_bf16 v[24:27], v[140:143], v[182:185], v[24:27]
	v_mfma_f32_16x16x32_bf16 v[16:19], v[132:135], v[190:193], v[16:19]
	v_mfma_f32_16x16x32_bf16 v[8:11], v[140:143], v[190:193], v[8:11]
	s_nop 0
	s_barrier
	s_add_u32 s64, s30, 0x20000
	s_addc_u32 s65, s31, 0
	s_add_i32 s66, s52, s39
	v_lshl_add_u64 v[128:129], s[64:65], 0, v[162:163]
	s_mov_b32 m0, s66
	s_nop 0
	global_load_lds_dwordx4 v[128:129], off
	v_lshl_add_u64 v[128:129], s[64:65], 0, v[166:167]
	s_add_i32 m0, s66, 0x2000
	s_nop 0
	global_load_lds_dwordx4 v[128:129], off
	s_waitcnt vmcnt(6)
	s_barrier
	s_nop 0
	v_mfma_f32_16x16x32_bf16 v[52:55], v[194:197], v[144:147], v[52:55]
	v_mfma_f32_16x16x32_bf16 v[44:47], v[202:205], v[144:147], v[44:47]
	v_mfma_f32_16x16x32_bf16 v[36:39], v[194:197], v[152:155], v[36:39]
	v_mfma_f32_16x16x32_bf16 v[28:31], v[202:205], v[152:155], v[28:31]
	v_mfma_f32_16x16x32_bf16 v[20:23], v[194:197], v[172:175], v[20:23]
	v_mfma_f32_16x16x32_bf16 v[12:15], v[202:205], v[172:175], v[12:15]
	v_mfma_f32_16x16x32_bf16 v[4:7], v[194:197], v[186:189], v[4:7]
	v_mfma_f32_16x16x32_bf16 v[0:3], v[202:205], v[186:189], v[0:3]
	v_mfma_f32_16x16x32_bf16 v[52:55], v[198:201], v[148:151], v[52:55]
	v_mfma_f32_16x16x32_bf16 v[44:47], v[206:209], v[148:151], v[44:47]
	v_mfma_f32_16x16x32_bf16 v[36:39], v[198:201], v[156:159], v[36:39]
	v_mfma_f32_16x16x32_bf16 v[28:31], v[206:209], v[156:159], v[28:31]
	v_mfma_f32_16x16x32_bf16 v[20:23], v[198:201], v[182:185], v[20:23]
	v_mfma_f32_16x16x32_bf16 v[12:15], v[206:209], v[182:185], v[12:15]
	v_mfma_f32_16x16x32_bf16 v[4:7], v[198:201], v[190:193], v[4:7]
	v_mfma_f32_16x16x32_bf16 v[0:3], v[206:209], v[190:193], v[0:3]
	s_nop 0
	s_add_i32 s64, 0, 0x18000
	v_add_u32_e32 v140, s64, v178
	s_barrier
	ds_read_b128 v[128:131], v140
	ds_read_b128 v[132:135], v140 offset:1024
	ds_read_b128 v[136:139], v140 offset:2048
	ds_read_b128 v[140:143], v140 offset:3072
	s_add_u32 s34, s34, 0x20000
	s_addc_u32 s35, s35, 0
	s_mov_b32 m0, s41
	v_lshl_add_u64 v[194:195], s[34:35], 0, v[160:161]
	ds_read_b128 v[144:147], v180 offset:32768
	ds_read_b128 v[148:151], v180 offset:33792
	ds_read_b128 v[152:155], v180 offset:34816
	ds_read_b128 v[156:159], v180 offset:35840
	ds_read_b128 v[172:175], v180 offset:36864
	ds_read_b128 v[182:185], v180 offset:37888
	ds_read_b128 v[186:189], v180 offset:38912
	ds_read_b128 v[190:193], v180 offset:39936
	global_load_lds_dwordx4 v[194:195], off
	v_lshl_add_u64 v[194:195], s[34:35], 0, v[164:165]
	s_mov_b32 m0, s42
	s_nop 0
	global_load_lds_dwordx4 v[194:195], off
	s_waitcnt lgkmcnt(8)
	s_barrier
	s_waitcnt lgkmcnt(0)
	s_nop 0
	s_waitcnt lgkmcnt(0)
	v_mfma_f32_16x16x32_bf16 v[124:127], v[128:131], v[144:147], v[124:127]
	v_mfma_f32_16x16x32_bf16 v[120:123], v[136:139], v[144:147], v[120:123]
	v_mfma_f32_16x16x32_bf16 v[112:115], v[128:131], v[152:155], v[112:115]
	v_mfma_f32_16x16x32_bf16 v[104:107], v[136:139], v[152:155], v[104:107]
	v_mfma_f32_16x16x32_bf16 v[96:99], v[128:131], v[172:175], v[96:99]
	v_mfma_f32_16x16x32_bf16 v[88:91], v[136:139], v[172:175], v[88:91]
	v_mfma_f32_16x16x32_bf16 v[80:83], v[128:131], v[186:189], v[80:83]
	v_mfma_f32_16x16x32_bf16 v[72:75], v[136:139], v[186:189], v[72:75]
	v_mfma_f32_16x16x32_bf16 v[124:127], v[132:135], v[148:151], v[124:127]
	v_mfma_f32_16x16x32_bf16 v[120:123], v[140:143], v[148:151], v[120:123]
	v_mfma_f32_16x16x32_bf16 v[112:115], v[132:135], v[156:159], v[112:115]
	v_mfma_f32_16x16x32_bf16 v[104:107], v[140:143], v[156:159], v[104:107]
	v_mfma_f32_16x16x32_bf16 v[96:99], v[132:135], v[182:185], v[96:99]
	v_mfma_f32_16x16x32_bf16 v[88:91], v[140:143], v[182:185], v[88:91]
	v_mfma_f32_16x16x32_bf16 v[80:83], v[132:135], v[190:193], v[80:83]
	v_mfma_f32_16x16x32_bf16 v[72:75], v[140:143], v[190:193], v[72:75]
	s_nop 0
	s_barrier
	s_add_i32 s34, 0, 0x1c000
	s_add_i32 s35, s64, s39
	v_add_u32_e32 v206, s34, v178
	v_lshl_add_u64 v[176:177], v[176:177], 0, s[6:7]
	s_mov_b32 m0, s35
	ds_read_b128 v[194:197], v206
	ds_read_b128 v[198:201], v206 offset:1024
	ds_read_b128 v[202:205], v206 offset:2048
	ds_read_b128 v[206:209], v206 offset:3072
	global_load_lds_dwordx4 v[176:177], off
	v_lshl_add_u64 v[176:177], v[210:211], 0, s[6:7]
	s_add_i32 m0, s35, 0x2000
	s_nop 0
	global_load_lds_dwordx4 v[176:177], off
	s_barrier
	s_waitcnt lgkmcnt(0)
	s_nop 0
	s_waitcnt lgkmcnt(0)
	v_mfma_f32_16x16x32_bf16 v[116:119], v[194:197], v[144:147], v[116:119]
	v_mfma_f32_16x16x32_bf16 v[108:111], v[202:205], v[144:147], v[108:111]
	v_mfma_f32_16x16x32_bf16 v[100:103], v[194:197], v[152:155], v[100:103]
	v_mfma_f32_16x16x32_bf16 v[92:95], v[202:205], v[152:155], v[92:95]
	v_mfma_f32_16x16x32_bf16 v[84:87], v[194:197], v[172:175], v[84:87]
	v_mfma_f32_16x16x32_bf16 v[76:79], v[202:205], v[172:175], v[76:79]
	v_mfma_f32_16x16x32_bf16 v[68:71], v[194:197], v[186:189], v[68:71]
	v_mfma_f32_16x16x32_bf16 v[64:67], v[202:205], v[186:189], v[64:67]
	v_mfma_f32_16x16x32_bf16 v[116:119], v[198:201], v[148:151], v[116:119]
	v_mfma_f32_16x16x32_bf16 v[108:111], v[206:209], v[148:151], v[108:111]
	v_mfma_f32_16x16x32_bf16 v[100:103], v[198:201], v[156:159], v[100:103]
	v_mfma_f32_16x16x32_bf16 v[92:95], v[206:209], v[156:159], v[92:95]
	v_mfma_f32_16x16x32_bf16 v[84:87], v[198:201], v[182:185], v[84:87]
	v_mfma_f32_16x16x32_bf16 v[76:79], v[206:209], v[182:185], v[76:79]
	v_mfma_f32_16x16x32_bf16 v[68:71], v[198:201], v[190:193], v[68:71]
	v_mfma_f32_16x16x32_bf16 v[64:67], v[206:209], v[190:193], v[64:67]
	s_nop 0
	s_mov_b32 m0, s45
	v_lshl_add_u64 v[176:177], v[212:213], 0, s[6:7]
	s_barrier
	ds_read_b128 v[144:147], v180 offset:49152
	ds_read_b128 v[148:151], v180 offset:50176
	ds_read_b128 v[152:155], v180 offset:51200
	ds_read_b128 v[156:159], v180 offset:52224
	ds_read_b128 v[172:175], v180 offset:53248
	ds_read_b128 v[182:185], v180 offset:54272
	ds_read_b128 v[186:189], v180 offset:55296
	ds_read_b128 v[190:193], v180 offset:56320
	global_load_lds_dwordx4 v[176:177], off
	v_lshl_add_u64 v[176:177], v[214:215], 0, s[6:7]
	s_mov_b32 m0, s48
	s_nop 0
	global_load_lds_dwordx4 v[176:177], off
	s_barrier
;     __device__ __forceinline__ void operator()(const f32x4 (&acc)[2][2][4][2], const Unit& u, int wr, int wc, int fr, int fq, const Pre&) const {
;         const size_t off0 = (size_t)(u.pm * 256 + wr * 64 + fr) * DM + u.pn * 256 + 32 * wc + 8 * fq;
;         u32x4 rb[2][4][2];
;         if (!RF32) {
; #pragma unroll
;             for (int ai = 0; ai < 2; ++ai)
; #pragma unroll
;                 for (int m = 0; m < 4; ++m)
; #pragma unroll
;                     for (int bj = 0; bj < 2; ++bj) rb[ai][m][bj] = *(const u32x4*)((const bf16_t*)resid + off0 + (size_t)(ai * 128 + m * 16) * DM + 128 * bj);
;         }
	s_waitcnt lgkmcnt(0)
	s_nop 0
	s_waitcnt lgkmcnt(0)
	v_mfma_f32_16x16x32_bf16 v[60:63], v[128:131], v[144:147], v[60:63]
	v_mfma_f32_16x16x32_bf16 v[56:59], v[136:139], v[144:147], v[56:59]
	v_mfma_f32_16x16x32_bf16 v[48:51], v[128:131], v[152:155], v[48:51]
	v_mfma_f32_16x16x32_bf16 v[40:43], v[136:139], v[152:155], v[40:43]
	v_mfma_f32_16x16x32_bf16 v[32:35], v[128:131], v[172:175], v[32:35]
	v_mfma_f32_16x16x32_bf16 v[24:27], v[136:139], v[172:175], v[24:27]
	v_mfma_f32_16x16x32_bf16 v[16:19], v[128:131], v[186:189], v[16:19]
	v_mfma_f32_16x16x32_bf16 v[8:11], v[136:139], v[186:189], v[8:11]
	v_mfma_f32_16x16x32_bf16 v[60:63], v[132:135], v[148:151], v[60:63]
	v_mfma_f32_16x16x32_bf16 v[56:59], v[140:143], v[148:151], v[56:59]
	v_mfma_f32_16x16x32_bf16 v[48:51], v[132:135], v[156:159], v[48:51]
	v_mfma_f32_16x16x32_bf16 v[40:43], v[140:143], v[156:159], v[40:43]
	v_mfma_f32_16x16x32_bf16 v[32:35], v[132:135], v[182:185], v[32:35]
	v_mfma_f32_16x16x32_bf16 v[24:27], v[140:143], v[182:185], v[24:27]
	v_mfma_f32_16x16x32_bf16 v[16:19], v[132:135], v[190:193], v[16:19]
	v_mfma_f32_16x16x32_bf16 v[8:11], v[140:143], v[190:193], v[8:11]
	s_nop 0
	s_barrier
	s_add_u32 s30, s30, 0x20080
	s_addc_u32 s31, s31, 0
	s_add_i32 s34, s34, s39
	v_lshl_add_u64 v[128:129], s[30:31], 0, v[162:163]
	s_mov_b32 m0, s34
	s_nop 0
	global_load_lds_dwordx4 v[128:129], off
	v_lshl_add_u64 v[128:129], s[30:31], 0, v[166:167]
	s_add_i32 m0, s34, 0x2000
	s_nop 0
	global_load_lds_dwordx4 v[128:129], off
	s_waitcnt vmcnt(6)
	s_barrier
	s_nop 0
	v_mfma_f32_16x16x32_bf16 v[52:55], v[194:197], v[144:147], v[52:55]
	v_mfma_f32_16x16x32_bf16 v[44:47], v[202:205], v[144:147], v[44:47]
	v_mfma_f32_16x16x32_bf16 v[36:39], v[194:197], v[152:155], v[36:39]
	v_mfma_f32_16x16x32_bf16 v[28:31], v[202:205], v[152:155], v[28:31]
	v_mfma_f32_16x16x32_bf16 v[20:23], v[194:197], v[172:175], v[20:23]
	v_mfma_f32_16x16x32_bf16 v[12:15], v[202:205], v[172:175], v[12:15]
	v_mfma_f32_16x16x32_bf16 v[4:7], v[194:197], v[186:189], v[4:7]
	v_mfma_f32_16x16x32_bf16 v[0:3], v[202:205], v[186:189], v[0:3]
	v_mfma_f32_16x16x32_bf16 v[52:55], v[198:201], v[148:151], v[52:55]
	v_mfma_f32_16x16x32_bf16 v[44:47], v[206:209], v[148:151], v[44:47]
	v_mfma_f32_16x16x32_bf16 v[36:39], v[198:201], v[156:159], v[36:39]
	v_mfma_f32_16x16x32_bf16 v[28:31], v[206:209], v[156:159], v[28:31]
	v_mfma_f32_16x16x32_bf16 v[20:23], v[198:201], v[182:185], v[20:23]
	v_mfma_f32_16x16x32_bf16 v[12:15], v[206:209], v[182:185], v[12:15]
	v_mfma_f32_16x16x32_bf16 v[4:7], v[198:201], v[190:193], v[4:7]
	v_mfma_f32_16x16x32_bf16 v[0:3], v[206:209], v[190:193], v[0:3]
	s_nop 0
	s_add_i32 s63, s63, 2
	s_add_u32 s28, s28, 0x100
	s_addc_u32 s29, s29, 0
	s_add_u32 s11, s11, 0x100
	s_addc_u32 s62, s62, 0
	s_cmp_gt_u32 s63, 5
	s_barrier
	s_cbranch_scc0 .LBB0_2485
	s_lshl_b32 s11, s16, 8
	v_mbcnt_lo_u32_b32 v130, -1, 0
	v_mbcnt_hi_u32_b32 v130, -1, v130
	s_add_i32 s11, s11, s44
	v_and_or_b32 v128, v130, 15, s11
	s_lshl_b32 s28, s61, 8
	v_ashrrev_i32_e32 v130, 1, v130
	s_ashr_i32 s29, s28, 31
	v_and_b32_e32 v130, -8, v130
	v_ashrrev_i32_e32 v129, 31, v128
	v_ashrrev_i32_e32 v131, 31, v130
	s_or_b64 s[28:29], s[28:29], s[0:1]
	v_lshlrev_b64 v[128:129], 11, v[128:129]
	v_lshl_add_u64 v[130:131], s[28:29], 0, v[130:131]
	v_lshl_add_u64 v[128:129], v[130:131], 0, v[128:129]
	v_lshlrev_b64 v[210:211], 1, v[128:129]
	v_lshl_add_u64 v[128:129], s[2:3], 0, v[210:211]
	v_add_co_u32_e32 v130, vcc, s43, v128
	global_load_dwordx4 v[172:175], v[128:129], off
	global_load_dwordx4 v[182:185], v[128:129], off offset:256
	v_addc_co_u32_e32 v131, vcc, 0, v129, vcc
	global_load_dwordx4 v[186:189], v[130:131], off
	global_load_dwordx4 v[190:193], v[130:131], off offset:256
	v_add_co_u32_e32 v130, vcc, s53, v128
	s_mov_b32 s16, s10
	s_nop 0
	v_addc_co_u32_e32 v131, vcc, 0, v129, vcc
	global_load_dwordx4 v[194:197], v[130:131], off
	global_load_dwordx4 v[198:201], v[130:131], off offset:256
	v_add_co_u32_e32 v130, vcc, s54, v128
	s_mov_b32 s61, s60
	s_nop 0
	v_addc_co_u32_e32 v131, vcc, 0, v129, vcc
	global_load_dwordx4 v[202:205], v[130:131], off
	global_load_dwordx4 v[206:209], v[130:131], off offset:256
	v_add_co_u32_e32 v130, vcc, s55, v128
	s_mov_b64 s[30:31], s[14:15]
	s_nop 0
	v_addc_co_u32_e32 v131, vcc, 0, v129, vcc
	v_add_co_u32_e32 v132, vcc, s56, v128
	s_mov_b64 s[28:29], s[12:13]
	s_nop 0
	v_addc_co_u32_e32 v133, vcc, 0, v129, vcc
	v_add_co_u32_e32 v134, vcc, s57, v128
	s_waitcnt vmcnt(0)
; __device__ __forceinline__ float bf_lo(unsigned w) { return __uint_as_float(w << 16); }
; __device__ __forceinline__ float bf_hi(unsigned w) { return __uint_as_float(w & 0xffff0000u); }
;     __device__ __forceinline__ void operator()(const f32x4 (&acc)[2][2][4][2], const Unit& u, int wr, int wc, int fr, int fq, const Pre&) const {
;     ...
; #pragma unroll
;         for (int ai = 0; ai < 2; ++ai) {
;             f32x4 r0[4][2], r1[4][2];
; #pragma unroll
;             for (int m = 0; m < 4; ++m)
; #pragma unroll
;                 for (int bj = 0; bj < 2; ++bj) {
;                     const size_t off = off0 + (size_t)(ai * 128 + m * 16) * DM + 128 * bj;
;                     if (RF32) { r0[m][bj] = *(const f32x4*)((const float*)resid + off); r1[m][bj] = *(const f32x4*)((const float*)resid + off + 4); }
;                     else { const u32x4 rbv = rb[ai][m][bj];
;                         r0[m][bj] = (f32x4){bf_lo(rbv.x), bf_hi(rbv.x), bf_lo(rbv.y), bf_hi(rbv.y)}; r1[m][bj] = (f32x4){bf_lo(rbv.z), bf_hi(rbv.z), bf_lo(rbv.w), bf_hi(rbv.w)}; }
;                 }
; #pragma unroll
;             for (int m = 0; m < 4; ++m) {
;                 const int row = u.pm * 256 + ai * 128 + wr * 64 + m * 16 + fr; float sq = 0.f;
; #pragma unroll
;                 for (int bj = 0; bj < 2; ++bj) {
;                     const size_t off = off0 + (size_t)(ai * 128 + m * 16) * DM + 128 * bj;
;                     const f32x4 v0 = acc[ai][bj][m][0] + r0[m][bj], v1 = acc[ai][bj][m][1] + r1[m][bj];
;                     st_bf16x8(hb + off, v0, v1);
;                     sq += v0[0] * v0[0] + v0[1] * v0[1] + v0[2] * v0[2] + v0[3] * v0[3] + v1[0] * v1[0] + v1[1] * v1[1] + v1[2] * v1[2] + v1[3] * v1[3];
;                 }
	v_lshlrev_b32_e32 v212, 16, v172
	v_addc_co_u32_e32 v135, vcc, 0, v129, vcc
	v_add_co_u32_e32 v128, vcc, s58, v128
	v_and_b32_e32 v213, 0xffff0000, v172
	s_nop 0
	v_addc_co_u32_e32 v129, vcc, 0, v129, vcc
	global_load_dwordx4 v[156:159], v[130:131], off
	global_load_dwordx4 v[152:155], v[130:131], off offset:256
	global_load_dwordx4 v[148:151], v[132:133], off
	global_load_dwordx4 v[144:147], v[132:133], off offset:256
	global_load_dwordx4 v[140:143], v[134:135], off
	global_load_dwordx4 v[136:139], v[134:135], off offset:256
	s_nop 0
	global_load_dwordx4 v[132:135], v[128:129], off
	s_nop 0
	global_load_dwordx4 v[128:131], v[128:129], off offset:256
	v_lshlrev_b32_e32 v214, 16, v173
	v_and_b32_e32 v215, 0xffff0000, v173
	v_lshlrev_b32_e32 v216, 16, v174
	v_and_b32_e32 v217, 0xffff0000, v174
	v_lshlrev_b32_e32 v218, 16, v175
	v_and_b32_e32 v219, 0xffff0000, v175
	v_lshlrev_b32_e32 v220, 16, v182
	v_and_b32_e32 v221, 0xffff0000, v182
	v_lshlrev_b32_e32 v182, 16, v183
	v_and_b32_e32 v183, 0xffff0000, v183
	v_lshlrev_b32_e32 v222, 16, v184
	v_and_b32_e32 v223, 0xffff0000, v184
	v_lshlrev_b32_e32 v184, 16, v185
	v_and_b32_e32 v185, 0xffff0000, v185
	v_lshlrev_b32_e32 v172, 16, v208
	v_and_b32_e32 v173, 0xffff0000, v208
	v_lshlrev_b32_e32 v176, 16, v209
	v_and_b32_e32 v177, 0xffff0000, v209
	v_pk_add_f32 v[126:127], v[126:127], v[214:215]
	v_pk_add_f32 v[124:125], v[124:125], v[212:213]
	v_pk_add_f32 v[208:209], v[122:123], v[218:219]
	v_pk_add_f32 v[212:213], v[120:121], v[216:217]
	v_lshl_add_u64 v[120:121], s[4:5], 0, v[210:211]
	v_cvt_pk_bf16_f32 v122, v124, v125
	v_cvt_pk_bf16_f32 v123, v126, v127
	v_lshlrev_b32_e32 v224, 16, v186
	v_and_b32_e32 v225, 0xffff0000, v186
	v_lshlrev_b32_e32 v186, 16, v187
	v_and_b32_e32 v187, 0xffff0000, v187
	v_cvt_pk_bf16_f32 v124, v212, v213
	v_cvt_pk_bf16_f32 v125, v208, v209
	global_store_dwordx4 v[120:121], v[122:125], off
	v_pk_add_f32 v[118:119], v[118:119], v[182:183]
	v_pk_add_f32 v[116:117], v[116:117], v[220:221]
	v_pk_add_f32 v[122:123], v[110:111], v[184:185]
	v_pk_add_f32 v[110:111], v[108:109], v[222:223]
	v_cvt_pk_bf16_f32 v108, v116, v117
	v_cvt_pk_bf16_f32 v109, v118, v119
	v_lshlrev_b32_e32 v226, 16, v188
	v_and_b32_e32 v227, 0xffff0000, v188
	v_lshlrev_b32_e32 v188, 16, v189
	v_and_b32_e32 v189, 0xffff0000, v189
	v_cvt_pk_bf16_f32 v110, v110, v111
	v_cvt_pk_bf16_f32 v111, v122, v123
	global_store_dwordx4 v[120:121], v[108:111], off offset:256
	v_lshlrev_b32_e32 v228, 16, v190
	v_and_b32_e32 v229, 0xffff0000, v190
	v_pk_add_f32 v[108:109], v[114:115], v[186:187]
	v_pk_add_f32 v[110:111], v[112:113], v[224:225]
	v_pk_add_f32 v[112:113], v[106:107], v[188:189]
	v_pk_add_f32 v[106:107], v[104:105], v[226:227]
	v_cvt_pk_bf16_f32 v104, v110, v111
	v_cvt_pk_bf16_f32 v105, v108, v109
	v_add_co_u32_e32 v108, vcc, s43, v120
	v_lshlrev_b32_e32 v190, 16, v191
	v_and_b32_e32 v191, 0xffff0000, v191
	v_lshlrev_b32_e32 v230, 16, v192
	v_and_b32_e32 v231, 0xffff0000, v192
	v_lshlrev_b32_e32 v192, 16, v193
	v_and_b32_e32 v193, 0xffff0000, v193
	v_addc_co_u32_e32 v109, vcc, 0, v121, vcc
	v_lshlrev_b32_e32 v232, 16, v194
	v_and_b32_e32 v233, 0xffff0000, v194
	v_lshlrev_b32_e32 v194, 16, v195
	v_and_b32_e32 v195, 0xffff0000, v195
	v_cvt_pk_bf16_f32 v106, v106, v107
	v_cvt_pk_bf16_f32 v107, v112, v113
	global_store_dwordx4 v[108:109], v[104:107], off
	v_pk_add_f32 v[102:103], v[102:103], v[190:191]
	v_pk_add_f32 v[100:101], v[100:101], v[228:229]
	v_pk_add_f32 v[104:105], v[94:95], v[192:193]
	v_pk_add_f32 v[94:95], v[92:93], v[230:231]
	v_cvt_pk_bf16_f32 v92, v100, v101
	v_cvt_pk_bf16_f32 v93, v102, v103
	v_lshlrev_b32_e32 v234, 16, v196
	v_and_b32_e32 v235, 0xffff0000, v196
	v_lshlrev_b32_e32 v196, 16, v197
	v_and_b32_e32 v197, 0xffff0000, v197
	v_cvt_pk_bf16_f32 v94, v94, v95
	v_cvt_pk_bf16_f32 v95, v104, v105
	global_store_dwordx4 v[108:109], v[92:95], off offset:256
	v_lshlrev_b32_e32 v236, 16, v198
	v_and_b32_e32 v237, 0xffff0000, v198
	v_pk_add_f32 v[92:93], v[98:99], v[194:195]
	v_pk_add_f32 v[94:95], v[96:97], v[232:233]
	v_pk_add_f32 v[96:97], v[90:91], v[196:197]
	v_pk_add_f32 v[90:91], v[88:89], v[234:235]
	v_cvt_pk_bf16_f32 v88, v94, v95
	v_cvt_pk_bf16_f32 v89, v92, v93
	v_add_co_u32_e32 v92, vcc, s53, v120
	v_lshlrev_b32_e32 v198, 16, v199
	v_and_b32_e32 v199, 0xffff0000, v199
	v_lshlrev_b32_e32 v238, 16, v200
	v_and_b32_e32 v239, 0xffff0000, v200
	v_lshlrev_b32_e32 v200, 16, v201
	v_and_b32_e32 v201, 0xffff0000, v201
	v_addc_co_u32_e32 v93, vcc, 0, v121, vcc
	v_lshlrev_b32_e32 v240, 16, v202
	v_and_b32_e32 v241, 0xffff0000, v202
	v_lshlrev_b32_e32 v202, 16, v203
	v_and_b32_e32 v203, 0xffff0000, v203
	v_cvt_pk_bf16_f32 v90, v90, v91
	v_cvt_pk_bf16_f32 v91, v96, v97
	global_store_dwordx4 v[92:93], v[88:91], off
	v_pk_add_f32 v[86:87], v[86:87], v[198:199]
	v_pk_add_f32 v[84:85], v[84:85], v[236:237]
	v_pk_add_f32 v[88:89], v[78:79], v[200:201]
	v_pk_add_f32 v[78:79], v[76:77], v[238:239]
	v_cvt_pk_bf16_f32 v76, v84, v85
	v_cvt_pk_bf16_f32 v77, v86, v87
	v_lshlrev_b32_e32 v242, 16, v204
	v_and_b32_e32 v243, 0xffff0000, v204
	v_lshlrev_b32_e32 v204, 16, v205
	v_and_b32_e32 v205, 0xffff0000, v205
	v_cvt_pk_bf16_f32 v78, v78, v79
	v_cvt_pk_bf16_f32 v79, v88, v89
	global_store_dwordx4 v[92:93], v[76:79], off offset:256
	v_lshlrev_b32_e32 v174, 16, v206
	v_and_b32_e32 v175, 0xffff0000, v206
	v_pk_add_f32 v[76:77], v[82:83], v[202:203]
	v_pk_add_f32 v[78:79], v[80:81], v[240:241]
	v_pk_add_f32 v[80:81], v[74:75], v[204:205]
	v_pk_add_f32 v[74:75], v[72:73], v[242:243]
	v_cvt_pk_bf16_f32 v72, v78, v79
	v_cvt_pk_bf16_f32 v73, v76, v77
	v_add_co_u32_e32 v76, vcc, s54, v120
	v_lshlrev_b32_e32 v206, 16, v207
	s_nop 0
	v_addc_co_u32_e32 v77, vcc, 0, v121, vcc
	v_and_b32_e32 v207, 0xffff0000, v207
	v_cvt_pk_bf16_f32 v74, v74, v75
	v_cvt_pk_bf16_f32 v75, v80, v81
	global_store_dwordx4 v[76:77], v[72:75], off
	v_pk_add_f32 v[70:71], v[70:71], v[206:207]
	v_pk_add_f32 v[68:69], v[68:69], v[174:175]
	v_pk_add_f32 v[72:73], v[66:67], v[176:177]
	v_pk_add_f32 v[66:67], v[64:65], v[172:173]
	v_cvt_pk_bf16_f32 v64, v68, v69
	v_cvt_pk_bf16_f32 v65, v70, v71
	s_waitcnt vmcnt(0)
; __device__ __forceinline__ float bf_lo(unsigned w) { return __uint_as_float(w << 16); }
; __device__ __forceinline__ float bf_hi(unsigned w) { return __uint_as_float(w & 0xffff0000u); }
;     __device__ __forceinline__ void operator()(const f32x4 (&acc)[2][2][4][2], const Unit& u, int wr, int wc, int fr, int fq, const Pre&) const {
;     ...
; #pragma unroll
;         for (int ai = 0; ai < 2; ++ai) {
;             f32x4 r0[4][2], r1[4][2];
; #pragma unroll
;             for (int m = 0; m < 4; ++m)
; #pragma unroll
;                 for (int bj = 0; bj < 2; ++bj) {
;                     const size_t off = off0 + (size_t)(ai * 128 + m * 16) * DM + 128 * bj;
;                     if (RF32) { r0[m][bj] = *(const f32x4*)((const float*)resid + off); r1[m][bj] = *(const f32x4*)((const float*)resid + off + 4); }
;                     else { const u32x4 rbv = rb[ai][m][bj];
;                         r0[m][bj] = (f32x4){bf_lo(rbv.x), bf_hi(rbv.x), bf_lo(rbv.y), bf_hi(rbv.y)}; r1[m][bj] = (f32x4){bf_lo(rbv.z), bf_hi(rbv.z), bf_lo(rbv.w), bf_hi(rbv.w)}; }
;                 }
; #pragma unroll
;             for (int m = 0; m < 4; ++m) {
;                 const int row = u.pm * 256 + ai * 128 + wr * 64 + m * 16 + fr; float sq = 0.f;
; #pragma unroll
;                 for (int bj = 0; bj < 2; ++bj) {
;                     const size_t off = off0 + (size_t)(ai * 128 + m * 16) * DM + 128 * bj;
;                     const f32x4 v0 = acc[ai][bj][m][0] + r0[m][bj], v1 = acc[ai][bj][m][1] + r1[m][bj];
;                     st_bf16x8(hb + off, v0, v1);
;                     sq += v0[0] * v0[0] + v0[1] * v0[1] + v0[2] * v0[2] + v0[3] * v0[3] + v1[0] * v1[0] + v1[1] * v1[1] + v1[2] * v1[2] + v1[3] * v1[3];
;                 }
	v_lshlrev_b32_e32 v78, 16, v159
	v_cvt_pk_bf16_f32 v66, v66, v67
	v_cvt_pk_bf16_f32 v67, v72, v73
	v_lshlrev_b32_e32 v72, 16, v156
	v_and_b32_e32 v73, 0xffff0000, v156
	global_store_dwordx4 v[76:77], v[64:67], off offset:256
	v_lshlrev_b32_e32 v76, 16, v158
	v_and_b32_e32 v77, 0xffff0000, v158
	v_and_b32_e32 v79, 0xffff0000, v159
	v_pk_add_f32 v[60:61], v[60:61], v[72:73]
	v_lshlrev_b32_e32 v74, 16, v157
	v_and_b32_e32 v75, 0xffff0000, v157
	v_pk_add_f32 v[72:73], v[58:59], v[78:79]
	v_pk_add_f32 v[58:59], v[56:57], v[76:77]
	v_cvt_pk_bf16_f32 v56, v60, v61
	v_add_co_u32_e32 v60, vcc, s55, v120
	v_lshlrev_b32_e32 v80, 16, v152
	v_and_b32_e32 v81, 0xffff0000, v152
	v_lshlrev_b32_e32 v82, 16, v153
	v_and_b32_e32 v83, 0xffff0000, v153
	v_lshlrev_b32_e32 v84, 16, v154
	v_and_b32_e32 v85, 0xffff0000, v154
	v_lshlrev_b32_e32 v86, 16, v155
	v_and_b32_e32 v87, 0xffff0000, v155
	v_pk_add_f32 v[62:63], v[62:63], v[74:75]
	v_addc_co_u32_e32 v61, vcc, 0, v121, vcc
	v_cvt_pk_bf16_f32 v57, v62, v63
	v_lshlrev_b32_e32 v90, 16, v149
	v_and_b32_e32 v91, 0xffff0000, v149
	v_cvt_pk_bf16_f32 v58, v58, v59
	v_cvt_pk_bf16_f32 v59, v72, v73
	global_store_dwordx4 v[60:61], v[56:59], off
	v_pk_add_f32 v[54:55], v[54:55], v[82:83]
	v_pk_add_f32 v[52:53], v[52:53], v[80:81]
	v_pk_add_f32 v[56:57], v[46:47], v[86:87]
	v_pk_add_f32 v[46:47], v[44:45], v[84:85]
	v_cvt_pk_bf16_f32 v44, v52, v53
	v_cvt_pk_bf16_f32 v45, v54, v55
	v_lshlrev_b32_e32 v88, 16, v148
	v_and_b32_e32 v89, 0xffff0000, v148
	v_lshlrev_b32_e32 v92, 16, v150
	v_and_b32_e32 v93, 0xffff0000, v150
	v_lshlrev_b32_e32 v94, 16, v151
	v_and_b32_e32 v95, 0xffff0000, v151
	v_cvt_pk_bf16_f32 v46, v46, v47
	v_cvt_pk_bf16_f32 v47, v56, v57
	global_store_dwordx4 v[60:61], v[44:47], off offset:256
	v_lshlrev_b32_e32 v96, 16, v144
	v_and_b32_e32 v97, 0xffff0000, v144
	v_pk_add_f32 v[44:45], v[50:51], v[90:91]
	v_pk_add_f32 v[46:47], v[48:49], v[88:89]
	v_pk_add_f32 v[48:49], v[42:43], v[94:95]
	v_pk_add_f32 v[42:43], v[40:41], v[92:93]
	v_cvt_pk_bf16_f32 v40, v46, v47
	v_cvt_pk_bf16_f32 v41, v44, v45
	v_add_co_u32_e32 v44, vcc, s56, v120
	v_lshlrev_b32_e32 v98, 16, v145
	v_and_b32_e32 v99, 0xffff0000, v145
	v_lshlrev_b32_e32 v100, 16, v146
	v_and_b32_e32 v101, 0xffff0000, v146
	v_lshlrev_b32_e32 v102, 16, v147
	v_and_b32_e32 v103, 0xffff0000, v147
	v_addc_co_u32_e32 v45, vcc, 0, v121, vcc
	v_lshlrev_b32_e32 v106, 16, v141
	v_and_b32_e32 v107, 0xffff0000, v141
	v_cvt_pk_bf16_f32 v42, v42, v43
	v_cvt_pk_bf16_f32 v43, v48, v49
	global_store_dwordx4 v[44:45], v[40:43], off
	v_pk_add_f32 v[38:39], v[38:39], v[98:99]
	v_pk_add_f32 v[36:37], v[36:37], v[96:97]
	v_pk_add_f32 v[40:41], v[30:31], v[102:103]
	v_pk_add_f32 v[30:31], v[28:29], v[100:101]
	v_cvt_pk_bf16_f32 v28, v36, v37
	v_cvt_pk_bf16_f32 v29, v38, v39
	v_lshlrev_b32_e32 v104, 16, v140
	v_and_b32_e32 v105, 0xffff0000, v140
	v_lshlrev_b32_e32 v108, 16, v142
	v_and_b32_e32 v109, 0xffff0000, v142
	v_lshlrev_b32_e32 v110, 16, v143
	v_and_b32_e32 v111, 0xffff0000, v143
	v_cvt_pk_bf16_f32 v30, v30, v31
	v_cvt_pk_bf16_f32 v31, v40, v41
	global_store_dwordx4 v[44:45], v[28:31], off offset:256
	v_lshlrev_b32_e32 v112, 16, v136
	v_and_b32_e32 v113, 0xffff0000, v136
	v_pk_add_f32 v[28:29], v[34:35], v[106:107]
	v_pk_add_f32 v[30:31], v[32:33], v[104:105]
	v_pk_add_f32 v[32:33], v[26:27], v[110:111]
	v_pk_add_f32 v[26:27], v[24:25], v[108:109]
	v_cvt_pk_bf16_f32 v24, v30, v31
	v_cvt_pk_bf16_f32 v25, v28, v29
	v_add_co_u32_e32 v28, vcc, s57, v120
	v_lshlrev_b32_e32 v114, 16, v137
	v_and_b32_e32 v115, 0xffff0000, v137
	v_lshlrev_b32_e32 v116, 16, v138
	v_and_b32_e32 v117, 0xffff0000, v138
	v_lshlrev_b32_e32 v118, 16, v139
	v_and_b32_e32 v119, 0xffff0000, v139
	v_addc_co_u32_e32 v29, vcc, 0, v121, vcc
	v_lshlrev_b32_e32 v124, 16, v133
	v_and_b32_e32 v125, 0xffff0000, v133
	v_cvt_pk_bf16_f32 v26, v26, v27
	v_cvt_pk_bf16_f32 v27, v32, v33
	global_store_dwordx4 v[28:29], v[24:27], off
	v_pk_add_f32 v[22:23], v[22:23], v[114:115]
	v_pk_add_f32 v[20:21], v[20:21], v[112:113]
	v_pk_add_f32 v[24:25], v[14:15], v[118:119]
	v_pk_add_f32 v[14:15], v[12:13], v[116:117]
	v_cvt_pk_bf16_f32 v12, v20, v21
	v_cvt_pk_bf16_f32 v13, v22, v23
	v_lshlrev_b32_e32 v122, 16, v132
	v_and_b32_e32 v123, 0xffff0000, v132
	v_lshlrev_b32_e32 v126, 16, v134
	v_and_b32_e32 v127, 0xffff0000, v134
	v_lshlrev_b32_e32 v132, 16, v135
	v_and_b32_e32 v133, 0xffff0000, v135
	v_cvt_pk_bf16_f32 v14, v14, v15
	v_cvt_pk_bf16_f32 v15, v24, v25
	global_store_dwordx4 v[28:29], v[12:15], off offset:256
	v_lshlrev_b32_e32 v64, 16, v130
	v_and_b32_e32 v65, 0xffff0000, v130
	v_pk_add_f32 v[12:13], v[18:19], v[124:125]
	v_pk_add_f32 v[14:15], v[16:17], v[122:123]
	v_pk_add_f32 v[16:17], v[10:11], v[132:133]
	v_pk_add_f32 v[10:11], v[8:9], v[126:127]
	v_cvt_pk_bf16_f32 v8, v14, v15
	v_cvt_pk_bf16_f32 v9, v12, v13
	v_add_co_u32_e32 v12, vcc, s58, v120
	v_lshlrev_b32_e32 v68, 16, v131
	v_and_b32_e32 v69, 0xffff0000, v131
	v_addc_co_u32_e32 v13, vcc, 0, v121, vcc
	v_lshlrev_b32_e32 v66, 16, v128
	v_and_b32_e32 v67, 0xffff0000, v128
	v_lshlrev_b32_e32 v70, 16, v129
	v_and_b32_e32 v71, 0xffff0000, v129
	v_cvt_pk_bf16_f32 v10, v10, v11
	v_cvt_pk_bf16_f32 v11, v16, v17
	global_store_dwordx4 v[12:13], v[8:11], off
	s_and_b64 vcc, exec, s[8:9]
	v_pk_add_f32 v[6:7], v[6:7], v[70:71]
	v_pk_add_f32 v[8:9], v[2:3], v[68:69]
	v_pk_add_f32 v[2:3], v[0:1], v[64:65]
	v_pk_add_f32 v[4:5], v[4:5], v[66:67]
	s_nop 0
	v_cvt_pk_bf16_f32 v0, v4, v5
	v_cvt_pk_bf16_f32 v1, v6, v7
	v_cvt_pk_bf16_f32 v2, v2, v3
	v_cvt_pk_bf16_f32 v3, v8, v9
	global_store_dwordx4 v[12:13], v[0:3], off offset:256
	s_cbranch_vccz .LBB0_2478
	s_waitcnt vmcnt(0)
	s_cmpk_gt_u32 s96, 0xff
	s_cbranch_scc1 .LBB0_2489
	s_barrier

.LBB0_2704:
	s_add_u32 s0, s0, 0x40000
	s_addc_u32 s1, s1, 0
	s_mov_b32 m0, s67
	v_lshl_add_u64 v[48:49], s[0:1], 0, v[198:199]
	global_load_lds_dwordx4 v[48:49], off
	v_lshl_add_u64 v[48:49], s[0:1], 0, v[194:195]
	s_mov_b32 m0, s68
	s_nop 0
	global_load_lds_dwordx4 v[48:49], off
	s_waitcnt lgkmcnt(8)
	s_barrier
	s_waitcnt lgkmcnt(0)
	s_nop 0
	s_waitcnt lgkmcnt(0)
	v_mfma_f32_16x16x128_f8f6f4 v[188:191], v[8:15], v[40:47], v[188:191]
	v_mfma_f32_16x16x128_f8f6f4 v[184:187], v[0:7], v[40:47], v[184:187]
	v_mfma_f32_16x16x128_f8f6f4 v[172:175], v[8:15], v[32:39], v[172:175]
	v_mfma_f32_16x16x128_f8f6f4 v[164:167], v[0:7], v[32:39], v[164:167]
	v_mfma_f32_16x16x128_f8f6f4 v[156:159], v[8:15], v[24:31], v[156:159]
	v_mfma_f32_16x16x128_f8f6f4 v[148:151], v[0:7], v[24:31], v[148:151]
	v_mfma_f32_16x16x128_f8f6f4 v[140:143], v[8:15], v[16:23], v[140:143]
	v_mfma_f32_16x16x128_f8f6f4 v[132:135], v[0:7], v[16:23], v[132:135]
	s_nop 0
	s_barrier
	s_add_i32 s0, 0, 0x1c000
	s_mov_b32 m0, s77
	v_add_u32_e32 v60, s0, v244
	v_lshl_add_u64 v[234:235], v[234:235], 0, s[14:15]
	ds_read_b128 v[48:51], v60
	ds_read_b128 v[52:55], v60 offset:1024
	ds_read_b128 v[56:59], v60 offset:2048
	ds_read_b128 v[60:63], v60 offset:3072
	global_load_lds_dwordx4 v[234:235], off
	v_lshl_add_u64 v[234:235], v[236:237], 0, s[14:15]
	s_mov_b32 m0, s78
	s_nop 0
	global_load_lds_dwordx4 v[234:235], off
	s_barrier
	s_waitcnt lgkmcnt(0)
	s_nop 0
	s_waitcnt lgkmcnt(0)
	v_mfma_f32_16x16x128_f8f6f4 v[180:183], v[48:55], v[40:47], v[180:183]
	v_mfma_f32_16x16x128_f8f6f4 v[176:179], v[56:63], v[40:47], v[176:179]
	v_mfma_f32_16x16x128_f8f6f4 v[168:171], v[48:55], v[32:39], v[168:171]
	v_mfma_f32_16x16x128_f8f6f4 v[160:163], v[56:63], v[32:39], v[160:163]
	v_mfma_f32_16x16x128_f8f6f4 v[152:155], v[48:55], v[24:31], v[152:155]
	v_mfma_f32_16x16x128_f8f6f4 v[144:147], v[56:63], v[24:31], v[144:147]
	v_mfma_f32_16x16x128_f8f6f4 v[136:139], v[48:55], v[16:23], v[136:139]
	v_mfma_f32_16x16x128_f8f6f4 v[128:131], v[56:63], v[16:23], v[128:131]
	s_nop 0
	s_mov_b32 m0, s79
	v_lshl_add_u64 v[234:235], v[238:239], 0, s[14:15]
	s_barrier
	ds_read_b128 v[16:19], v246 offset:49152
	ds_read_b128 v[20:23], v246 offset:50176
	ds_read_b128 v[24:27], v246 offset:51200
	ds_read_b128 v[28:31], v246 offset:52224
	ds_read_b128 v[32:35], v246 offset:53248
	ds_read_b128 v[36:39], v246 offset:54272
	ds_read_b128 v[40:43], v246 offset:55296
	ds_read_b128 v[44:47], v246 offset:56320
	global_load_lds_dwordx4 v[234:235], off
	v_lshl_add_u64 v[234:235], v[240:241], 0, s[14:15]
	s_mov_b32 m0, s80
	s_nop 0
	global_load_lds_dwordx4 v[234:235], off
	s_barrier
	s_waitcnt lgkmcnt(0)
	s_nop 0
	s_waitcnt lgkmcnt(0)
	v_mfma_f32_16x16x128_f8f6f4 v[116:119], v[8:15], v[16:23], v[116:119]
	v_mfma_f32_16x16x128_f8f6f4 v[108:111], v[0:7], v[16:23], v[108:111]
	v_mfma_f32_16x16x128_f8f6f4 v[100:103], v[8:15], v[24:31], v[100:103]
	v_mfma_f32_16x16x128_f8f6f4 v[92:95], v[0:7], v[24:31], v[92:95]
	v_mfma_f32_16x16x128_f8f6f4 v[84:87], v[8:15], v[32:39], v[84:87]
	v_mfma_f32_16x16x128_f8f6f4 v[76:79], v[0:7], v[32:39], v[76:79]
	v_mfma_f32_16x16x128_f8f6f4 v[68:71], v[8:15], v[40:47], v[68:71]
	v_mfma_f32_16x16x128_f8f6f4 v[64:67], v[0:7], v[40:47], v[64:67]
	s_nop 0
	s_barrier
	v_lshl_add_u64 v[0:1], v[232:233], 0, s[16:17]
	s_add_i32 s0, s0, s61
	v_lshl_add_u64 v[2:3], v[0:1], 0, v[196:197]
	s_mov_b32 m0, s0
	v_lshl_add_u64 v[0:1], v[0:1], 0, v[192:193]
	global_load_lds_dwordx4 v[2:3], off
	s_add_i32 m0, s0, 0x2000
	s_nop 0
	global_load_lds_dwordx4 v[0:1], off
	s_waitcnt vmcnt(6)
	s_barrier
	s_nop 0
	v_mfma_f32_16x16x128_f8f6f4 v[124:127], v[48:55], v[16:23], v[124:127]
	v_mfma_f32_16x16x128_f8f6f4 v[120:123], v[56:63], v[16:23], v[120:123]
	v_mfma_f32_16x16x128_f8f6f4 v[112:115], v[48:55], v[24:31], v[112:115]
	v_mfma_f32_16x16x128_f8f6f4 v[104:107], v[56:63], v[24:31], v[104:107]
	v_mfma_f32_16x16x128_f8f6f4 v[96:99], v[48:55], v[32:39], v[96:99]
	v_mfma_f32_16x16x128_f8f6f4 v[88:91], v[56:63], v[32:39], v[88:91]
	v_mfma_f32_16x16x128_f8f6f4 v[80:83], v[48:55], v[40:47], v[80:83]
	v_mfma_f32_16x16x128_f8f6f4 v[72:75], v[56:63], v[40:47], v[72:75]
	s_nop 0
	s_add_i32 s39, s39, 2
	s_add_u32 s52, s52, 0x100
	s_addc_u32 s53, s53, 0
	s_cmp_gt_u32 s39, 13
	v_lshl_add_u64 v[230:231], v[230:231], 0, s[30:31]
	s_barrier
	s_cbranch_scc1 .LBB0_2717
.LBB0_2705:
	v_add_u32_e32 v225, 0, v244
	v_add_u32_e32 v12, 0x10000, v225
	ds_read_b128 v[0:3], v12
	ds_read_b128 v[4:7], v12 offset:1024
	ds_read_b128 v[8:11], v12 offset:2048
	ds_read_b128 v[12:15], v12 offset:3072
	s_xor_b64 s[54:55], s[46:47], -1
	v_lshl_add_u64 v[16:17], s[52:53], 0, v[210:211]
	s_add_i32 m0, s51, 0xc000
	ds_read_b128 v[56:59], v246
	ds_read_b128 v[60:63], v246 offset:1024
	ds_read_b128 v[48:51], v246 offset:2048
	ds_read_b128 v[52:55], v246 offset:3072
	ds_read_b128 v[40:43], v246 offset:4096
	ds_read_b128 v[44:47], v246 offset:5120
	ds_read_b128 v[32:35], v246 offset:6144
	ds_read_b128 v[36:39], v246 offset:7168
	global_load_lds_dwordx4 v[16:17], off
	v_lshl_add_u64 v[16:17], s[52:53], 0, v[212:213]
	s_add_i32 m0, s51, 0xe000
	s_nop 0
	global_load_lds_dwordx4 v[16:17], off
	s_waitcnt lgkmcnt(8)
	s_barrier
	s_waitcnt lgkmcnt(0)
	s_nop 0
	s_waitcnt lgkmcnt(0)
	v_mfma_f32_16x16x128_f8f6f4 v[188:191], v[0:7], v[56:63], v[188:191]
	v_mfma_f32_16x16x128_f8f6f4 v[184:187], v[8:15], v[56:63], v[184:187]
	v_mfma_f32_16x16x128_f8f6f4 v[172:175], v[0:7], v[48:55], v[172:175]
	v_mfma_f32_16x16x128_f8f6f4 v[164:167], v[8:15], v[48:55], v[164:167]
	v_mfma_f32_16x16x128_f8f6f4 v[156:159], v[0:7], v[40:47], v[156:159]
	v_mfma_f32_16x16x128_f8f6f4 v[148:151], v[8:15], v[40:47], v[148:151]
	v_mfma_f32_16x16x128_f8f6f4 v[140:143], v[0:7], v[32:39], v[140:143]
	v_mfma_f32_16x16x128_f8f6f4 v[132:135], v[8:15], v[32:39], v[132:135]
	s_nop 0
	s_barrier
	v_add_u32_e32 v20, 0x14000, v225
	ds_read_b128 v[24:27], v20
	ds_read_b128 v[28:31], v20 offset:1024
	ds_read_b128 v[16:19], v20 offset:2048
	ds_read_b128 v[20:23], v20 offset:3072
	s_and_b64 vcc, exec, s[54:55]
	s_cbranch_vccnz .LBB0_2707
	v_add_u32_e32 v220, v243, v242
	ds_read2_b32 v[214:215], v220 offset1:32
	ds_read2_b32 v[216:217], v220 offset0:64 offset1:96
	ds_read2_b32 v[218:219], v220 offset0:128 offset1:160
	ds_read2_b32 v[220:221], v220 offset0:192 offset1:224

.LBB0_2709:
	s_nop 0
	s_waitcnt lgkmcnt(0)
	v_mfma_f32_16x16x128_f8f6f4 v[180:183], v[24:31], v[56:63], v[180:183]
	v_mfma_f32_16x16x128_f8f6f4 v[176:179], v[16:23], v[56:63], v[176:179]
	v_mfma_f32_16x16x128_f8f6f4 v[168:171], v[24:31], v[48:55], v[168:171]
	v_mfma_f32_16x16x128_f8f6f4 v[160:163], v[16:23], v[48:55], v[160:163]
	v_mfma_f32_16x16x128_f8f6f4 v[152:155], v[24:31], v[40:47], v[152:155]
	v_mfma_f32_16x16x128_f8f6f4 v[144:147], v[16:23], v[40:47], v[144:147]
	v_mfma_f32_16x16x128_f8f6f4 v[136:139], v[24:31], v[32:39], v[136:139]
	v_mfma_f32_16x16x128_f8f6f4 v[128:131], v[16:23], v[32:39], v[128:131]
	s_nop 0
	s_barrier
	ds_read_b128 v[56:59], v246 offset:16384
	ds_read_b128 v[60:63], v246 offset:17408
	ds_read_b128 v[48:51], v246 offset:18432
	ds_read_b128 v[52:55], v246 offset:19456
	ds_read_b128 v[40:43], v246 offset:20480
	ds_read_b128 v[44:47], v246 offset:21504
	ds_read_b128 v[32:35], v246 offset:22528
	ds_read_b128 v[36:39], v246 offset:23552
	s_and_b64 vcc, exec, s[2:3]
	s_cbranch_vccnz .LBB0_2711
	v_lshl_add_u64 v[238:239], v[206:207], 0, s[28:29]
	global_store_dwordx2 v[238:239], v[222:223], off
.LBB0_2711:
	s_add_u32 s2, s52, 0xfffc0080
	s_addc_u32 s3, s53, -1
	s_and_b64 s[0:1], s[0:1], exec
	s_cselect_b32 s1, s45, s3
	s_cselect_b32 s0, s44, s2
	s_mov_b32 m0, s51
	v_lshl_add_u64 v[238:239], s[0:1], 0, v[198:199]
	global_load_lds_dwordx4 v[238:239], off
	v_lshl_add_u64 v[240:241], s[0:1], 0, v[194:195]
	s_mov_b32 m0, s64
	s_nop 0
	global_load_lds_dwordx4 v[240:241], off
	s_barrier
	s_waitcnt lgkmcnt(0)
	s_nop 0
	s_waitcnt lgkmcnt(0)
	v_mfma_f32_16x16x128_f8f6f4 v[116:119], v[0:7], v[56:63], v[116:119]
	v_mfma_f32_16x16x128_f8f6f4 v[108:111], v[8:15], v[56:63], v[108:111]
	v_mfma_f32_16x16x128_f8f6f4 v[100:103], v[0:7], v[48:55], v[100:103]
	v_mfma_f32_16x16x128_f8f6f4 v[92:95], v[8:15], v[48:55], v[92:95]
	v_mfma_f32_16x16x128_f8f6f4 v[84:87], v[0:7], v[40:47], v[84:87]
	v_mfma_f32_16x16x128_f8f6f4 v[76:79], v[8:15], v[40:47], v[76:79]
	v_mfma_f32_16x16x128_f8f6f4 v[68:71], v[0:7], v[32:39], v[68:71]
	v_mfma_f32_16x16x128_f8f6f4 v[64:67], v[8:15], v[32:39], v[64:67]
	s_nop 0
	s_barrier
	v_lshl_add_u64 v[0:1], v[232:233], 0, s[8:9]
	s_mov_b32 m0, s65
	v_lshl_add_u64 v[2:3], v[0:1], 0, v[196:197]
	global_load_lds_dwordx4 v[2:3], off
	v_lshl_add_u64 v[0:1], v[0:1], 0, v[192:193]
	s_mov_b32 m0, s66
	s_mov_b64 s[2:3], -1
	global_load_lds_dwordx4 v[0:1], off
	s_and_b64 vcc, exec, s[54:55]
	s_cbranch_vccz .LBB0_2713
	s_waitcnt vmcnt(6)
	s_mov_b64 s[2:3], 0

;     __device__ __forceinline__ void decode(int j, size_t& soff, int& sld, size_t& doff) const {
;     ...
;         else { const int e = j >> 10, r = j & 1023, nt = r >> 4, kt = r & 15, n0 = nt * 32;
;             sld = 2048; soff = (size_t)e * 2048 * 2048 + (size_t)(kt * 128) * 2048 + n0; doff = (size_t)e * 2048 * 2048 + (size_t)n0 * 2048 + kt * 128; }
.LBB0_2715:
	s_barrier
	s_nop 0
	v_mfma_f32_16x16x128_f8f6f4 v[124:127], v[24:31], v[56:63], v[124:127]
	v_mfma_f32_16x16x128_f8f6f4 v[120:123], v[16:23], v[56:63], v[120:123]
	v_mfma_f32_16x16x128_f8f6f4 v[112:115], v[24:31], v[48:55], v[112:115]
	v_mfma_f32_16x16x128_f8f6f4 v[104:107], v[16:23], v[48:55], v[104:107]
	v_mfma_f32_16x16x128_f8f6f4 v[96:99], v[24:31], v[40:47], v[96:99]
	v_mfma_f32_16x16x128_f8f6f4 v[88:91], v[16:23], v[40:47], v[88:91]
	v_mfma_f32_16x16x128_f8f6f4 v[80:83], v[24:31], v[32:39], v[80:83]
	v_mfma_f32_16x16x128_f8f6f4 v[72:75], v[16:23], v[32:39], v[72:75]
	s_nop 0
	v_add_u32_e32 v4, 0x18000, v225
	s_barrier
	ds_read_b128 v[8:11], v4
	ds_read_b128 v[12:15], v4 offset:1024
	ds_read_b128 v[0:3], v4 offset:2048
	ds_read_b128 v[4:7], v4 offset:3072
	ds_read_b128 v[40:43], v246 offset:32768
	ds_read_b128 v[44:47], v246 offset:33792
	ds_read_b128 v[32:35], v246 offset:34816
	ds_read_b128 v[36:39], v246 offset:35840
	ds_read_b128 v[24:27], v246 offset:36864
	ds_read_b128 v[28:31], v246 offset:37888
	ds_read_b128 v[16:19], v246 offset:38912
	ds_read_b128 v[20:23], v246 offset:39936
	s_mul_i32 s2, s49, s19
	s_add_i32 s2, s2, s18
	s_cmp_lt_i32 s2, 0x8000
	s_cselect_b64 s[46:47], -1, 0
	s_cmpk_gt_i32 s2, 0x7fff
	s_cbranch_scc1 .LBB0_2704
	s_lshl_b32 s3, s2, 1
	s_ashr_i32 s54, s2, 10
	s_and_b32 s41, s3, 0x7e0
	s_ashr_i32 s55, s54, 31
	s_lshl_b64 s[28:29], s[54:55], 22
	s_lshl_b32 s2, s2, 7
	s_lshl_b32 s3, s41, 11
	s_and_b32 s2, s2, 0x780
	s_or_b32 s3, s28, s3
	s_or_b32 s28, s3, s2
	s_lshl_b32 s2, s2, 13
	s_add_u32 s87, s72, s2
	s_addc_u32 s88, s73, 0
	s_lshl_b64 s[2:3], s[54:55], 24
	s_add_u32 s2, s87, s2
	s_addc_u32 s3, s88, s3
	s_lshl_b32 s41, s41, 2
	s_add_u32 s2, s2, s41
	s_addc_u32 s3, s3, 0
	v_lshl_add_u64 v[48:49], s[2:3], 0, v[208:209]
	v_lshl_add_u64 v[48:49], v[48:49], 0, v[200:201]
	s_add_i32 m0, s83, 0x20000
	s_add_i32 s49, s49, 1
	global_load_lds_dwordx4 v[48:49], off nt
	v_lshl_add_u64 v[48:49], v[48:49], 0, s[34:35]
	s_mov_b32 m0, s84
	s_nop 0
	global_load_lds_dwordx4 v[48:49], off nt
	s_branch .LBB0_2704

.LBB0_2796:
	ds_read_b128 v[0:3], v175
	ds_read_b128 v[4:7], v175 offset:1024
	ds_read_b128 v[8:11], v175 offset:2048
	ds_read_b128 v[12:15], v175 offset:3072
	s_add_u32 s34, s30, 0xfffc0080
	s_addc_u32 s35, s31, -1
	s_cmp_eq_u32 s57, 12
	s_cselect_b32 s37, s15, s35
	s_cselect_b32 s36, s14, s34
	s_cselect_b32 s35, s17, s55
	s_cselect_b32 s34, s16, s13
	v_lshl_add_u64 v[16:17], s[30:31], 0, v[160:161]
	s_add_i32 m0, s29, 0xc000
	ds_read_b128 v[188:191], v176
	ds_read_b128 v[192:195], v176 offset:1024
	ds_read_b128 v[196:199], v176 offset:2048
	ds_read_b128 v[200:203], v176 offset:3072
	ds_read_b128 v[204:207], v176 offset:4096
	ds_read_b128 v[208:211], v176 offset:5120
	ds_read_b128 v[212:215], v176 offset:6144
	ds_read_b128 v[216:219], v176 offset:7168
	global_load_lds_dwordx4 v[16:17], off
	v_lshl_add_u64 v[16:17], s[30:31], 0, v[162:163]
	s_add_i32 m0, s29, 0xe000
	s_nop 0
	global_load_lds_dwordx4 v[16:17], off
	s_waitcnt lgkmcnt(8)
	s_barrier
	s_waitcnt lgkmcnt(0)
	s_nop 0
	s_waitcnt lgkmcnt(0)
	v_mfma_f32_16x16x128_f8f6f4 v[148:151], v[0:7], v[188:195], v[148:151]
	v_mfma_f32_16x16x128_f8f6f4 v[144:147], v[8:15], v[188:195], v[144:147]
	v_mfma_f32_16x16x128_f8f6f4 v[140:143], v[0:7], v[196:203], v[140:143]
	v_mfma_f32_16x16x128_f8f6f4 v[136:139], v[8:15], v[196:203], v[136:139]
	v_mfma_f32_16x16x128_f8f6f4 v[132:135], v[0:7], v[204:211], v[132:135]
	v_mfma_f32_16x16x128_f8f6f4 v[120:123], v[8:15], v[204:211], v[120:123]
	v_mfma_f32_16x16x128_f8f6f4 v[100:103], v[0:7], v[212:219], v[100:103]
	v_mfma_f32_16x16x128_f8f6f4 v[96:99], v[8:15], v[212:219], v[96:99]
	s_nop 0
	s_barrier
	s_add_i32 s58, s53, s43
	v_lshl_add_u64 v[166:167], s[34:35], 0, v[156:157]
	s_mov_b32 m0, s58
	ds_read_b128 v[16:19], v178
	ds_read_b128 v[20:23], v178 offset:1024
	ds_read_b128 v[220:223], v178 offset:2048
	ds_read_b128 v[224:227], v178 offset:3072
	global_load_lds_dwordx4 v[166:167], off
	v_lshl_add_u64 v[168:169], s[34:35], 0, v[152:153]
	s_add_i32 m0, s58, 0x2000
	s_nop 0
	global_load_lds_dwordx4 v[168:169], off
	s_barrier
	s_waitcnt lgkmcnt(0)
	s_nop 0
	s_waitcnt lgkmcnt(0)
	v_mfma_f32_16x16x128_f8f6f4 v[128:131], v[16:23], v[188:195], v[128:131]
	v_mfma_f32_16x16x128_f8f6f4 v[124:127], v[220:227], v[188:195], v[124:127]
	v_mfma_f32_16x16x128_f8f6f4 v[116:119], v[16:23], v[196:203], v[116:119]
	v_mfma_f32_16x16x128_f8f6f4 v[112:115], v[220:227], v[196:203], v[112:115]
	v_mfma_f32_16x16x128_f8f6f4 v[108:111], v[16:23], v[204:211], v[108:111]
	v_mfma_f32_16x16x128_f8f6f4 v[104:107], v[220:227], v[204:211], v[104:107]
	v_mfma_f32_16x16x128_f8f6f4 v[92:95], v[16:23], v[212:219], v[92:95]
	v_mfma_f32_16x16x128_f8f6f4 v[88:91], v[220:227], v[212:219], v[88:91]
	s_nop 0
	s_mov_b32 m0, s29
	v_lshl_add_u64 v[170:171], s[36:37], 0, v[158:159]
	s_barrier
	ds_read_b128 v[188:191], v176 offset:16384
	ds_read_b128 v[192:195], v176 offset:17408
	ds_read_b128 v[196:199], v176 offset:18432
	ds_read_b128 v[200:203], v176 offset:19456
	ds_read_b128 v[204:207], v176 offset:20480
	ds_read_b128 v[208:211], v176 offset:21504
	ds_read_b128 v[212:215], v176 offset:22528
	ds_read_b128 v[216:219], v176 offset:23552
	global_load_lds_dwordx4 v[170:171], off
	v_lshl_add_u64 v[172:173], s[36:37], 0, v[154:155]
	s_mov_b32 m0, s45
	s_nop 0
	global_load_lds_dwordx4 v[172:173], off
	s_barrier
	s_waitcnt lgkmcnt(0)
	s_nop 0
	s_waitcnt lgkmcnt(0)
	v_mfma_f32_16x16x128_f8f6f4 v[84:87], v[0:7], v[188:195], v[84:87]
	v_mfma_f32_16x16x128_f8f6f4 v[80:83], v[8:15], v[188:195], v[80:83]
	v_mfma_f32_16x16x128_f8f6f4 v[68:71], v[0:7], v[196:203], v[68:71]
	v_mfma_f32_16x16x128_f8f6f4 v[64:67], v[8:15], v[196:203], v[64:67]
	v_mfma_f32_16x16x128_f8f6f4 v[52:55], v[0:7], v[204:211], v[52:55]
	v_mfma_f32_16x16x128_f8f6f4 v[48:51], v[8:15], v[204:211], v[48:51]
	v_mfma_f32_16x16x128_f8f6f4 v[36:39], v[0:7], v[212:219], v[36:39]
	v_mfma_f32_16x16x128_f8f6f4 v[32:35], v[8:15], v[212:219], v[32:35]
	s_nop 0
	s_barrier
	s_add_u32 s58, s34, 0x40000
	s_addc_u32 s59, s35, 0
	s_add_i32 s60, s54, s43
	v_lshl_add_u64 v[0:1], s[58:59], 0, v[156:157]
	s_mov_b32 m0, s60
	s_nop 0
	global_load_lds_dwordx4 v[0:1], off
	v_lshl_add_u64 v[0:1], s[58:59], 0, v[152:153]
	s_add_i32 m0, s60, 0x2000
	s_nop 0
	global_load_lds_dwordx4 v[0:1], off
	s_waitcnt vmcnt(6)
	s_barrier
	s_nop 0
	v_mfma_f32_16x16x128_f8f6f4 v[76:79], v[16:23], v[188:195], v[76:79]
	v_mfma_f32_16x16x128_f8f6f4 v[72:75], v[220:227], v[188:195], v[72:75]
	v_mfma_f32_16x16x128_f8f6f4 v[60:63], v[16:23], v[196:203], v[60:63]
	v_mfma_f32_16x16x128_f8f6f4 v[56:59], v[220:227], v[196:203], v[56:59]
	v_mfma_f32_16x16x128_f8f6f4 v[44:47], v[16:23], v[204:211], v[44:47]
	v_mfma_f32_16x16x128_f8f6f4 v[40:43], v[220:227], v[204:211], v[40:43]
	v_mfma_f32_16x16x128_f8f6f4 v[28:31], v[16:23], v[212:219], v[28:31]
	v_mfma_f32_16x16x128_f8f6f4 v[24:27], v[220:227], v[212:219], v[24:27]
	s_nop 0
	s_add_i32 s58, 0, 0x18000
	v_add_u32_e32 v12, s58, v174
	s_barrier
	ds_read_b128 v[0:3], v12
	ds_read_b128 v[4:7], v12 offset:1024
	ds_read_b128 v[8:11], v12 offset:2048
	ds_read_b128 v[12:15], v12 offset:3072
	s_add_u32 s36, s36, 0x40000
	s_addc_u32 s37, s37, 0
	s_mov_b32 m0, s46
	v_lshl_add_u64 v[212:213], s[36:37], 0, v[158:159]
	ds_read_b128 v[16:19], v176 offset:32768
	ds_read_b128 v[20:23], v176 offset:33792
	ds_read_b128 v[188:191], v176 offset:34816
	ds_read_b128 v[192:195], v176 offset:35840
	ds_read_b128 v[196:199], v176 offset:36864
	ds_read_b128 v[200:203], v176 offset:37888
	ds_read_b128 v[204:207], v176 offset:38912
	ds_read_b128 v[208:211], v176 offset:39936
	global_load_lds_dwordx4 v[212:213], off
	v_lshl_add_u64 v[212:213], s[36:37], 0, v[154:155]
	s_mov_b32 m0, s47
	s_nop 0
	global_load_lds_dwordx4 v[212:213], off
	s_waitcnt lgkmcnt(8)
	s_barrier
;     __device__ __forceinline__ void operator()(const f32x4 (&acc)[2][2][4][2], const Unit& u, int wr, int wc, int fr, int fq, const Pre& pr) const {
;         const int c0 = 256 * u.pn + 32 * wc + 8 * fq; const float* bp = bdn + (size_t)u.aux * DM + c0;
;         const f32x4 b00 = *(const f32x4*)bp, b01 = *(const f32x4*)(bp + 4), b10 = *(const f32x4*)(bp + 128), b11 = *(const f32x4*)(bp + 132); const float (&gwv)[8] = pr.gwv;
	s_waitcnt lgkmcnt(0)
	s_nop 0
	s_waitcnt lgkmcnt(0)
	v_mfma_f32_16x16x128_f8f6f4 v[148:151], v[0:7], v[16:23], v[148:151]
	v_mfma_f32_16x16x128_f8f6f4 v[144:147], v[8:15], v[16:23], v[144:147]
	v_mfma_f32_16x16x128_f8f6f4 v[140:143], v[0:7], v[188:195], v[140:143]
	v_mfma_f32_16x16x128_f8f6f4 v[136:139], v[8:15], v[188:195], v[136:139]
	v_mfma_f32_16x16x128_f8f6f4 v[132:135], v[0:7], v[196:203], v[132:135]
	v_mfma_f32_16x16x128_f8f6f4 v[120:123], v[8:15], v[196:203], v[120:123]
	v_mfma_f32_16x16x128_f8f6f4 v[100:103], v[0:7], v[204:211], v[100:103]
	v_mfma_f32_16x16x128_f8f6f4 v[96:99], v[8:15], v[204:211], v[96:99]
	s_nop 0
	s_barrier
	s_add_i32 s36, 0, 0x1c000
	s_add_i32 s37, s58, s43
	v_add_u32_e32 v165, s36, v174
	v_lshl_add_u64 v[166:167], v[166:167], 0, s[4:5]
	s_mov_b32 m0, s37
	ds_read_b128 v[212:215], v165
	ds_read_b128 v[216:219], v165 offset:1024
	ds_read_b128 v[220:223], v165 offset:2048
	ds_read_b128 v[224:227], v165 offset:3072
	global_load_lds_dwordx4 v[166:167], off
	v_lshl_add_u64 v[166:167], v[168:169], 0, s[4:5]
	s_add_i32 m0, s37, 0x2000
	s_nop 0
	global_load_lds_dwordx4 v[166:167], off
	s_barrier
	s_waitcnt lgkmcnt(0)
	s_nop 0
	s_waitcnt lgkmcnt(0)
	v_mfma_f32_16x16x128_f8f6f4 v[128:131], v[212:219], v[16:23], v[128:131]
	v_mfma_f32_16x16x128_f8f6f4 v[124:127], v[220:227], v[16:23], v[124:127]
	v_mfma_f32_16x16x128_f8f6f4 v[116:119], v[212:219], v[188:195], v[116:119]
	v_mfma_f32_16x16x128_f8f6f4 v[112:115], v[220:227], v[188:195], v[112:115]
	v_mfma_f32_16x16x128_f8f6f4 v[108:111], v[212:219], v[196:203], v[108:111]
	v_mfma_f32_16x16x128_f8f6f4 v[104:107], v[220:227], v[196:203], v[104:107]
	v_mfma_f32_16x16x128_f8f6f4 v[92:95], v[212:219], v[204:211], v[92:95]
	v_mfma_f32_16x16x128_f8f6f4 v[88:91], v[220:227], v[204:211], v[88:91]
	s_nop 0
	s_mov_b32 m0, s50
	v_lshl_add_u64 v[166:167], v[170:171], 0, s[4:5]
	s_barrier
	ds_read_b128 v[16:19], v176 offset:49152
	ds_read_b128 v[20:23], v176 offset:50176
	ds_read_b128 v[188:191], v176 offset:51200
	ds_read_b128 v[192:195], v176 offset:52224
	ds_read_b128 v[196:199], v176 offset:53248
	ds_read_b128 v[200:203], v176 offset:54272
	ds_read_b128 v[204:207], v176 offset:55296
	ds_read_b128 v[208:211], v176 offset:56320
	global_load_lds_dwordx4 v[166:167], off
	v_lshl_add_u64 v[166:167], v[172:173], 0, s[4:5]
	s_mov_b32 m0, s51
	s_nop 0
	global_load_lds_dwordx4 v[166:167], off
	s_barrier
	s_waitcnt lgkmcnt(0)
	s_nop 0
	s_waitcnt lgkmcnt(0)
	v_mfma_f32_16x16x128_f8f6f4 v[84:87], v[0:7], v[16:23], v[84:87]
	v_mfma_f32_16x16x128_f8f6f4 v[80:83], v[8:15], v[16:23], v[80:83]
	v_mfma_f32_16x16x128_f8f6f4 v[68:71], v[0:7], v[188:195], v[68:71]
	v_mfma_f32_16x16x128_f8f6f4 v[64:67], v[8:15], v[188:195], v[64:67]
	v_mfma_f32_16x16x128_f8f6f4 v[52:55], v[0:7], v[196:203], v[52:55]
	v_mfma_f32_16x16x128_f8f6f4 v[48:51], v[8:15], v[196:203], v[48:51]
	v_mfma_f32_16x16x128_f8f6f4 v[36:39], v[0:7], v[204:211], v[36:39]
	v_mfma_f32_16x16x128_f8f6f4 v[32:35], v[8:15], v[204:211], v[32:35]
	s_nop 0
	s_barrier
	s_add_u32 s34, s34, 0x40080
	s_addc_u32 s35, s35, 0
	s_add_i32 s36, s36, s43
	v_lshl_add_u64 v[0:1], s[34:35], 0, v[156:157]
	s_mov_b32 m0, s36
	s_nop 0
	global_load_lds_dwordx4 v[0:1], off
	v_lshl_add_u64 v[0:1], s[34:35], 0, v[152:153]
	s_add_i32 m0, s36, 0x2000
	s_nop 0
	global_load_lds_dwordx4 v[0:1], off
	s_waitcnt vmcnt(6)
	s_barrier
	s_nop 0
	v_mfma_f32_16x16x128_f8f6f4 v[76:79], v[212:219], v[16:23], v[76:79]
	v_mfma_f32_16x16x128_f8f6f4 v[72:75], v[220:227], v[16:23], v[72:75]
	v_mfma_f32_16x16x128_f8f6f4 v[60:63], v[212:219], v[188:195], v[60:63]
	v_mfma_f32_16x16x128_f8f6f4 v[56:59], v[220:227], v[188:195], v[56:59]
	v_mfma_f32_16x16x128_f8f6f4 v[44:47], v[212:219], v[196:203], v[44:47]
	v_mfma_f32_16x16x128_f8f6f4 v[40:43], v[220:227], v[196:203], v[40:43]
	v_mfma_f32_16x16x128_f8f6f4 v[28:31], v[212:219], v[204:211], v[28:31]
	v_mfma_f32_16x16x128_f8f6f4 v[24:27], v[220:227], v[204:211], v[24:27]
	s_nop 0
	s_add_i32 s57, s57, 2
	s_add_u32 s30, s30, 0x100
	s_addc_u32 s31, s31, 0
	s_add_u32 s13, s13, 0x100
	s_addc_u32 s55, s55, 0
	s_cmp_gt_u32 s57, 13
	s_barrier
	s_cbranch_scc0 .LBB0_2796
	s_nop 15
 s_nop 7
	v_mbcnt_lo_u32_b32 v18, -1, 0
	v_mbcnt_hi_u32_b32 v18, -1, v18
	s_lshl_b32 s13, s28, 8
	v_ashrrev_i32_e32 v0, 1, v18
	v_and_b32_e32 v0, -8, v0
	s_or_b32 s13, s13, s49
	v_ashrrev_i32_e32 v165, 31, v164
	v_add_u32_e32 v16, s13, v0
	v_lshlrev_b64 v[0:1], 13, v[164:165]
	v_lshl_add_u64 v[0:1], s[74:75], 0, v[0:1]
	v_ashrrev_i32_e32 v17, 31, v16
	v_lshl_add_u64 v[0:1], v[16:17], 2, v[0:1]
	global_load_dwordx4 v[12:15], v[0:1], off
	global_load_dwordx4 v[8:11], v[0:1], off offset:16
	global_load_dwordx4 v[4:7], v[0:1], off offset:512
	s_nop 0
	global_load_dwordx4 v[0:3], v[0:1], off offset:528
	s_waitcnt vmcnt(0)
;     __device__ __forceinline__ void operator()(const f32x4 (&acc)[2][2][4][2], const Unit& u, int wr, int wc, int fr, int fq, const Pre& pr) const {
;     ...
; #pragma unroll
;         for (int ai = 0; ai < 2; ++ai)
; #pragma unroll
;             for (int m = 0; m < 4; ++m) {
;                 const int row = u.pm * 256 + ai * 128 + wr * 64 + m * 16 + fr; const float gw = gwv[ai * 4 + m] * YS_SCALE;
;                 constexpr float iw = 1.0f / W8_SCALE;
;                 const f32x4 o0 = (acc[ai][0][m][0] * iw + b00) * gw, o1 = (acc[ai][0][m][1] * iw + b01) * gw, o2 = (acc[ai][1][m][0] * iw + b10) * gw, o3 = (acc[ai][1][m][1] * iw + b11) * gw;
;                 *(u32x2*)(ys + (size_t)row * DM + c0) = pack_fp8x8(o0[0], o0[1], o0[2], o0[3], o1[0], o1[1], o1[2], o1[3]);
;                 *(u32x2*)(ys + (size_t)row * DM + c0 + 128) = pack_fp8x8(o2[0], o2[1], o2[2], o2[3], o3[0], o3[1], o3[2], o3[3]);
;             }
	v_mul_f32_e32 v20, 0x41800000, v187
	v_mov_b32_e32 v22, 0
	v_mov_b32_e32 v23, 0
	v_mov_b32_e32 v164, 0
	v_mov_b32_e32 v165, 0
	v_mul_f32_e32 v166, 0x41800000, v186
	v_mov_b32_e32 v168, 0
	v_mov_b32_e32 v169, 0
	v_mov_b32_e32 v170, 0
	v_mov_b32_e32 v171, 0
	v_and_or_b32 v18, v18, 15, s48
	v_add_u32_e32 v18, s11, v18
	v_ashrrev_i32_e32 v19, 31, v18
	v_add_u32_e32 v186, 16, v18
	v_lshlrev_b64 v[190:191], 11, v[18:19]
	v_ashrrev_i32_e32 v187, 31, v186
	v_lshl_add_u64 v[190:191], s[2:3], 0, v[190:191]
	v_lshlrev_b64 v[186:187], 11, v[186:187]
	v_mul_f32_e32 v172, 0x41800000, v185
	v_lshl_add_u64 v[190:191], v[190:191], 0, v[16:17]
	v_lshl_add_u64 v[186:187], s[2:3], 0, v[186:187]
	v_lshl_add_u64 v[186:187], v[186:187], 0, v[16:17]
	v_add_u32_e32 v188, 32, v18
	v_ashrrev_i32_e32 v189, 31, v188
	s_and_b64 vcc, exec, s[8:9]
	s_mov_b32 s34, s12
	s_mov_b32 s28, s10
	s_mov_b64 s[36:37], s[16:17]
	s_mov_b64 s[30:31], s[14:15]
	v_pk_fma_f32 v[148:149], v[148:149], s[6:7], v[12:13] op_sel_hi:[1,0,1]
	v_pk_fma_f32 v[144:145], v[144:145], s[6:7], v[8:9] op_sel_hi:[1,0,1]
	v_pk_fma_f32 v[150:151], v[150:151], s[6:7], v[14:15] op_sel_hi:[1,0,1]
	v_pk_fma_f32 v[146:147], v[146:147], s[6:7], v[10:11] op_sel_hi:[1,0,1]
	v_pk_fma_f32 v[130:131], v[130:131], s[6:7], v[6:7] op_sel_hi:[1,0,1]
	v_pk_fma_f32 v[128:129], v[128:129], s[6:7], v[4:5] op_sel_hi:[1,0,1]
	v_pk_fma_f32 v[126:127], v[126:127], s[6:7], v[2:3] op_sel_hi:[1,0,1]
	v_pk_fma_f32 v[124:125], v[124:125], s[6:7], v[0:1] op_sel_hi:[1,0,1]
	v_pk_mul_f32 v[148:149], v[20:21], v[148:149] op_sel_hi:[0,1]
	v_pk_mul_f32 v[144:145], v[20:21], v[144:145] op_sel_hi:[0,1]
	v_pk_fma_f32 v[140:141], v[140:141], s[6:7], v[12:13] op_sel_hi:[1,0,1]
	v_pk_fma_f32 v[136:137], v[136:137], s[6:7], v[8:9] op_sel_hi:[1,0,1]
	v_pk_mul_f32 v[150:151], v[20:21], v[150:151] op_sel_hi:[0,1]
	v_pk_mul_f32 v[146:147], v[20:21], v[146:147] op_sel_hi:[0,1]
	v_pk_mul_f32 v[130:131], v[20:21], v[130:131] op_sel_hi:[0,1]
	v_pk_mul_f32 v[128:129], v[20:21], v[128:129] op_sel_hi:[0,1]
	v_pk_mul_f32 v[126:127], v[20:21], v[126:127] op_sel_hi:[0,1]
	v_pk_mul_f32 v[20:21], v[20:21], v[124:125] op_sel_hi:[0,1]
	v_cvt_pk_fp8_f32 v22, v148, v149
	v_cvt_pk_fp8_f32 v23, v144, v145
	v_pk_fma_f32 v[116:117], v[116:117], s[6:7], v[4:5] op_sel_hi:[1,0,1]
	v_pk_fma_f32 v[112:113], v[112:113], s[6:7], v[0:1] op_sel_hi:[1,0,1]
	v_pk_mul_f32 v[140:141], v[166:167], v[140:141] op_sel_hi:[0,1]
	v_pk_mul_f32 v[136:137], v[166:167], v[136:137] op_sel_hi:[0,1]
	v_cvt_pk_fp8_f32 v164, v128, v129
	v_cvt_pk_fp8_f32 v165, v20, v21
	v_pk_mul_f32 v[116:117], v[166:167], v[116:117] op_sel_hi:[0,1]
	v_pk_mul_f32 v[112:113], v[166:167], v[112:113] op_sel_hi:[0,1]
	v_cvt_pk_fp8_f32 v168, v140, v141
	v_cvt_pk_fp8_f32 v169, v136, v137
	v_cvt_pk_fp8_f32 v170, v116, v117
	v_cvt_pk_fp8_f32 v171, v112, v113
	v_pk_fma_f32 v[142:143], v[142:143], s[6:7], v[14:15] op_sel_hi:[1,0,1]
	v_pk_fma_f32 v[138:139], v[138:139], s[6:7], v[10:11] op_sel_hi:[1,0,1]
	v_cvt_pk_fp8_f32 v22, v150, v151 op_sel:[0,0,1]
	v_cvt_pk_fp8_f32 v23, v146, v147 op_sel:[0,0,1]
	v_pk_fma_f32 v[118:119], v[118:119], s[6:7], v[6:7] op_sel_hi:[1,0,1]
	v_pk_fma_f32 v[114:115], v[114:115], s[6:7], v[2:3] op_sel_hi:[1,0,1]
	v_pk_mul_f32 v[124:125], v[166:167], v[142:143] op_sel_hi:[0,1]
	v_pk_mul_f32 v[138:139], v[166:167], v[138:139] op_sel_hi:[0,1]
	v_cvt_pk_fp8_f32 v164, v130, v131 op_sel:[0,0,1]
	v_cvt_pk_fp8_f32 v165, v126, v127 op_sel:[0,0,1]
	v_pk_mul_f32 v[118:119], v[166:167], v[118:119] op_sel_hi:[0,1]
	v_pk_mul_f32 v[114:115], v[166:167], v[114:115] op_sel_hi:[0,1]
	v_cvt_pk_fp8_f32 v168, v124, v125 op_sel:[0,0,1]
	v_cvt_pk_fp8_f32 v169, v138, v139 op_sel:[0,0,1]
	v_pk_fma_f32 v[120:121], v[120:121], s[6:7], v[8:9] op_sel_hi:[1,0,1]
	v_cvt_pk_fp8_f32 v170, v118, v119 op_sel:[0,0,1]
	v_cvt_pk_fp8_f32 v171, v114, v115 op_sel:[0,0,1]
	global_store_dwordx2 v[190:191], v[22:23], off
	global_store_dwordx2 v[190:191], v[164:165], off offset:128
	global_store_dwordx2 v[186:187], v[168:169], off
	global_store_dwordx2 v[186:187], v[170:171], off offset:128
	v_pk_mul_f32 v[22:23], v[172:173], v[120:121] op_sel_hi:[0,1]
	v_mov_b32_e32 v113, 0
	v_cvt_pk_fp8_f32 v113, v22, v23
	v_pk_fma_f32 v[132:133], v[132:133], s[6:7], v[12:13] op_sel_hi:[1,0,1]
	v_pk_fma_f32 v[122:123], v[122:123], s[6:7], v[10:11] op_sel_hi:[1,0,1]
	v_pk_mul_f32 v[132:133], v[172:173], v[132:133] op_sel_hi:[0,1]
	v_pk_mul_f32 v[20:21], v[172:173], v[122:123] op_sel_hi:[0,1]
	v_pk_fma_f32 v[108:109], v[108:109], s[6:7], v[4:5] op_sel_hi:[1,0,1]
	v_pk_fma_f32 v[104:105], v[104:105], s[6:7], v[0:1] op_sel_hi:[1,0,1]
	v_mov_b32_e32 v112, 0
	v_pk_mul_f32 v[108:109], v[172:173], v[108:109] op_sel_hi:[0,1]
	v_cvt_pk_fp8_f32 v112, v132, v133
	v_pk_mul_f32 v[104:105], v[172:173], v[104:105] op_sel_hi:[0,1]
	v_cvt_pk_fp8_f32 v113, v20, v21 op_sel:[0,0,1]
	v_mov_b32_e32 v20, 0
	v_mov_b32_e32 v21, 0
	v_cvt_pk_fp8_f32 v20, v108, v109
	v_cvt_pk_fp8_f32 v21, v104, v105
	v_pk_fma_f32 v[134:135], v[134:135], s[6:7], v[14:15] op_sel_hi:[1,0,1]
	v_pk_fma_f32 v[110:111], v[110:111], s[6:7], v[6:7] op_sel_hi:[1,0,1]
	v_pk_mul_f32 v[134:135], v[172:173], v[134:135] op_sel_hi:[0,1]
	v_pk_fma_f32 v[106:107], v[106:107], s[6:7], v[2:3] op_sel_hi:[1,0,1]
	v_pk_mul_f32 v[110:111], v[172:173], v[110:111] op_sel_hi:[0,1]
	v_pk_mul_f32 v[22:23], v[172:173], v[106:107] op_sel_hi:[0,1]
	v_cvt_pk_fp8_f32 v112, v134, v135 op_sel:[0,0,1]
	v_lshlrev_b64 v[104:105], 11, v[188:189]
	v_cvt_pk_fp8_f32 v20, v110, v111 op_sel:[0,0,1]
	v_cvt_pk_fp8_f32 v21, v22, v23 op_sel:[0,0,1]
	v_lshl_add_u64 v[22:23], s[2:3], 0, v[104:105]
	v_lshl_add_u64 v[22:23], v[22:23], 0, v[16:17]
;     __device__ __forceinline__ void operator()(const f32x4 (&acc)[2][2][4][2], const Unit& u, int wr, int wc, int fr, int fq, const Pre& pr) const {
;     ...
; #pragma unroll
;         for (int ai = 0; ai < 2; ++ai)
; #pragma unroll
;             for (int m = 0; m < 4; ++m) {
;                 const int row = u.pm * 256 + ai * 128 + wr * 64 + m * 16 + fr; const float gw = gwv[ai * 4 + m] * YS_SCALE;
;                 constexpr float iw = 1.0f / W8_SCALE;
;                 const f32x4 o0 = (acc[ai][0][m][0] * iw + b00) * gw, o1 = (acc[ai][0][m][1] * iw + b01) * gw, o2 = (acc[ai][1][m][0] * iw + b10) * gw, o3 = (acc[ai][1][m][1] * iw + b11) * gw;
;                 *(u32x2*)(ys + (size_t)row * DM + c0) = pack_fp8x8(o0[0], o0[1], o0[2], o0[3], o1[0], o1[1], o1[2], o1[3]);
;                 *(u32x2*)(ys + (size_t)row * DM + c0 + 128) = pack_fp8x8(o2[0], o2[1], o2[2], o2[3], o3[0], o3[1], o3[2], o3[3]);
;             }
	global_store_dwordx2 v[22:23], v[112:113], off
	global_store_dwordx2 v[22:23], v[20:21], off offset:128
	v_mul_f32_e32 v22, 0x41800000, v184
	v_pk_fma_f32 v[100:101], v[100:101], s[6:7], v[12:13] op_sel_hi:[1,0,1]
	v_pk_fma_f32 v[96:97], v[96:97], s[6:7], v[8:9] op_sel_hi:[1,0,1]
	v_pk_fma_f32 v[102:103], v[102:103], s[6:7], v[14:15] op_sel_hi:[1,0,1]
	v_pk_mul_f32 v[100:101], v[22:23], v[100:101] op_sel_hi:[0,1]
	v_pk_fma_f32 v[98:99], v[98:99], s[6:7], v[10:11] op_sel_hi:[1,0,1]
	v_pk_mul_f32 v[96:97], v[22:23], v[96:97] op_sel_hi:[0,1]
	v_pk_fma_f32 v[94:95], v[94:95], s[6:7], v[6:7] op_sel_hi:[1,0,1]
	v_pk_fma_f32 v[92:93], v[92:93], s[6:7], v[4:5] op_sel_hi:[1,0,1]
	v_pk_fma_f32 v[90:91], v[90:91], s[6:7], v[2:3] op_sel_hi:[1,0,1]
	v_pk_fma_f32 v[88:89], v[88:89], s[6:7], v[0:1] op_sel_hi:[1,0,1]
	v_mov_b32_e32 v104, 0
	v_mov_b32_e32 v105, 0
	v_pk_mul_f32 v[102:103], v[22:23], v[102:103] op_sel_hi:[0,1]
	v_pk_mul_f32 v[98:99], v[22:23], v[98:99] op_sel_hi:[0,1]
	v_pk_mul_f32 v[94:95], v[22:23], v[94:95] op_sel_hi:[0,1]
	v_pk_mul_f32 v[92:93], v[22:23], v[92:93] op_sel_hi:[0,1]
	v_cvt_pk_fp8_f32 v104, v100, v101
	v_cvt_pk_fp8_f32 v105, v96, v97
	v_pk_mul_f32 v[90:91], v[22:23], v[90:91] op_sel_hi:[0,1]
	v_pk_mul_f32 v[22:23], v[22:23], v[88:89] op_sel_hi:[0,1]
	v_mov_b32_e32 v88, 0
	v_mov_b32_e32 v89, 0
	v_cvt_pk_fp8_f32 v88, v92, v93
	v_cvt_pk_fp8_f32 v89, v22, v23
	v_add_u32_e32 v20, 48, v18
	v_cvt_pk_fp8_f32 v104, v102, v103 op_sel:[0,0,1]
	v_cvt_pk_fp8_f32 v105, v98, v99 op_sel:[0,0,1]
	v_ashrrev_i32_e32 v21, 31, v20
	v_lshlrev_b64 v[20:21], 11, v[20:21]
	v_cvt_pk_fp8_f32 v88, v94, v95 op_sel:[0,0,1]
	v_cvt_pk_fp8_f32 v89, v90, v91 op_sel:[0,0,1]
	v_lshl_add_u64 v[20:21], s[2:3], 0, v[20:21]
	v_lshl_add_u64 v[20:21], v[20:21], 0, v[16:17]
	v_mul_f32_e32 v22, 0x41800000, v183
	v_pk_fma_f32 v[84:85], v[84:85], s[6:7], v[12:13] op_sel_hi:[1,0,1]
	v_pk_fma_f32 v[80:81], v[80:81], s[6:7], v[8:9] op_sel_hi:[1,0,1]
	global_store_dwordx2 v[20:21], v[104:105], off
	global_store_dwordx2 v[20:21], v[88:89], off offset:128
	v_pk_fma_f32 v[86:87], v[86:87], s[6:7], v[14:15] op_sel_hi:[1,0,1]
	v_pk_mul_f32 v[84:85], v[22:23], v[84:85] op_sel_hi:[0,1]
	v_pk_fma_f32 v[82:83], v[82:83], s[6:7], v[10:11] op_sel_hi:[1,0,1]
	v_pk_mul_f32 v[80:81], v[22:23], v[80:81] op_sel_hi:[0,1]
	v_pk_fma_f32 v[78:79], v[78:79], s[6:7], v[6:7] op_sel_hi:[1,0,1]
	v_pk_fma_f32 v[76:77], v[76:77], s[6:7], v[4:5] op_sel_hi:[1,0,1]
	v_pk_fma_f32 v[74:75], v[74:75], s[6:7], v[2:3] op_sel_hi:[1,0,1]
	v_pk_fma_f32 v[72:73], v[72:73], s[6:7], v[0:1] op_sel_hi:[1,0,1]
	v_mov_b32_e32 v88, 0
	v_mov_b32_e32 v89, 0
	v_pk_mul_f32 v[86:87], v[22:23], v[86:87] op_sel_hi:[0,1]
	v_pk_mul_f32 v[82:83], v[22:23], v[82:83] op_sel_hi:[0,1]
	v_pk_mul_f32 v[78:79], v[22:23], v[78:79] op_sel_hi:[0,1]
	v_pk_mul_f32 v[76:77], v[22:23], v[76:77] op_sel_hi:[0,1]
	v_cvt_pk_fp8_f32 v88, v84, v85
	v_cvt_pk_fp8_f32 v89, v80, v81
	v_pk_mul_f32 v[74:75], v[22:23], v[74:75] op_sel_hi:[0,1]
	v_pk_mul_f32 v[22:23], v[22:23], v[72:73] op_sel_hi:[0,1]
	v_mov_b32_e32 v72, 0
	v_mov_b32_e32 v73, 0
	v_cvt_pk_fp8_f32 v72, v76, v77
	v_cvt_pk_fp8_f32 v73, v22, v23
	v_add_u32_e32 v20, 0x80, v18
	v_cvt_pk_fp8_f32 v88, v86, v87 op_sel:[0,0,1]
	v_cvt_pk_fp8_f32 v89, v82, v83 op_sel:[0,0,1]
	v_ashrrev_i32_e32 v21, 31, v20
	v_lshlrev_b64 v[20:21], 11, v[20:21]
	v_cvt_pk_fp8_f32 v72, v78, v79 op_sel:[0,0,1]
	v_cvt_pk_fp8_f32 v73, v74, v75 op_sel:[0,0,1]
	v_lshl_add_u64 v[20:21], s[2:3], 0, v[20:21]
	v_lshl_add_u64 v[20:21], v[20:21], 0, v[16:17]
	v_mul_f32_e32 v22, 0x41800000, v182
	v_pk_fma_f32 v[68:69], v[68:69], s[6:7], v[12:13] op_sel_hi:[1,0,1]
	v_pk_fma_f32 v[64:65], v[64:65], s[6:7], v[8:9] op_sel_hi:[1,0,1]
	global_store_dwordx2 v[20:21], v[88:89], off
	global_store_dwordx2 v[20:21], v[72:73], off offset:128
	v_pk_fma_f32 v[70:71], v[70:71], s[6:7], v[14:15] op_sel_hi:[1,0,1]
	v_pk_mul_f32 v[68:69], v[22:23], v[68:69] op_sel_hi:[0,1]
	v_pk_fma_f32 v[66:67], v[66:67], s[6:7], v[10:11] op_sel_hi:[1,0,1]
	v_pk_mul_f32 v[64:65], v[22:23], v[64:65] op_sel_hi:[0,1]
	v_pk_fma_f32 v[62:63], v[62:63], s[6:7], v[6:7] op_sel_hi:[1,0,1]
	v_pk_fma_f32 v[60:61], v[60:61], s[6:7], v[4:5] op_sel_hi:[1,0,1]
	v_pk_fma_f32 v[58:59], v[58:59], s[6:7], v[2:3] op_sel_hi:[1,0,1]
	v_pk_fma_f32 v[56:57], v[56:57], s[6:7], v[0:1] op_sel_hi:[1,0,1]
	v_mov_b32_e32 v72, 0
	v_mov_b32_e32 v73, 0
	v_pk_mul_f32 v[70:71], v[22:23], v[70:71] op_sel_hi:[0,1]
	v_pk_mul_f32 v[66:67], v[22:23], v[66:67] op_sel_hi:[0,1]
;     __device__ __forceinline__ void operator()(const f32x4 (&acc)[2][2][4][2], const Unit& u, int wr, int wc, int fr, int fq, const Pre& pr) const {
;     ...
; #pragma unroll
;         for (int ai = 0; ai < 2; ++ai)
; #pragma unroll
;             for (int m = 0; m < 4; ++m) {
;                 const int row = u.pm * 256 + ai * 128 + wr * 64 + m * 16 + fr; const float gw = gwv[ai * 4 + m] * YS_SCALE;
;                 constexpr float iw = 1.0f / W8_SCALE;
;                 const f32x4 o0 = (acc[ai][0][m][0] * iw + b00) * gw, o1 = (acc[ai][0][m][1] * iw + b01) * gw, o2 = (acc[ai][1][m][0] * iw + b10) * gw, o3 = (acc[ai][1][m][1] * iw + b11) * gw;
;                 *(u32x2*)(ys + (size_t)row * DM + c0) = pack_fp8x8(o0[0], o0[1], o0[2], o0[3], o1[0], o1[1], o1[2], o1[3]);
;                 *(u32x2*)(ys + (size_t)row * DM + c0 + 128) = pack_fp8x8(o2[0], o2[1], o2[2], o2[3], o3[0], o3[1], o3[2], o3[3]);
;             }
	v_pk_mul_f32 v[62:63], v[22:23], v[62:63] op_sel_hi:[0,1]
	v_pk_mul_f32 v[60:61], v[22:23], v[60:61] op_sel_hi:[0,1]
	v_cvt_pk_fp8_f32 v72, v68, v69
	v_cvt_pk_fp8_f32 v73, v64, v65
	v_pk_mul_f32 v[58:59], v[22:23], v[58:59] op_sel_hi:[0,1]
	v_pk_mul_f32 v[22:23], v[22:23], v[56:57] op_sel_hi:[0,1]
	v_mov_b32_e32 v56, 0
	v_mov_b32_e32 v57, 0
	v_cvt_pk_fp8_f32 v56, v60, v61
	v_cvt_pk_fp8_f32 v57, v22, v23
	v_add_u32_e32 v20, 0x90, v18
	v_cvt_pk_fp8_f32 v72, v70, v71 op_sel:[0,0,1]
	v_cvt_pk_fp8_f32 v73, v66, v67 op_sel:[0,0,1]
	v_ashrrev_i32_e32 v21, 31, v20
	v_lshlrev_b64 v[20:21], 11, v[20:21]
	v_cvt_pk_fp8_f32 v56, v62, v63 op_sel:[0,0,1]
	v_cvt_pk_fp8_f32 v57, v58, v59 op_sel:[0,0,1]
	v_lshl_add_u64 v[20:21], s[2:3], 0, v[20:21]
	v_lshl_add_u64 v[20:21], v[20:21], 0, v[16:17]
	v_mul_f32_e32 v22, 0x41800000, v181
	v_pk_fma_f32 v[52:53], v[52:53], s[6:7], v[12:13] op_sel_hi:[1,0,1]
	v_pk_fma_f32 v[48:49], v[48:49], s[6:7], v[8:9] op_sel_hi:[1,0,1]
	global_store_dwordx2 v[20:21], v[72:73], off
	global_store_dwordx2 v[20:21], v[56:57], off offset:128
	v_pk_fma_f32 v[54:55], v[54:55], s[6:7], v[14:15] op_sel_hi:[1,0,1]
	v_pk_mul_f32 v[52:53], v[22:23], v[52:53] op_sel_hi:[0,1]
	v_pk_fma_f32 v[50:51], v[50:51], s[6:7], v[10:11] op_sel_hi:[1,0,1]
	v_pk_mul_f32 v[48:49], v[22:23], v[48:49] op_sel_hi:[0,1]
	v_pk_fma_f32 v[46:47], v[46:47], s[6:7], v[6:7] op_sel_hi:[1,0,1]
	v_pk_fma_f32 v[44:45], v[44:45], s[6:7], v[4:5] op_sel_hi:[1,0,1]
	v_pk_fma_f32 v[42:43], v[42:43], s[6:7], v[2:3] op_sel_hi:[1,0,1]
	v_pk_fma_f32 v[40:41], v[40:41], s[6:7], v[0:1] op_sel_hi:[1,0,1]
	v_mov_b32_e32 v56, 0
	v_mov_b32_e32 v57, 0
	v_pk_mul_f32 v[54:55], v[22:23], v[54:55] op_sel_hi:[0,1]
	v_pk_mul_f32 v[50:51], v[22:23], v[50:51] op_sel_hi:[0,1]
	v_pk_mul_f32 v[46:47], v[22:23], v[46:47] op_sel_hi:[0,1]
	v_pk_mul_f32 v[44:45], v[22:23], v[44:45] op_sel_hi:[0,1]
	v_cvt_pk_fp8_f32 v56, v52, v53
	v_cvt_pk_fp8_f32 v57, v48, v49
	v_pk_mul_f32 v[42:43], v[22:23], v[42:43] op_sel_hi:[0,1]
	v_pk_mul_f32 v[22:23], v[22:23], v[40:41] op_sel_hi:[0,1]
	v_mov_b32_e32 v40, 0
	v_mov_b32_e32 v41, 0
	v_cvt_pk_fp8_f32 v40, v44, v45
	v_cvt_pk_fp8_f32 v41, v22, v23
	v_add_u32_e32 v20, 0xa0, v18
	v_cvt_pk_fp8_f32 v56, v54, v55 op_sel:[0,0,1]
	v_cvt_pk_fp8_f32 v57, v50, v51 op_sel:[0,0,1]
	v_ashrrev_i32_e32 v21, 31, v20
	v_lshlrev_b64 v[20:21], 11, v[20:21]
	v_cvt_pk_fp8_f32 v40, v46, v47 op_sel:[0,0,1]
	v_cvt_pk_fp8_f32 v41, v42, v43 op_sel:[0,0,1]
	v_lshl_add_u64 v[20:21], s[2:3], 0, v[20:21]
	v_lshl_add_u64 v[20:21], v[20:21], 0, v[16:17]
	global_store_dwordx2 v[20:21], v[56:57], off
	global_store_dwordx2 v[20:21], v[40:41], off offset:128
	v_mul_f32_e32 v20, 0x41800000, v180
	v_pk_fma_f32 v[12:13], v[36:37], s[6:7], v[12:13] op_sel_hi:[1,0,1]
	v_pk_fma_f32 v[8:9], v[32:33], s[6:7], v[8:9] op_sel_hi:[1,0,1]
	v_pk_mul_f32 v[12:13], v[20:21], v[12:13] op_sel_hi:[0,1]
	v_pk_mul_f32 v[8:9], v[20:21], v[8:9] op_sel_hi:[0,1]
	v_pk_fma_f32 v[4:5], v[28:29], s[6:7], v[4:5] op_sel_hi:[1,0,1]
	v_pk_fma_f32 v[0:1], v[24:25], s[6:7], v[0:1] op_sel_hi:[1,0,1]
	v_mov_b32_e32 v22, 0
	v_mov_b32_e32 v23, 0
	v_pk_mul_f32 v[4:5], v[20:21], v[4:5] op_sel_hi:[0,1]
	v_cvt_pk_fp8_f32 v22, v12, v13
	v_cvt_pk_fp8_f32 v23, v8, v9
	v_pk_mul_f32 v[0:1], v[20:21], v[0:1] op_sel_hi:[0,1]
	v_mov_b32_e32 v8, 0
	v_mov_b32_e32 v9, 0
	v_cvt_pk_fp8_f32 v8, v4, v5
	v_cvt_pk_fp8_f32 v9, v0, v1
	v_pk_fma_f32 v[14:15], v[38:39], s[6:7], v[14:15] op_sel_hi:[1,0,1]
	v_pk_fma_f32 v[10:11], v[34:35], s[6:7], v[10:11] op_sel_hi:[1,0,1]
	v_add_u32_e32 v18, 0xb0, v18
	v_pk_mul_f32 v[14:15], v[20:21], v[14:15] op_sel_hi:[0,1]
	v_pk_mul_f32 v[10:11], v[20:21], v[10:11] op_sel_hi:[0,1]
	v_pk_fma_f32 v[6:7], v[30:31], s[6:7], v[6:7] op_sel_hi:[1,0,1]
	v_pk_fma_f32 v[2:3], v[26:27], s[6:7], v[2:3] op_sel_hi:[1,0,1]
	v_pk_mul_f32 v[6:7], v[20:21], v[6:7] op_sel_hi:[0,1]
	v_pk_mul_f32 v[2:3], v[20:21], v[2:3] op_sel_hi:[0,1]
	v_cvt_pk_fp8_f32 v22, v14, v15 op_sel:[0,0,1]
	v_cvt_pk_fp8_f32 v23, v10, v11 op_sel:[0,0,1]
	v_ashrrev_i32_e32 v19, 31, v18
	v_lshlrev_b64 v[0:1], 11, v[18:19]
	v_cvt_pk_fp8_f32 v8, v6, v7 op_sel:[0,0,1]
	v_cvt_pk_fp8_f32 v9, v2, v3 op_sel:[0,0,1]
	v_lshl_add_u64 v[0:1], s[2:3], 0, v[0:1]
	v_lshl_add_u64 v[0:1], v[0:1], 0, v[16:17]
	v_mov_b32_e32 v164, v179
	global_store_dwordx2 v[0:1], v[22:23], off
	global_store_dwordx2 v[0:1], v[8:9], off offset:128
	s_cbranch_vccz .LBB0_2793
	s_waitcnt vmcnt(0)
	s_cmpk_gt_u32 s96, 0xff
	s_cbranch_scc1 .LBB0_2800
	s_barrier
